# K-loop load segments reordered: LDS-DMA issue moved ahead of the ds_read block (earlier prefetch issue)
# baseline (speedup 1.0000x reference)
; #define G_STAGE(bufoff, gbase, voff) do { _Pragma("unroll") for (int _i = 0; _i < 2; ++_i) \
;         __builtin_amdgcn_global_load_lds((const unsigned*)((const char*)(gbase) + (voff)[_i]), (LAS unsigned*)(lds + (bufoff) + ldsw + _i * 8192), 16, 0, 0); } while (0)
; #define G_LDA(dst, b, h) do { _Pragma("unroll") for (int m = 0; m < 4; ++m) G_LD8(dst[m], lds + G_SA(b, h) + aoff + m * 2048); } while (0)
; #define G_LDB(dst, b, h) do { _Pragma("unroll") for (int n = 0; n < 2; ++n) G_LD8(dst[n], lds + G_SB(b, h) + boff + n * 2048); } while (0)
; #define G_WAIT_V(n) asm volatile("s_waitcnt vmcnt(" #n ")" ::: "memory")
; #define G_WAIT_L(n) asm volatile("s_waitcnt lgkmcnt(" #n ")" ::: "memory")
; #define G_BAR __builtin_amdgcn_s_barrier()
; #define G_SCHED __builtin_amdgcn_sched_barrier(0)
;     __device__ __forceinline__ unsigned row_off(const Unit& u, int r, LAS unsigned char* lds) const { return (unsigned)((const LAS int*)(lds + LDS_STAGE + u.q * 4096))[r] * (unsigned)rowbytes; }
;     ...
;             const char* a11 = cur.a1 + (size_t)(t + 1) * kstep;
;             const char* a02 = last ? nxt.a0 : cur.a0 + (size_t)(t + 2) * kstep; const char* a12 = last ? nxt.a1 : cur.a1 + (size_t)(t + 2) * kstep;
;             const char* b02 = last ? nxt.b0 : cur.b0 + (size_t)(t + 2) * kstep; const char* b12 = last ? nxt.b1 : cur.b1 + (size_t)(t + 2) * kstep;
;             G_LDB(B0, 0, 0); G_LDB(B1, 0, 1); G_SCHED; G_LDA(At, 0, 0); G_STAGE(G_SA(1, 1), a11, vA1);
;             if constexpr (GATHER) { if (last) { int tz = tid; asm volatile("" : "+v"(tz));
; #pragma unroll
;                 for (int i = 0; i < 2; ++i) { int R, C; stage_rc(tz * 16 + i * 8192, R, C); gc0[i] = S.row_off(nxt, R, lds) + (unsigned)C * 2u; gc1[i] = S.row_off(nxt, 128 + R, lds) + (unsigned)C * 2u; } } }
;             G_WAIT_L(0); G_BAR; G_MMA(0, 0, At, B0); G_MMA(0, 1, At, B1); G_WAIT_V(8); G_BAR; G_SCHED;
;             G_LDA(At, 0, 1); G_STAGE(G_SB(0, 0), b02, voffB); G_STAGE(G_SB(0, 1), b12, voffB); G_STAGE(G_SA(0, 0), a02, vA0);
.LBB0_179:
	s_add_i32 s63, s59, 2
	s_add_u32 s73, s74, 0x80
	s_addc_u32 s76, s75, 0
	s_add_i32 s83, s91, s97
	s_add_i32 m0, s22, 0xc000
	s_add_i32 s82, s22, 0xe000
	s_add_i32 s89, s83, 0x2000
	s_cmp_eq_u32 s20, s59
	s_cselect_b32 s79, s65, s33
	s_cselect_b32 s78, s64, s19
	s_cselect_b32 s81, s69, s2
	s_cselect_b32 s80, s68, s0
	s_cselect_b32 s77, s67, s76
	s_cselect_b32 s76, s66, s73
	global_load_lds_dwordx4 v240, s[74:75]
	s_mov_b32 m0, s82
	s_nop 0
	global_load_lds_dwordx4 v242, s[74:75]
	v_add_u32_e32 v144, s91, v163
	v_add_u32_e32 v170, s3, v163
	ds_read_b128 v[34:37], v144
	ds_read_b128 v[38:41], v144 offset:1024
	ds_read_b128 v[42:45], v144 offset:2048
	ds_read_b128 v[144:147], v144 offset:3072
	ds_read_b128 v[150:153], v170
	ds_read_b128 v[154:157], v170 offset:1024
	ds_read_b128 v[166:169], v170 offset:2048
	ds_read_b128 v[170:173], v170 offset:3072
	ds_read_b128 v[174:177], v164
	ds_read_b128 v[178:181], v164 offset:1024
	ds_read_b128 v[182:185], v164 offset:2048
	ds_read_b128 v[186:189], v164 offset:3072
	ds_read_b128 v[190:193], v164 offset:4096
	ds_read_b128 v[194:197], v164 offset:5120
	ds_read_b128 v[198:201], v164 offset:6144
	ds_read_b128 v[202:205], v164 offset:7168
	s_waitcnt lgkmcnt(0)
	v_mov_b32_e32 v33, v149
	s_barrier
	s_setprio 1
	s_waitcnt lgkmcnt(0)
	v_mfma_i32_16x16x64_i8 v[140:143], v[34:37], v[174:177], v[140:143]
	v_mfma_i32_16x16x64_i8 v[132:135], v[42:45], v[174:177], v[132:135]
	v_mfma_i32_16x16x64_i8 v[124:127], v[34:37], v[182:185], v[124:127]
	v_mfma_i32_16x16x64_i8 v[116:119], v[42:45], v[182:185], v[116:119]
	v_mfma_i32_16x16x64_i8 v[108:111], v[34:37], v[190:193], v[108:111]
	v_mfma_i32_16x16x64_i8 v[100:103], v[42:45], v[190:193], v[100:103]
	v_mfma_i32_16x16x64_i8 v[92:95], v[34:37], v[198:201], v[92:95]
	v_mfma_i32_16x16x64_i8 v[84:87], v[42:45], v[198:201], v[84:87]
	v_mfma_i32_16x16x64_i8 v[140:143], v[38:41], v[178:181], v[140:143]
	v_mfma_i32_16x16x64_i8 v[132:135], v[144:147], v[178:181], v[132:135]
	v_mfma_i32_16x16x64_i8 v[124:127], v[38:41], v[186:189], v[124:127]
	v_mfma_i32_16x16x64_i8 v[116:119], v[144:147], v[186:189], v[116:119]
	v_mfma_i32_16x16x64_i8 v[108:111], v[38:41], v[194:197], v[108:111]
	v_mfma_i32_16x16x64_i8 v[100:103], v[144:147], v[194:197], v[100:103]
	v_mfma_i32_16x16x64_i8 v[92:95], v[38:41], v[202:205], v[92:95]
	v_mfma_i32_16x16x64_i8 v[84:87], v[144:147], v[202:205], v[84:87]
	v_mfma_i32_16x16x64_i8 v[136:139], v[150:153], v[174:177], v[136:139]
	v_mfma_i32_16x16x64_i8 v[128:131], v[166:169], v[174:177], v[128:131]
	v_mfma_i32_16x16x64_i8 v[120:123], v[150:153], v[182:185], v[120:123]
	v_mfma_i32_16x16x64_i8 v[112:115], v[166:169], v[182:185], v[112:115]
	v_mfma_i32_16x16x64_i8 v[104:107], v[150:153], v[190:193], v[104:107]
	v_mfma_i32_16x16x64_i8 v[96:99], v[166:169], v[190:193], v[96:99]
	v_mfma_i32_16x16x64_i8 v[88:91], v[150:153], v[198:201], v[88:91]
	v_mfma_i32_16x16x64_i8 v[80:83], v[166:169], v[198:201], v[80:83]
	v_mfma_i32_16x16x64_i8 v[136:139], v[154:157], v[178:181], v[136:139]
	v_mfma_i32_16x16x64_i8 v[128:131], v[170:173], v[178:181], v[128:131]
	v_mfma_i32_16x16x64_i8 v[120:123], v[154:157], v[186:189], v[120:123]
	v_mfma_i32_16x16x64_i8 v[112:115], v[170:173], v[186:189], v[112:115]
	v_mfma_i32_16x16x64_i8 v[104:107], v[154:157], v[194:197], v[104:107]
	v_mfma_i32_16x16x64_i8 v[96:99], v[170:173], v[194:197], v[96:99]
	v_mfma_i32_16x16x64_i8 v[88:91], v[154:157], v[202:205], v[88:91]
	v_mfma_i32_16x16x64_i8 v[80:83], v[170:173], v[202:205], v[80:83]
	s_setprio 0
	s_waitcnt vmcnt(8)
	s_barrier
	s_mov_b32 m0, s83
	v_mov_b32_e32 v47, v149
	global_load_lds_dwordx4 v244, s[80:81]
	v_mov_b32_e32 v159, v149
	s_mov_b32 m0, s89
	v_lshl_add_u64 v[206:207], s[80:81], 0, v[244:245]
	v_lshl_add_u64 v[208:209], s[80:81], 0, v[246:247]
	global_load_lds_dwordx4 v246, s[80:81]
	s_cselect_b32 s81, s71, s6
	s_cselect_b32 s80, s70, s5
	s_add_i32 s59, s3, s97
	s_mov_b32 m0, s59
	v_lshl_add_u64 v[210:211], s[80:81], 0, v[244:245]
	global_load_lds_dwordx4 v244, s[80:81]
	s_add_i32 m0, s59, 0x2000
	v_lshl_add_u64 v[212:213], s[80:81], 0, v[246:247]
	global_load_lds_dwordx4 v246, s[80:81]
	s_mov_b32 m0, s22
	v_lshl_add_u64 v[158:159], s[78:79], 0, v[240:241]
	global_load_lds_dwordx4 v240, s[78:79]
	s_mov_b32 m0, s23
	v_lshl_add_u64 v[214:215], s[78:79], 0, v[242:243]
	global_load_lds_dwordx4 v242, s[78:79]
	ds_read_b128 v[174:177], v164 offset:16384
	ds_read_b128 v[178:181], v164 offset:17408
	ds_read_b128 v[182:185], v164 offset:18432
	ds_read_b128 v[186:189], v164 offset:19456
	ds_read_b128 v[190:193], v164 offset:20480
	ds_read_b128 v[194:197], v164 offset:21504
	ds_read_b128 v[198:201], v164 offset:22528
	ds_read_b128 v[202:205], v164 offset:23552
	s_waitcnt lgkmcnt(0)
	s_barrier
; #define G_STAGE(bufoff, gbase, voff) do { _Pragma("unroll") for (int _i = 0; _i < 2; ++_i) \
;         __builtin_amdgcn_global_load_lds((const unsigned*)((const char*)(gbase) + (voff)[_i]), (LAS unsigned*)(lds + (bufoff) + ldsw + _i * 8192), 16, 0, 0); } while (0)
; #define G_LDA(dst, b, h) do { _Pragma("unroll") for (int m = 0; m < 4; ++m) G_LD8(dst[m], lds + G_SA(b, h) + aoff + m * 2048); } while (0)
; #define G_LDB(dst, b, h) do { _Pragma("unroll") for (int n = 0; n < 2; ++n) G_LD8(dst[n], lds + G_SB(b, h) + boff + n * 2048); } while (0)
; #define G_WAIT_V(n) asm volatile("s_waitcnt vmcnt(" #n ")" ::: "memory")
; #define G_WAIT_L(n) asm volatile("s_waitcnt lgkmcnt(" #n ")" ::: "memory")
; #define G_BAR __builtin_amdgcn_s_barrier()
; #define G_SCHED __builtin_amdgcn_sched_barrier(0)
;     ...
;             G_WAIT_L(0); G_BAR; G_MMA(0, 0, At, B0); G_MMA(0, 1, At, B1); G_WAIT_V(8); G_BAR; G_SCHED;
;             G_LDA(At, 0, 1); G_STAGE(G_SB(0, 0), b02, voffB); G_STAGE(G_SB(0, 1), b12, voffB); G_STAGE(G_SA(0, 0), a02, vA0);
;             G_WAIT_L(0); G_BAR; G_MMA(1, 0, At, B0); G_MMA(1, 1, At, B1); G_WAIT_V(8); G_BAR; G_SCHED;
;             G_LDB(B0, 1, 0); G_LDB(B1, 1, 1); G_SCHED; G_LDA(At, 1, 0); G_STAGE(G_SA(0, 1), a12, vA1);
;             G_WAIT_L(0); G_BAR; G_MMA(0, 0, At, B0); G_MMA(0, 1, At, B1); G_WAIT_V(8); G_BAR; G_SCHED;
	s_setprio 1
	s_waitcnt lgkmcnt(0)
	v_mfma_i32_16x16x64_i8 v[76:79], v[34:37], v[174:177], v[76:79]
	v_mfma_i32_16x16x64_i8 v[68:71], v[42:45], v[174:177], v[68:71]
	v_mfma_i32_16x16x64_i8 v[60:63], v[34:37], v[182:185], v[60:63]
	v_mfma_i32_16x16x64_i8 v[52:55], v[42:45], v[182:185], v[52:55]
	v_mfma_i32_16x16x64_i8 v[28:31], v[34:37], v[190:193], v[28:31]
	v_mfma_i32_16x16x64_i8 v[20:23], v[42:45], v[190:193], v[20:23]
	v_mfma_i32_16x16x64_i8 v[12:15], v[34:37], v[198:201], v[12:15]
	v_mfma_i32_16x16x64_i8 v[4:7], v[42:45], v[198:201], v[4:7]
	v_mfma_i32_16x16x64_i8 v[76:79], v[38:41], v[178:181], v[76:79]
	v_mfma_i32_16x16x64_i8 v[68:71], v[144:147], v[178:181], v[68:71]
	v_mfma_i32_16x16x64_i8 v[60:63], v[38:41], v[186:189], v[60:63]
	v_mfma_i32_16x16x64_i8 v[52:55], v[144:147], v[186:189], v[52:55]
	v_mfma_i32_16x16x64_i8 v[28:31], v[38:41], v[194:197], v[28:31]
	v_mfma_i32_16x16x64_i8 v[20:23], v[144:147], v[194:197], v[20:23]
	v_mfma_i32_16x16x64_i8 v[12:15], v[38:41], v[202:205], v[12:15]
	v_mfma_i32_16x16x64_i8 v[4:7], v[144:147], v[202:205], v[4:7]
	v_mfma_i32_16x16x64_i8 v[46:49], v[166:169], v[182:185], v[48:51]
	v_mfma_i32_16x16x64_i8 v[24:27], v[150:153], v[190:193], v[24:27]
	v_mfma_i32_16x16x64_i8 v[16:19], v[166:169], v[190:193], v[16:19]
	v_mfma_i32_16x16x64_i8 v[8:11], v[150:153], v[198:201], v[8:11]
	v_mfma_i32_16x16x64_i8 v[0:3], v[166:169], v[198:201], v[0:3]
	v_mfma_i32_16x16x64_i8 v[34:37], v[150:153], v[174:177], v[72:75]
	v_mfma_i32_16x16x64_i8 v[38:41], v[166:169], v[174:177], v[64:67]
	v_mfma_i32_16x16x64_i8 v[42:45], v[150:153], v[182:185], v[56:59]
	v_mfma_i32_16x16x64_i8 v[46:49], v[170:173], v[186:189], v[46:49]
	v_mfma_i32_16x16x64_i8 v[24:27], v[154:157], v[194:197], v[24:27]
	v_mfma_i32_16x16x64_i8 v[16:19], v[170:173], v[194:197], v[16:19]
	v_mfma_i32_16x16x64_i8 v[8:11], v[154:157], v[202:205], v[8:11]
	v_mfma_i32_16x16x64_i8 v[0:3], v[170:173], v[202:205], v[0:3]
	v_mfma_i32_16x16x64_i8 v[34:37], v[154:157], v[178:181], v[34:37]
	v_mfma_i32_16x16x64_i8 v[38:41], v[170:173], v[178:181], v[38:41]
	v_mfma_i32_16x16x64_i8 v[42:45], v[154:157], v[186:189], v[42:45]
	s_setprio 0
	s_waitcnt vmcnt(8)
	s_barrier
	s_add_i32 s59, 0, 0x18000
	s_add_i32 s73, 0, 0x1c000
	s_mov_b32 m0, s55
	s_nop 0
	global_load_lds_dwordx4 v240, s[76:77]
	s_mov_b32 m0, s84
	s_nop 0
	global_load_lds_dwordx4 v242, s[76:77]
	v_add_u32_e32 v33, s59, v163
	ds_read_b128 v[56:59], v33
	ds_read_b128 v[64:67], v33 offset:1024
	ds_read_b128 v[72:75], v33 offset:2048
	ds_read_b128 v[144:147], v33 offset:3072
	v_add_u32_e32 v33, s73, v163
	ds_read_b128 v[150:153], v33
	ds_read_b128 v[154:157], v33 offset:1024
	ds_read_b128 v[166:169], v33 offset:2048
	ds_read_b128 v[170:173], v33 offset:3072
	ds_read_b128 v[174:177], v164 offset:32768
	ds_read_b128 v[178:181], v164 offset:33792
	ds_read_b128 v[182:185], v164 offset:34816
	ds_read_b128 v[186:189], v164 offset:35840
	ds_read_b128 v[190:193], v164 offset:36864
	ds_read_b128 v[194:197], v164 offset:37888
	ds_read_b128 v[198:201], v164 offset:38912
	ds_read_b128 v[202:205], v164 offset:39936
	s_waitcnt lgkmcnt(0)
	s_barrier
	s_setprio 1
	s_waitcnt lgkmcnt(0)
	v_mfma_i32_16x16x64_i8 v[140:143], v[56:59], v[174:177], v[140:143]
	v_mfma_i32_16x16x64_i8 v[132:135], v[72:75], v[174:177], v[132:135]
	v_mfma_i32_16x16x64_i8 v[124:127], v[56:59], v[182:185], v[124:127]
	v_mfma_i32_16x16x64_i8 v[116:119], v[72:75], v[182:185], v[116:119]
	v_mfma_i32_16x16x64_i8 v[108:111], v[56:59], v[190:193], v[108:111]
	v_mfma_i32_16x16x64_i8 v[100:103], v[72:75], v[190:193], v[100:103]
	v_mfma_i32_16x16x64_i8 v[92:95], v[56:59], v[198:201], v[92:95]
	v_mfma_i32_16x16x64_i8 v[84:87], v[72:75], v[198:201], v[84:87]
	v_mfma_i32_16x16x64_i8 v[140:143], v[64:67], v[178:181], v[140:143]
	v_mfma_i32_16x16x64_i8 v[132:135], v[144:147], v[178:181], v[132:135]
	v_mfma_i32_16x16x64_i8 v[124:127], v[64:67], v[186:189], v[124:127]
	v_mfma_i32_16x16x64_i8 v[116:119], v[144:147], v[186:189], v[116:119]
	v_mfma_i32_16x16x64_i8 v[108:111], v[64:67], v[194:197], v[108:111]
	v_mfma_i32_16x16x64_i8 v[100:103], v[144:147], v[194:197], v[100:103]
	v_mfma_i32_16x16x64_i8 v[92:95], v[64:67], v[202:205], v[92:95]
	v_mfma_i32_16x16x64_i8 v[84:87], v[144:147], v[202:205], v[84:87]
	v_mfma_i32_16x16x64_i8 v[136:139], v[150:153], v[174:177], v[136:139]
	v_mfma_i32_16x16x64_i8 v[128:131], v[166:169], v[174:177], v[128:131]
	v_mfma_i32_16x16x64_i8 v[120:123], v[150:153], v[182:185], v[120:123]
	v_mfma_i32_16x16x64_i8 v[112:115], v[166:169], v[182:185], v[112:115]
	v_mfma_i32_16x16x64_i8 v[104:107], v[150:153], v[190:193], v[104:107]
	v_mfma_i32_16x16x64_i8 v[96:99], v[166:169], v[190:193], v[96:99]
	v_mfma_i32_16x16x64_i8 v[88:91], v[150:153], v[198:201], v[88:91]
	v_mfma_i32_16x16x64_i8 v[80:83], v[166:169], v[198:201], v[80:83]
	v_mfma_i32_16x16x64_i8 v[136:139], v[154:157], v[178:181], v[136:139]
	v_mfma_i32_16x16x64_i8 v[128:131], v[170:173], v[178:181], v[128:131]
	v_mfma_i32_16x16x64_i8 v[120:123], v[154:157], v[186:189], v[120:123]
	v_mfma_i32_16x16x64_i8 v[112:115], v[170:173], v[186:189], v[112:115]
	v_mfma_i32_16x16x64_i8 v[104:107], v[154:157], v[194:197], v[104:107]
	v_mfma_i32_16x16x64_i8 v[96:99], v[170:173], v[194:197], v[96:99]
	v_mfma_i32_16x16x64_i8 v[88:91], v[154:157], v[202:205], v[88:91]
	v_mfma_i32_16x16x64_i8 v[80:83], v[170:173], v[202:205], v[80:83]
	s_setprio 0
	s_waitcnt vmcnt(8)
	s_barrier
; #define G_STAGE(bufoff, gbase, voff) do { _Pragma("unroll") for (int _i = 0; _i < 2; ++_i) \
;         __builtin_amdgcn_global_load_lds((const unsigned*)((const char*)(gbase) + (voff)[_i]), (LAS unsigned*)(lds + (bufoff) + ldsw + _i * 8192), 16, 0, 0); } while (0)
; #define G_LDA(dst, b, h) do { _Pragma("unroll") for (int m = 0; m < 4; ++m) G_LD8(dst[m], lds + G_SA(b, h) + aoff + m * 2048); } while (0)
; #define G_WAIT_V(n) asm volatile("s_waitcnt vmcnt(" #n ")" ::: "memory")
; #define G_WAIT_L(n) asm volatile("s_waitcnt lgkmcnt(" #n ")" ::: "memory")
; #define G_BAR __builtin_amdgcn_s_barrier()
; #define G_SCHED __builtin_amdgcn_sched_barrier(0)
;     ...
;             G_LDA(At, 1, 1); G_STAGE(G_SB(1, 0), b02 + kstep, voffB); G_STAGE(G_SB(1, 1), b12 + kstep, voffB); G_STAGE(G_SA(1, 0), a02 + kstep, vA0);
;             G_WAIT_L(0); G_BAR; G_MMA(1, 0, At, B0); G_MMA(1, 1, At, B1); G_WAIT_V(8); G_BAR; G_SCHED;
;         }
	s_add_i32 s59, s59, s97
	v_lshl_add_u64 v[32:33], v[206:207], 0, s[46:47]
	s_mov_b32 m0, s59
	s_nop 0
	global_load_lds_dwordx4 v[32:33], off
	v_lshl_add_u64 v[32:33], v[208:209], 0, s[46:47]
	s_add_i32 m0, s59, 0x2000
	s_add_i32 s59, s73, s97
	global_load_lds_dwordx4 v[32:33], off
	v_lshl_add_u64 v[32:33], v[210:211], 0, s[46:47]
	s_mov_b32 m0, s59
	s_nop 0
	global_load_lds_dwordx4 v[32:33], off
	v_lshl_add_u64 v[32:33], v[212:213], 0, s[46:47]
	s_add_i32 m0, s59, 0x2000
	s_nop 0
	global_load_lds_dwordx4 v[32:33], off
	v_lshl_add_u64 v[32:33], v[158:159], 0, s[46:47]
	s_mov_b32 m0, s86
	s_nop 0
	global_load_lds_dwordx4 v[32:33], off
	v_lshl_add_u64 v[32:33], v[214:215], 0, s[46:47]
	s_mov_b32 m0, s87
	s_nop 0
	global_load_lds_dwordx4 v[32:33], off
	ds_read_b128 v[174:177], v164 offset:49152
	ds_read_b128 v[178:181], v164 offset:50176
	ds_read_b128 v[182:185], v164 offset:51200
	ds_read_b128 v[186:189], v164 offset:52224
	ds_read_b128 v[190:193], v164 offset:53248
	ds_read_b128 v[194:197], v164 offset:54272
	ds_read_b128 v[198:201], v164 offset:55296
	ds_read_b128 v[202:205], v164 offset:56320
	s_waitcnt lgkmcnt(0)
	s_barrier
	s_setprio 1
	s_waitcnt lgkmcnt(0)
	v_mfma_i32_16x16x64_i8 v[76:79], v[56:59], v[174:177], v[76:79]
	v_mfma_i32_16x16x64_i8 v[68:71], v[72:75], v[174:177], v[68:71]
	v_mfma_i32_16x16x64_i8 v[60:63], v[56:59], v[182:185], v[60:63]
	v_mfma_i32_16x16x64_i8 v[50:53], v[72:75], v[182:185], v[52:55]
	v_mfma_i32_16x16x64_i8 v[28:31], v[56:59], v[190:193], v[28:31]
	v_mfma_i32_16x16x64_i8 v[20:23], v[72:75], v[190:193], v[20:23]
	v_mfma_i32_16x16x64_i8 v[12:15], v[56:59], v[198:201], v[12:15]
	v_mfma_i32_16x16x64_i8 v[4:7], v[72:75], v[198:201], v[4:7]
	v_mfma_i32_16x16x64_i8 v[76:79], v[64:67], v[178:181], v[76:79]
	v_mfma_i32_16x16x64_i8 v[68:71], v[144:147], v[178:181], v[68:71]
	v_mfma_i32_16x16x64_i8 v[60:63], v[64:67], v[186:189], v[60:63]
	v_mfma_i32_16x16x64_i8 v[52:55], v[144:147], v[186:189], v[50:53]
	v_mfma_i32_16x16x64_i8 v[28:31], v[64:67], v[194:197], v[28:31]
	v_mfma_i32_16x16x64_i8 v[20:23], v[144:147], v[194:197], v[20:23]
	v_mfma_i32_16x16x64_i8 v[12:15], v[64:67], v[202:205], v[12:15]
	v_mfma_i32_16x16x64_i8 v[4:7], v[144:147], v[202:205], v[4:7]
	v_mfma_i32_16x16x64_i8 v[32:35], v[150:153], v[174:177], v[34:37]
	v_mfma_i32_16x16x64_i8 v[72:75], v[154:157], v[178:181], v[32:35]
	v_mfma_i32_16x16x64_i8 v[32:35], v[166:169], v[174:177], v[38:41]
	v_mfma_i32_16x16x64_i8 v[64:67], v[170:173], v[178:181], v[32:35]
	v_mfma_i32_16x16x64_i8 v[32:35], v[150:153], v[182:185], v[42:45]
	v_mfma_i32_16x16x64_i8 v[56:59], v[154:157], v[186:189], v[32:35]
	v_mfma_i32_16x16x64_i8 v[32:35], v[166:169], v[182:185], v[46:49]
	v_mfma_i32_16x16x64_i8 v[24:27], v[150:153], v[190:193], v[24:27]
	v_mfma_i32_16x16x64_i8 v[16:19], v[166:169], v[190:193], v[16:19]
	v_mfma_i32_16x16x64_i8 v[8:11], v[150:153], v[198:201], v[8:11]
	v_mfma_i32_16x16x64_i8 v[0:3], v[166:169], v[198:201], v[0:3]
	v_mfma_i32_16x16x64_i8 v[48:51], v[170:173], v[186:189], v[32:35]
	v_mfma_i32_16x16x64_i8 v[24:27], v[154:157], v[194:197], v[24:27]
	v_mfma_i32_16x16x64_i8 v[16:19], v[170:173], v[194:197], v[16:19]
	v_mfma_i32_16x16x64_i8 v[8:11], v[154:157], v[202:205], v[8:11]
	v_mfma_i32_16x16x64_i8 v[0:3], v[170:173], v[202:205], v[0:3]
	s_setprio 0
	s_waitcnt vmcnt(8)
	s_barrier
	s_add_u32 s0, s0, 0x100
	s_addc_u32 s2, s2, 0
	s_add_u32 s5, s5, 0x100
	s_addc_u32 s6, s6, 0
	s_add_u32 s19, s19, 0x100
	s_addc_u32 s33, s33, 0
	s_add_u32 s74, s74, 0x100
	s_addc_u32 s75, s75, 0
	s_cmp_ge_i32 s63, s25
	s_mov_b32 s59, s63
	s_cbranch_scc0 .LBB0_179
	s_and_b64 vcc, exec, s[50:51]
	s_cbranch_vccz .LBB0_182

; #define G_STAGE(bufoff, gbase, voff) do { _Pragma("unroll") for (int _i = 0; _i < 2; ++_i) \
;         __builtin_amdgcn_global_load_lds((const unsigned*)((const char*)(gbase) + (voff)[_i]), (LAS unsigned*)(lds + (bufoff) + ldsw + _i * 8192), 16, 0, 0); } while (0)
; #define G_LDA(dst, b, h) do { _Pragma("unroll") for (int m = 0; m < 4; ++m) G_LD8(dst[m], lds + G_SA(b, h) + aoff + m * 2048); } while (0)
; #define G_LDB(dst, b, h) do { _Pragma("unroll") for (int n = 0; n < 2; ++n) G_LD8(dst[n], lds + G_SB(b, h) + boff + n * 2048); } while (0)
; #define G_WAIT_V(n) asm volatile("s_waitcnt vmcnt(" #n ")" ::: "memory")
; #define G_WAIT_L(n) asm volatile("s_waitcnt lgkmcnt(" #n ")" ::: "memory")
; #define G_BAR __builtin_amdgcn_s_barrier()
; #define G_SCHED __builtin_amdgcn_sched_barrier(0)
;     __device__ __forceinline__ unsigned row_off(const Unit& u, int r, LAS unsigned char* lds) const { return (unsigned)((const LAS int*)(lds + LDS_STAGE + u.q * 4096))[r] * (unsigned)rowbytes; }
;     ...
;             const char* a11 = cur.a1 + (size_t)(t + 1) * kstep;
;             const char* a02 = last ? nxt.a0 : cur.a0 + (size_t)(t + 2) * kstep; const char* a12 = last ? nxt.a1 : cur.a1 + (size_t)(t + 2) * kstep;
;             const char* b02 = last ? nxt.b0 : cur.b0 + (size_t)(t + 2) * kstep; const char* b12 = last ? nxt.b1 : cur.b1 + (size_t)(t + 2) * kstep;
;             G_LDB(B0, 0, 0); G_LDB(B1, 0, 1); G_SCHED; G_LDA(At, 0, 0); G_STAGE(G_SA(1, 1), a11, vA1);
;             if constexpr (GATHER) { if (last) { int tz = tid; asm volatile("" : "+v"(tz));
; #pragma unroll
;                 for (int i = 0; i < 2; ++i) { int R, C; stage_rc(tz * 16 + i * 8192, R, C); gc0[i] = S.row_off(nxt, R, lds) + (unsigned)C * 2u; gc1[i] = S.row_off(nxt, 128 + R, lds) + (unsigned)C * 2u; } } }
;             G_WAIT_L(0); G_BAR; G_MMA(0, 0, At, B0); G_MMA(0, 1, At, B1); G_WAIT_V(8); G_BAR; G_SCHED;
;             G_LDA(At, 0, 1); G_STAGE(G_SB(0, 0), b02, voffB); G_STAGE(G_SB(0, 1), b12, voffB); G_STAGE(G_SA(0, 0), a02, vA0);
.LBB0_249:
	s_add_i32 s68, s58, 2
	s_add_u32 s69, s56, 0x80
	s_addc_u32 s59, s57, 0
	s_add_i32 s71, s23, s97
	s_add_i32 m0, s2, 0xc000
	s_add_i32 s70, s2, 0xe000
	s_add_i32 s72, s71, 0x2000
	s_cmp_eq_u32 s22, s58
	s_cselect_b32 s58, s46, s69
	s_cselect_b32 s61, s45, s67
	s_cselect_b32 s60, s44, s66
	s_cselect_b32 s63, s49, s55
	s_cselect_b32 s62, s48, s43
	s_cselect_b32 s59, s47, s59
	global_load_lds_dwordx4 v240, s[56:57]
	s_mov_b32 m0, s70
	s_nop 0
	global_load_lds_dwordx4 v242, s[56:57]
	v_add_u32_e32 v144, s23, v151
	v_add_u32_e32 v166, s24, v151
	ds_read_b128 v[132:135], v144
	ds_read_b128 v[136:139], v144 offset:1024
	ds_read_b128 v[140:143], v144 offset:2048
	ds_read_b128 v[144:147], v144 offset:3072
	ds_read_b128 v[154:157], v166
	ds_read_b128 v[158:161], v166 offset:1024
	ds_read_b128 v[162:165], v166 offset:2048
	ds_read_b128 v[166:169], v166 offset:3072
	ds_read_b128 v[170:173], v152
	ds_read_b128 v[174:177], v152 offset:1024
	ds_read_b128 v[178:181], v152 offset:2048
	ds_read_b128 v[182:185], v152 offset:3072
	ds_read_b128 v[186:189], v152 offset:4096
	ds_read_b128 v[190:193], v152 offset:5120
	ds_read_b128 v[194:197], v152 offset:6144
	ds_read_b128 v[198:201], v152 offset:7168
	s_waitcnt lgkmcnt(0)
	v_mov_b32_e32 v131, v129
	s_barrier
	s_setprio 1
	s_waitcnt lgkmcnt(0)
	v_mfma_i32_16x16x64_i8 v[124:127], v[132:135], v[170:173], v[124:127]
	v_mfma_i32_16x16x64_i8 v[120:123], v[140:143], v[170:173], v[120:123]
	v_mfma_i32_16x16x64_i8 v[108:111], v[132:135], v[178:181], v[108:111]
	v_mfma_i32_16x16x64_i8 v[104:107], v[140:143], v[178:181], v[104:107]
	v_mfma_i32_16x16x64_i8 v[92:95], v[132:135], v[186:189], v[92:95]
	v_mfma_i32_16x16x64_i8 v[88:91], v[140:143], v[186:189], v[88:91]
	v_mfma_i32_16x16x64_i8 v[76:79], v[132:135], v[194:197], v[76:79]
	v_mfma_i32_16x16x64_i8 v[72:75], v[140:143], v[194:197], v[72:75]
	v_mfma_i32_16x16x64_i8 v[124:127], v[136:139], v[174:177], v[124:127]
	v_mfma_i32_16x16x64_i8 v[120:123], v[144:147], v[174:177], v[120:123]
	v_mfma_i32_16x16x64_i8 v[108:111], v[136:139], v[182:185], v[108:111]
	v_mfma_i32_16x16x64_i8 v[104:107], v[144:147], v[182:185], v[104:107]
	v_mfma_i32_16x16x64_i8 v[92:95], v[136:139], v[190:193], v[92:95]
	v_mfma_i32_16x16x64_i8 v[88:91], v[144:147], v[190:193], v[88:91]
	v_mfma_i32_16x16x64_i8 v[76:79], v[136:139], v[198:201], v[76:79]
	v_mfma_i32_16x16x64_i8 v[72:75], v[144:147], v[198:201], v[72:75]
	v_mfma_i32_16x16x64_i8 v[116:119], v[154:157], v[170:173], v[116:119]
	v_mfma_i32_16x16x64_i8 v[112:115], v[162:165], v[170:173], v[112:115]
	v_mfma_i32_16x16x64_i8 v[100:103], v[154:157], v[178:181], v[100:103]
	v_mfma_i32_16x16x64_i8 v[96:99], v[162:165], v[178:181], v[96:99]
	v_mfma_i32_16x16x64_i8 v[84:87], v[154:157], v[186:189], v[84:87]
	v_mfma_i32_16x16x64_i8 v[80:83], v[162:165], v[186:189], v[80:83]
	v_mfma_i32_16x16x64_i8 v[68:71], v[154:157], v[194:197], v[68:71]
	v_mfma_i32_16x16x64_i8 v[64:67], v[162:165], v[194:197], v[64:67]
	v_mfma_i32_16x16x64_i8 v[116:119], v[158:161], v[174:177], v[116:119]
	v_mfma_i32_16x16x64_i8 v[112:115], v[166:169], v[174:177], v[112:115]
	v_mfma_i32_16x16x64_i8 v[100:103], v[158:161], v[182:185], v[100:103]
	v_mfma_i32_16x16x64_i8 v[96:99], v[166:169], v[182:185], v[96:99]
	v_mfma_i32_16x16x64_i8 v[84:87], v[158:161], v[190:193], v[84:87]
	v_mfma_i32_16x16x64_i8 v[80:83], v[166:169], v[190:193], v[80:83]
	v_mfma_i32_16x16x64_i8 v[68:71], v[158:161], v[198:201], v[68:71]
	v_mfma_i32_16x16x64_i8 v[64:67], v[166:169], v[198:201], v[64:67]
	s_setprio 0
	s_waitcnt vmcnt(8)
	s_barrier
	s_mov_b32 m0, s71
	v_mov_b32_e32 v203, v129
	global_load_lds_dwordx4 v244, s[62:63]
	v_mov_b32_e32 v205, v129
	s_mov_b32 m0, s72
	v_lshl_add_u64 v[206:207], s[62:63], 0, v[244:245]
	v_lshl_add_u64 v[208:209], s[62:63], 0, v[246:247]
	global_load_lds_dwordx4 v246, s[62:63]
	s_cselect_b32 s63, s51, s65
	s_cselect_b32 s62, s50, s64
	s_add_i32 s69, s24, s97
	s_mov_b32 m0, s69
	v_lshl_add_u64 v[210:211], s[62:63], 0, v[244:245]
	global_load_lds_dwordx4 v244, s[62:63]
	s_add_i32 m0, s69, 0x2000
	v_lshl_add_u64 v[202:203], s[62:63], 0, v[246:247]
	global_load_lds_dwordx4 v246, s[62:63]
	s_mov_b32 m0, s2
	v_lshl_add_u64 v[204:205], s[60:61], 0, v[240:241]
	global_load_lds_dwordx4 v240, s[60:61]
	s_mov_b32 m0, s10
	v_lshl_add_u64 v[212:213], s[60:61], 0, v[242:243]
	global_load_lds_dwordx4 v242, s[60:61]
	ds_read_b128 v[170:173], v152 offset:16384
	ds_read_b128 v[174:177], v152 offset:17408
	ds_read_b128 v[178:181], v152 offset:18432
	ds_read_b128 v[182:185], v152 offset:19456
	ds_read_b128 v[186:189], v152 offset:20480
	ds_read_b128 v[190:193], v152 offset:21504
	ds_read_b128 v[194:197], v152 offset:22528
	ds_read_b128 v[198:201], v152 offset:23552
	s_waitcnt lgkmcnt(0)
	s_barrier
; #define G_STAGE(bufoff, gbase, voff) do { _Pragma("unroll") for (int _i = 0; _i < 2; ++_i) \
;         __builtin_amdgcn_global_load_lds((const unsigned*)((const char*)(gbase) + (voff)[_i]), (LAS unsigned*)(lds + (bufoff) + ldsw + _i * 8192), 16, 0, 0); } while (0)
; #define G_LDA(dst, b, h) do { _Pragma("unroll") for (int m = 0; m < 4; ++m) G_LD8(dst[m], lds + G_SA(b, h) + aoff + m * 2048); } while (0)
; #define G_LDB(dst, b, h) do { _Pragma("unroll") for (int n = 0; n < 2; ++n) G_LD8(dst[n], lds + G_SB(b, h) + boff + n * 2048); } while (0)
; #define G_WAIT_V(n) asm volatile("s_waitcnt vmcnt(" #n ")" ::: "memory")
; #define G_WAIT_L(n) asm volatile("s_waitcnt lgkmcnt(" #n ")" ::: "memory")
; #define G_BAR __builtin_amdgcn_s_barrier()
; #define G_SCHED __builtin_amdgcn_sched_barrier(0)
;     ...
;             G_WAIT_L(0); G_BAR; G_MMA(0, 0, At, B0); G_MMA(0, 1, At, B1); G_WAIT_V(8); G_BAR; G_SCHED;
;             G_LDA(At, 0, 1); G_STAGE(G_SB(0, 0), b02, voffB); G_STAGE(G_SB(0, 1), b12, voffB); G_STAGE(G_SA(0, 0), a02, vA0);
;             G_WAIT_L(0); G_BAR; G_MMA(1, 0, At, B0); G_MMA(1, 1, At, B1); G_WAIT_V(8); G_BAR; G_SCHED;
;             G_LDB(B0, 1, 0); G_LDB(B1, 1, 1); G_SCHED; G_LDA(At, 1, 0); G_STAGE(G_SA(0, 1), a12, vA1);
;             G_WAIT_L(0); G_BAR; G_MMA(0, 0, At, B0); G_MMA(0, 1, At, B1); G_WAIT_V(8); G_BAR; G_SCHED;
	s_setprio 1
	s_waitcnt lgkmcnt(0)
	v_mfma_i32_16x16x64_i8 v[60:63], v[132:135], v[170:173], v[60:63]
	v_mfma_i32_16x16x64_i8 v[56:59], v[140:143], v[170:173], v[56:59]
	v_mfma_i32_16x16x64_i8 v[44:47], v[132:135], v[178:181], v[44:47]
	v_mfma_i32_16x16x64_i8 v[40:43], v[140:143], v[178:181], v[40:43]
	v_mfma_i32_16x16x64_i8 v[28:31], v[132:135], v[186:189], v[28:31]
	v_mfma_i32_16x16x64_i8 v[24:27], v[140:143], v[186:189], v[24:27]
	v_mfma_i32_16x16x64_i8 v[12:15], v[132:135], v[194:197], v[12:15]
	v_mfma_i32_16x16x64_i8 v[8:11], v[140:143], v[194:197], v[8:11]
	v_mfma_i32_16x16x64_i8 v[60:63], v[136:139], v[174:177], v[60:63]
	v_mfma_i32_16x16x64_i8 v[56:59], v[144:147], v[174:177], v[56:59]
	v_mfma_i32_16x16x64_i8 v[44:47], v[136:139], v[182:185], v[44:47]
	v_mfma_i32_16x16x64_i8 v[40:43], v[144:147], v[182:185], v[40:43]
	v_mfma_i32_16x16x64_i8 v[28:31], v[136:139], v[190:193], v[28:31]
	v_mfma_i32_16x16x64_i8 v[24:27], v[144:147], v[190:193], v[24:27]
	v_mfma_i32_16x16x64_i8 v[12:15], v[136:139], v[198:201], v[12:15]
	v_mfma_i32_16x16x64_i8 v[8:11], v[144:147], v[198:201], v[8:11]
	v_mfma_i32_16x16x64_i8 v[52:55], v[154:157], v[170:173], v[52:55]
	v_mfma_i32_16x16x64_i8 v[48:51], v[162:165], v[170:173], v[48:51]
	v_mfma_i32_16x16x64_i8 v[36:39], v[154:157], v[178:181], v[36:39]
	v_mfma_i32_16x16x64_i8 v[32:35], v[162:165], v[178:181], v[32:35]
	v_mfma_i32_16x16x64_i8 v[20:23], v[154:157], v[186:189], v[20:23]
	v_mfma_i32_16x16x64_i8 v[16:19], v[162:165], v[186:189], v[16:19]
	v_mfma_i32_16x16x64_i8 v[4:7], v[154:157], v[194:197], v[4:7]
	v_mfma_i32_16x16x64_i8 v[0:3], v[162:165], v[194:197], v[0:3]
	v_mfma_i32_16x16x64_i8 v[52:55], v[158:161], v[174:177], v[52:55]
	v_mfma_i32_16x16x64_i8 v[48:51], v[166:169], v[174:177], v[48:51]
	v_mfma_i32_16x16x64_i8 v[36:39], v[158:161], v[182:185], v[36:39]
	v_mfma_i32_16x16x64_i8 v[32:35], v[166:169], v[182:185], v[32:35]
	v_mfma_i32_16x16x64_i8 v[20:23], v[158:161], v[190:193], v[20:23]
	v_mfma_i32_16x16x64_i8 v[16:19], v[166:169], v[190:193], v[16:19]
	v_mfma_i32_16x16x64_i8 v[4:7], v[158:161], v[198:201], v[4:7]
	v_mfma_i32_16x16x64_i8 v[0:3], v[166:169], v[198:201], v[0:3]
	s_setprio 0
	s_waitcnt vmcnt(8)
	s_barrier
	s_add_i32 s60, 0, 0x18000
	s_add_i32 s61, 0, 0x1c000
	s_mov_b32 m0, s11
	s_nop 0
	global_load_lds_dwordx4 v240, s[58:59]
	s_mov_b32 m0, s18
	s_nop 0
	global_load_lds_dwordx4 v242, s[58:59]
	v_add_u32_e32 v131, s60, v151
	ds_read_b128 v[132:135], v131
	ds_read_b128 v[136:139], v131 offset:1024
	ds_read_b128 v[140:143], v131 offset:2048
	ds_read_b128 v[144:147], v131 offset:3072
	v_add_u32_e32 v131, s61, v151
	ds_read_b128 v[154:157], v131
	ds_read_b128 v[158:161], v131 offset:1024
	ds_read_b128 v[162:165], v131 offset:2048
	ds_read_b128 v[166:169], v131 offset:3072
	ds_read_b128 v[170:173], v152 offset:32768
	ds_read_b128 v[174:177], v152 offset:33792
	ds_read_b128 v[178:181], v152 offset:34816
	ds_read_b128 v[182:185], v152 offset:35840
	ds_read_b128 v[186:189], v152 offset:36864
	ds_read_b128 v[190:193], v152 offset:37888
	ds_read_b128 v[194:197], v152 offset:38912
	ds_read_b128 v[198:201], v152 offset:39936
	s_waitcnt lgkmcnt(0)
	s_barrier
	s_setprio 1
	s_waitcnt lgkmcnt(0)
	v_mfma_i32_16x16x64_i8 v[124:127], v[132:135], v[170:173], v[124:127]
	v_mfma_i32_16x16x64_i8 v[120:123], v[140:143], v[170:173], v[120:123]
	v_mfma_i32_16x16x64_i8 v[108:111], v[132:135], v[178:181], v[108:111]
	v_mfma_i32_16x16x64_i8 v[104:107], v[140:143], v[178:181], v[104:107]
	v_mfma_i32_16x16x64_i8 v[92:95], v[132:135], v[186:189], v[92:95]
	v_mfma_i32_16x16x64_i8 v[88:91], v[140:143], v[186:189], v[88:91]
	v_mfma_i32_16x16x64_i8 v[76:79], v[132:135], v[194:197], v[76:79]
	v_mfma_i32_16x16x64_i8 v[72:75], v[140:143], v[194:197], v[72:75]
	v_mfma_i32_16x16x64_i8 v[124:127], v[136:139], v[174:177], v[124:127]
	v_mfma_i32_16x16x64_i8 v[120:123], v[144:147], v[174:177], v[120:123]
	v_mfma_i32_16x16x64_i8 v[108:111], v[136:139], v[182:185], v[108:111]
	v_mfma_i32_16x16x64_i8 v[104:107], v[144:147], v[182:185], v[104:107]
	v_mfma_i32_16x16x64_i8 v[92:95], v[136:139], v[190:193], v[92:95]
	v_mfma_i32_16x16x64_i8 v[88:91], v[144:147], v[190:193], v[88:91]
	v_mfma_i32_16x16x64_i8 v[76:79], v[136:139], v[198:201], v[76:79]
	v_mfma_i32_16x16x64_i8 v[72:75], v[144:147], v[198:201], v[72:75]
	v_mfma_i32_16x16x64_i8 v[116:119], v[154:157], v[170:173], v[116:119]
	v_mfma_i32_16x16x64_i8 v[112:115], v[162:165], v[170:173], v[112:115]
	v_mfma_i32_16x16x64_i8 v[100:103], v[154:157], v[178:181], v[100:103]
	v_mfma_i32_16x16x64_i8 v[96:99], v[162:165], v[178:181], v[96:99]
	v_mfma_i32_16x16x64_i8 v[84:87], v[154:157], v[186:189], v[84:87]
	v_mfma_i32_16x16x64_i8 v[80:83], v[162:165], v[186:189], v[80:83]
	v_mfma_i32_16x16x64_i8 v[68:71], v[154:157], v[194:197], v[68:71]
	v_mfma_i32_16x16x64_i8 v[64:67], v[162:165], v[194:197], v[64:67]
	v_mfma_i32_16x16x64_i8 v[116:119], v[158:161], v[174:177], v[116:119]
	v_mfma_i32_16x16x64_i8 v[112:115], v[166:169], v[174:177], v[112:115]
	v_mfma_i32_16x16x64_i8 v[100:103], v[158:161], v[182:185], v[100:103]
	v_mfma_i32_16x16x64_i8 v[96:99], v[166:169], v[182:185], v[96:99]
	v_mfma_i32_16x16x64_i8 v[84:87], v[158:161], v[190:193], v[84:87]
	v_mfma_i32_16x16x64_i8 v[80:83], v[166:169], v[190:193], v[80:83]
	v_mfma_i32_16x16x64_i8 v[68:71], v[158:161], v[198:201], v[68:71]
	v_mfma_i32_16x16x64_i8 v[64:67], v[166:169], v[198:201], v[64:67]
	s_setprio 0
	s_waitcnt vmcnt(8)
	s_barrier
; #define G_STAGE(bufoff, gbase, voff) do { _Pragma("unroll") for (int _i = 0; _i < 2; ++_i) \
;         __builtin_amdgcn_global_load_lds((const unsigned*)((const char*)(gbase) + (voff)[_i]), (LAS unsigned*)(lds + (bufoff) + ldsw + _i * 8192), 16, 0, 0); } while (0)
; #define G_LDA(dst, b, h) do { _Pragma("unroll") for (int m = 0; m < 4; ++m) G_LD8(dst[m], lds + G_SA(b, h) + aoff + m * 2048); } while (0)
; #define G_WAIT_V(n) asm volatile("s_waitcnt vmcnt(" #n ")" ::: "memory")
; #define G_WAIT_L(n) asm volatile("s_waitcnt lgkmcnt(" #n ")" ::: "memory")
; #define G_BAR __builtin_amdgcn_s_barrier()
; #define G_SCHED __builtin_amdgcn_sched_barrier(0)
;     ...
;             G_LDA(At, 1, 1); G_STAGE(G_SB(1, 0), b02 + kstep, voffB); G_STAGE(G_SB(1, 1), b12 + kstep, voffB); G_STAGE(G_SA(1, 0), a02 + kstep, vA0);
;             G_WAIT_L(0); G_BAR; G_MMA(1, 0, At, B0); G_MMA(1, 1, At, B1); G_WAIT_V(8); G_BAR; G_SCHED;
;         }
	s_add_i32 s58, s60, s97
	v_lshl_add_u64 v[130:131], v[206:207], 0, s[8:9]
	s_mov_b32 m0, s58
	s_nop 0
	global_load_lds_dwordx4 v[130:131], off
	v_lshl_add_u64 v[130:131], v[208:209], 0, s[8:9]
	s_add_i32 m0, s58, 0x2000
	s_add_i32 s58, s61, s97
	global_load_lds_dwordx4 v[130:131], off
	v_lshl_add_u64 v[130:131], v[210:211], 0, s[8:9]
	s_mov_b32 m0, s58
	s_nop 0
	global_load_lds_dwordx4 v[130:131], off
	v_lshl_add_u64 v[130:131], v[202:203], 0, s[8:9]
	s_add_i32 m0, s58, 0x2000
	s_nop 0
	global_load_lds_dwordx4 v[130:131], off
	v_lshl_add_u64 v[130:131], v[204:205], 0, s[8:9]
	s_mov_b32 m0, s20
	s_nop 0
	global_load_lds_dwordx4 v[130:131], off
	v_lshl_add_u64 v[130:131], v[212:213], 0, s[8:9]
	s_mov_b32 m0, s21
	s_nop 0
	global_load_lds_dwordx4 v[130:131], off
	ds_read_b128 v[170:173], v152 offset:49152
	ds_read_b128 v[174:177], v152 offset:50176
	ds_read_b128 v[178:181], v152 offset:51200
	ds_read_b128 v[182:185], v152 offset:52224
	ds_read_b128 v[186:189], v152 offset:53248
	ds_read_b128 v[190:193], v152 offset:54272
	ds_read_b128 v[194:197], v152 offset:55296
	ds_read_b128 v[198:201], v152 offset:56320
	s_waitcnt lgkmcnt(0)
	s_barrier
	s_setprio 1
	s_waitcnt lgkmcnt(0)
	v_mfma_i32_16x16x64_i8 v[60:63], v[132:135], v[170:173], v[60:63]
	v_mfma_i32_16x16x64_i8 v[56:59], v[140:143], v[170:173], v[56:59]
	v_mfma_i32_16x16x64_i8 v[44:47], v[132:135], v[178:181], v[44:47]
	v_mfma_i32_16x16x64_i8 v[40:43], v[140:143], v[178:181], v[40:43]
	v_mfma_i32_16x16x64_i8 v[28:31], v[132:135], v[186:189], v[28:31]
	v_mfma_i32_16x16x64_i8 v[24:27], v[140:143], v[186:189], v[24:27]
	v_mfma_i32_16x16x64_i8 v[12:15], v[132:135], v[194:197], v[12:15]
	v_mfma_i32_16x16x64_i8 v[8:11], v[140:143], v[194:197], v[8:11]
	v_mfma_i32_16x16x64_i8 v[60:63], v[136:139], v[174:177], v[60:63]
	v_mfma_i32_16x16x64_i8 v[56:59], v[144:147], v[174:177], v[56:59]
	v_mfma_i32_16x16x64_i8 v[44:47], v[136:139], v[182:185], v[44:47]
	v_mfma_i32_16x16x64_i8 v[40:43], v[144:147], v[182:185], v[40:43]
	v_mfma_i32_16x16x64_i8 v[28:31], v[136:139], v[190:193], v[28:31]
	v_mfma_i32_16x16x64_i8 v[24:27], v[144:147], v[190:193], v[24:27]
	v_mfma_i32_16x16x64_i8 v[12:15], v[136:139], v[198:201], v[12:15]
	v_mfma_i32_16x16x64_i8 v[8:11], v[144:147], v[198:201], v[8:11]
	v_mfma_i32_16x16x64_i8 v[52:55], v[154:157], v[170:173], v[52:55]
	v_mfma_i32_16x16x64_i8 v[48:51], v[162:165], v[170:173], v[48:51]
	v_mfma_i32_16x16x64_i8 v[36:39], v[154:157], v[178:181], v[36:39]
	v_mfma_i32_16x16x64_i8 v[32:35], v[162:165], v[178:181], v[32:35]
	v_mfma_i32_16x16x64_i8 v[20:23], v[154:157], v[186:189], v[20:23]
	v_mfma_i32_16x16x64_i8 v[16:19], v[162:165], v[186:189], v[16:19]
	v_mfma_i32_16x16x64_i8 v[4:7], v[154:157], v[194:197], v[4:7]
	v_mfma_i32_16x16x64_i8 v[0:3], v[162:165], v[194:197], v[0:3]
	v_mfma_i32_16x16x64_i8 v[52:55], v[158:161], v[174:177], v[52:55]
	v_mfma_i32_16x16x64_i8 v[48:51], v[166:169], v[174:177], v[48:51]
	v_mfma_i32_16x16x64_i8 v[36:39], v[158:161], v[182:185], v[36:39]
	v_mfma_i32_16x16x64_i8 v[32:35], v[166:169], v[182:185], v[32:35]
	v_mfma_i32_16x16x64_i8 v[20:23], v[158:161], v[190:193], v[20:23]
	v_mfma_i32_16x16x64_i8 v[16:19], v[166:169], v[190:193], v[16:19]
	v_mfma_i32_16x16x64_i8 v[4:7], v[158:161], v[198:201], v[4:7]
	v_mfma_i32_16x16x64_i8 v[0:3], v[166:169], v[198:201], v[0:3]
	s_setprio 0
	s_waitcnt vmcnt(8)
	s_barrier
	s_add_u32 s43, s43, 0x100
	s_addc_u32 s55, s55, 0
	s_add_u32 s64, s64, 0x100
	s_addc_u32 s65, s65, 0
	s_add_u32 s66, s66, 0x100
	s_addc_u32 s67, s67, 0
	s_add_u32 s56, s56, 0x100
	s_addc_u32 s57, s57, 0
	s_cmp_ge_i32 s68, s0
	s_mov_b32 s58, s68
	s_cbranch_scc0 .LBB0_249
	s_and_b64 vcc, exec, s[40:41]
	s_cbranch_vccz .LBB0_252

; #define G_STAGE(bufoff, gbase, voff) do { _Pragma("unroll") for (int _i = 0; _i < 2; ++_i) \
;         __builtin_amdgcn_global_load_lds((const unsigned*)((const char*)(gbase) + (voff)[_i]), (LAS unsigned*)(lds + (bufoff) + ldsw + _i * 8192), 16, 0, 0); } while (0)
; #define G_LDA(dst, b, h) do { _Pragma("unroll") for (int m = 0; m < 4; ++m) G_LD8(dst[m], lds + G_SA(b, h) + aoff + m * 2048); } while (0)
; #define G_LDB(dst, b, h) do { _Pragma("unroll") for (int n = 0; n < 2; ++n) G_LD8(dst[n], lds + G_SB(b, h) + boff + n * 2048); } while (0)
; #define G_WAIT_V(n) asm volatile("s_waitcnt vmcnt(" #n ")" ::: "memory")
; #define G_WAIT_L(n) asm volatile("s_waitcnt lgkmcnt(" #n ")" ::: "memory")
; #define G_BAR __builtin_amdgcn_s_barrier()
; #define G_SCHED __builtin_amdgcn_sched_barrier(0)
;     __device__ __forceinline__ unsigned row_off(const Unit& u, int r, LAS unsigned char* lds) const { return (unsigned)((const LAS int*)(lds + LDS_STAGE + u.q * 4096))[r] * (unsigned)rowbytes; }
;     ...
;             const char* a11 = cur.a1 + (size_t)(t + 1) * kstep;
;             const char* a02 = last ? nxt.a0 : cur.a0 + (size_t)(t + 2) * kstep; const char* a12 = last ? nxt.a1 : cur.a1 + (size_t)(t + 2) * kstep;
;             const char* b02 = last ? nxt.b0 : cur.b0 + (size_t)(t + 2) * kstep; const char* b12 = last ? nxt.b1 : cur.b1 + (size_t)(t + 2) * kstep;
;             G_LDB(B0, 0, 0); G_LDB(B1, 0, 1); G_SCHED; G_LDA(At, 0, 0); G_STAGE(G_SA(1, 1), a11, vA1);
;             if constexpr (GATHER) { if (last) { int tz = tid; asm volatile("" : "+v"(tz));
; #pragma unroll
;                 for (int i = 0; i < 2; ++i) { int R, C; stage_rc(tz * 16 + i * 8192, R, C); gc0[i] = S.row_off(nxt, R, lds) + (unsigned)C * 2u; gc1[i] = S.row_off(nxt, 128 + R, lds) + (unsigned)C * 2u; } } }
;             G_WAIT_L(0); G_BAR; G_MMA(0, 0, At, B0); G_MMA(0, 1, At, B1); G_WAIT_V(8); G_BAR; G_SCHED;
;             G_LDA(At, 0, 1); G_STAGE(G_SB(0, 0), b02, voffB); G_STAGE(G_SB(0, 1), b12, voffB); G_STAGE(G_SA(0, 0), a02, vA0);
.LBB0_284:
	s_add_i32 s76, s64, 2
	s_add_u32 s77, s62, 0x80
	s_addc_u32 s65, s63, 0
	s_add_i32 s79, s24, s97
	s_add_i32 m0, s0, 0xc000
	s_add_i32 s78, s0, 0xe000
	s_add_i32 s80, s79, 0x2000
	s_cmp_eq_u32 s23, s64
	s_cselect_b32 s64, s50, s77
	s_cselect_b32 s67, s49, s75
	s_cselect_b32 s66, s48, s71
	s_cselect_b32 s69, s53, s59
	s_cselect_b32 s68, s52, s45
	s_cselect_b32 s65, s51, s65
	global_load_lds_dwordx4 v240, s[62:63]
	s_mov_b32 m0, s78
	s_nop 0
	global_load_lds_dwordx4 v242, s[62:63]
	v_add_u32_e32 v144, s24, v157
	v_add_u32_e32 v168, s25, v157
	ds_read_b128 v[100:103], v144
	ds_read_b128 v[112:115], v144 offset:1024
	ds_read_b128 v[120:123], v144 offset:2048
	ds_read_b128 v[144:147], v144 offset:3072
	ds_read_b128 v[150:153], v168
	ds_read_b128 v[160:163], v168 offset:1024
	ds_read_b128 v[164:167], v168 offset:2048
	ds_read_b128 v[168:171], v168 offset:3072
	ds_read_b128 v[172:175], v158
	ds_read_b128 v[176:179], v158 offset:1024
	ds_read_b128 v[180:183], v158 offset:2048
	ds_read_b128 v[184:187], v158 offset:3072
	ds_read_b128 v[188:191], v158 offset:4096
	ds_read_b128 v[192:195], v158 offset:5120
	ds_read_b128 v[196:199], v158 offset:6144
	ds_read_b128 v[200:203], v158 offset:7168
	s_waitcnt lgkmcnt(0)
	v_mov_b32_e32 v93, v149
	s_barrier
	s_setprio 1
	s_waitcnt lgkmcnt(0)
	v_mfma_i32_16x16x64_i8 v[140:143], v[100:103], v[172:175], v[140:143]
	v_mfma_i32_16x16x64_i8 v[132:135], v[120:123], v[172:175], v[132:135]
	v_mfma_i32_16x16x64_i8 v[94:97], v[100:103], v[180:183], v[96:99]
	v_mfma_i32_16x16x64_i8 v[88:91], v[120:123], v[180:183], v[88:91]
	v_mfma_i32_16x16x64_i8 v[60:63], v[100:103], v[188:191], v[60:63]
	v_mfma_i32_16x16x64_i8 v[56:59], v[120:123], v[188:191], v[56:59]
	v_mfma_i32_16x16x64_i8 v[28:31], v[100:103], v[196:199], v[28:31]
	v_mfma_i32_16x16x64_i8 v[24:27], v[120:123], v[196:199], v[24:27]
	v_mfma_i32_16x16x64_i8 v[140:143], v[112:115], v[176:179], v[140:143]
	v_mfma_i32_16x16x64_i8 v[132:135], v[144:147], v[176:179], v[132:135]
	v_mfma_i32_16x16x64_i8 v[94:97], v[112:115], v[184:187], v[94:97]
	v_mfma_i32_16x16x64_i8 v[88:91], v[144:147], v[184:187], v[88:91]
	v_mfma_i32_16x16x64_i8 v[60:63], v[112:115], v[192:195], v[60:63]
	v_mfma_i32_16x16x64_i8 v[56:59], v[144:147], v[192:195], v[56:59]
	v_mfma_i32_16x16x64_i8 v[28:31], v[112:115], v[200:203], v[28:31]
	v_mfma_i32_16x16x64_i8 v[24:27], v[144:147], v[200:203], v[24:27]
	v_mfma_i32_16x16x64_i8 v[124:127], v[150:153], v[172:175], v[124:127]
	v_mfma_i32_16x16x64_i8 v[108:111], v[164:167], v[172:175], v[108:111]
	v_mfma_i32_16x16x64_i8 v[76:79], v[150:153], v[180:183], v[76:79]
	v_mfma_i32_16x16x64_i8 v[72:75], v[164:167], v[180:183], v[72:75]
	v_mfma_i32_16x16x64_i8 v[44:47], v[150:153], v[188:191], v[44:47]
	v_mfma_i32_16x16x64_i8 v[40:43], v[164:167], v[188:191], v[40:43]
	v_mfma_i32_16x16x64_i8 v[12:15], v[150:153], v[196:199], v[12:15]
	v_mfma_i32_16x16x64_i8 v[8:11], v[164:167], v[196:199], v[8:11]
	v_mfma_i32_16x16x64_i8 v[124:127], v[160:163], v[176:179], v[124:127]
	v_mfma_i32_16x16x64_i8 v[108:111], v[168:171], v[176:179], v[108:111]
	v_mfma_i32_16x16x64_i8 v[76:79], v[160:163], v[184:187], v[76:79]
	v_mfma_i32_16x16x64_i8 v[72:75], v[168:171], v[184:187], v[72:75]
	v_mfma_i32_16x16x64_i8 v[44:47], v[160:163], v[192:195], v[44:47]
	v_mfma_i32_16x16x64_i8 v[40:43], v[168:171], v[192:195], v[40:43]
	v_mfma_i32_16x16x64_i8 v[12:15], v[160:163], v[200:203], v[12:15]
	v_mfma_i32_16x16x64_i8 v[8:11], v[168:171], v[200:203], v[8:11]
	s_setprio 0
	s_waitcnt vmcnt(8)
	s_barrier
	s_mov_b32 m0, s79
	v_mov_b32_e32 v205, v149
	global_load_lds_dwordx4 v244, s[68:69]
	v_mov_b32_e32 v207, v149
	s_mov_b32 m0, s80
	v_lshl_add_u64 v[208:209], s[68:69], 0, v[244:245]
	v_lshl_add_u64 v[210:211], s[68:69], 0, v[246:247]
	global_load_lds_dwordx4 v246, s[68:69]
	s_cselect_b32 s69, s55, s70
	s_cselect_b32 s68, s54, s61
	s_add_i32 s77, s25, s97
	s_mov_b32 m0, s77
	v_lshl_add_u64 v[212:213], s[68:69], 0, v[244:245]
	global_load_lds_dwordx4 v244, s[68:69]
	s_add_i32 m0, s77, 0x2000
	v_lshl_add_u64 v[204:205], s[68:69], 0, v[246:247]
	global_load_lds_dwordx4 v246, s[68:69]
	s_mov_b32 m0, s0
	v_lshl_add_u64 v[206:207], s[66:67], 0, v[240:241]
	global_load_lds_dwordx4 v240, s[66:67]
	s_mov_b32 m0, s11
	v_lshl_add_u64 v[214:215], s[66:67], 0, v[242:243]
	global_load_lds_dwordx4 v242, s[66:67]
	ds_read_b128 v[172:175], v158 offset:16384
	ds_read_b128 v[176:179], v158 offset:17408
	ds_read_b128 v[180:183], v158 offset:18432
	ds_read_b128 v[184:187], v158 offset:19456
	ds_read_b128 v[188:191], v158 offset:20480
	ds_read_b128 v[192:195], v158 offset:21504
	ds_read_b128 v[196:199], v158 offset:22528
	ds_read_b128 v[200:203], v158 offset:23552
	s_waitcnt lgkmcnt(0)
	s_barrier
; #define G_STAGE(bufoff, gbase, voff) do { _Pragma("unroll") for (int _i = 0; _i < 2; ++_i) \
;         __builtin_amdgcn_global_load_lds((const unsigned*)((const char*)(gbase) + (voff)[_i]), (LAS unsigned*)(lds + (bufoff) + ldsw + _i * 8192), 16, 0, 0); } while (0)
; #define G_LDA(dst, b, h) do { _Pragma("unroll") for (int m = 0; m < 4; ++m) G_LD8(dst[m], lds + G_SA(b, h) + aoff + m * 2048); } while (0)
; #define G_LDB(dst, b, h) do { _Pragma("unroll") for (int n = 0; n < 2; ++n) G_LD8(dst[n], lds + G_SB(b, h) + boff + n * 2048); } while (0)
; #define G_WAIT_V(n) asm volatile("s_waitcnt vmcnt(" #n ")" ::: "memory")
; #define G_WAIT_L(n) asm volatile("s_waitcnt lgkmcnt(" #n ")" ::: "memory")
; #define G_BAR __builtin_amdgcn_s_barrier()
; #define G_SCHED __builtin_amdgcn_sched_barrier(0)
;     ...
;             G_WAIT_L(0); G_BAR; G_MMA(0, 0, At, B0); G_MMA(0, 1, At, B1); G_WAIT_V(8); G_BAR; G_SCHED;
;             G_LDA(At, 0, 1); G_STAGE(G_SB(0, 0), b02, voffB); G_STAGE(G_SB(0, 1), b12, voffB); G_STAGE(G_SA(0, 0), a02, vA0);
;             G_WAIT_L(0); G_BAR; G_MMA(1, 0, At, B0); G_MMA(1, 1, At, B1); G_WAIT_V(8); G_BAR; G_SCHED;
;             G_LDB(B0, 1, 0); G_LDB(B1, 1, 1); G_SCHED; G_LDA(At, 1, 0); G_STAGE(G_SA(0, 1), a12, vA1);
;             G_WAIT_L(0); G_BAR; G_MMA(0, 0, At, B0); G_MMA(0, 1, At, B1); G_WAIT_V(8); G_BAR; G_SCHED;
	s_setprio 1
	s_waitcnt lgkmcnt(0)
	v_mfma_i32_16x16x64_i8 v[136:139], v[100:103], v[172:175], v[136:139]
	v_mfma_i32_16x16x64_i8 v[128:131], v[120:123], v[172:175], v[128:131]
	v_mfma_i32_16x16x64_i8 v[84:87], v[100:103], v[180:183], v[84:87]
	v_mfma_i32_16x16x64_i8 v[80:83], v[120:123], v[180:183], v[80:83]
	v_mfma_i32_16x16x64_i8 v[52:55], v[100:103], v[188:191], v[52:55]
	v_mfma_i32_16x16x64_i8 v[48:51], v[120:123], v[188:191], v[48:51]
	v_mfma_i32_16x16x64_i8 v[20:23], v[100:103], v[196:199], v[20:23]
	v_mfma_i32_16x16x64_i8 v[16:19], v[120:123], v[196:199], v[16:19]
	v_mfma_i32_16x16x64_i8 v[136:139], v[112:115], v[176:179], v[136:139]
	v_mfma_i32_16x16x64_i8 v[128:131], v[144:147], v[176:179], v[128:131]
	v_mfma_i32_16x16x64_i8 v[84:87], v[112:115], v[184:187], v[84:87]
	v_mfma_i32_16x16x64_i8 v[80:83], v[144:147], v[184:187], v[80:83]
	v_mfma_i32_16x16x64_i8 v[52:55], v[112:115], v[192:195], v[52:55]
	v_mfma_i32_16x16x64_i8 v[48:51], v[144:147], v[192:195], v[48:51]
	v_mfma_i32_16x16x64_i8 v[20:23], v[112:115], v[200:203], v[20:23]
	v_mfma_i32_16x16x64_i8 v[16:19], v[144:147], v[200:203], v[16:19]
	v_mfma_i32_16x16x64_i8 v[104:107], v[164:167], v[172:175], v[104:107]
	v_mfma_i32_16x16x64_i8 v[68:71], v[150:153], v[180:183], v[68:71]
	v_mfma_i32_16x16x64_i8 v[64:67], v[164:167], v[180:183], v[64:67]
	v_mfma_i32_16x16x64_i8 v[36:39], v[150:153], v[188:191], v[36:39]
	v_mfma_i32_16x16x64_i8 v[32:35], v[164:167], v[188:191], v[32:35]
	v_mfma_i32_16x16x64_i8 v[4:7], v[150:153], v[196:199], v[4:7]
	v_mfma_i32_16x16x64_i8 v[0:3], v[164:167], v[196:199], v[0:3]
	v_mfma_i32_16x16x64_i8 v[98:101], v[150:153], v[172:175], v[116:119]
	v_mfma_i32_16x16x64_i8 v[104:107], v[168:171], v[176:179], v[104:107]
	v_mfma_i32_16x16x64_i8 v[68:71], v[160:163], v[184:187], v[68:71]
	v_mfma_i32_16x16x64_i8 v[64:67], v[168:171], v[184:187], v[64:67]
	v_mfma_i32_16x16x64_i8 v[36:39], v[160:163], v[192:195], v[36:39]
	v_mfma_i32_16x16x64_i8 v[32:35], v[168:171], v[192:195], v[32:35]
	v_mfma_i32_16x16x64_i8 v[4:7], v[160:163], v[200:203], v[4:7]
	v_mfma_i32_16x16x64_i8 v[0:3], v[168:171], v[200:203], v[0:3]
	v_mfma_i32_16x16x64_i8 v[100:103], v[160:163], v[176:179], v[98:101]
	s_setprio 0
	s_waitcnt vmcnt(8)
	s_barrier
	s_add_i32 s66, 0, 0x18000
	s_add_i32 s67, 0, 0x1c000
	s_mov_b32 m0, s18
	s_nop 0
	global_load_lds_dwordx4 v240, s[64:65]
	s_mov_b32 m0, s19
	s_nop 0
	global_load_lds_dwordx4 v242, s[64:65]
	v_add_u32_e32 v93, s66, v157
	ds_read_b128 v[112:115], v93
	ds_read_b128 v[116:119], v93 offset:1024
	ds_read_b128 v[120:123], v93 offset:2048
	ds_read_b128 v[144:147], v93 offset:3072
	v_add_u32_e32 v93, s67, v157
	ds_read_b128 v[150:153], v93
	ds_read_b128 v[160:163], v93 offset:1024
	ds_read_b128 v[164:167], v93 offset:2048
	ds_read_b128 v[168:171], v93 offset:3072
	ds_read_b128 v[172:175], v158 offset:32768
	ds_read_b128 v[176:179], v158 offset:33792
	ds_read_b128 v[180:183], v158 offset:34816
	ds_read_b128 v[184:187], v158 offset:35840
	ds_read_b128 v[188:191], v158 offset:36864
	ds_read_b128 v[192:195], v158 offset:37888
	ds_read_b128 v[196:199], v158 offset:38912
	ds_read_b128 v[200:203], v158 offset:39936
	s_waitcnt lgkmcnt(0)
	s_barrier
	s_setprio 1
	s_waitcnt lgkmcnt(0)
	v_mfma_i32_16x16x64_i8 v[140:143], v[112:115], v[172:175], v[140:143]
	v_mfma_i32_16x16x64_i8 v[132:135], v[120:123], v[172:175], v[132:135]
	v_mfma_i32_16x16x64_i8 v[92:95], v[112:115], v[180:183], v[94:97]
	v_mfma_i32_16x16x64_i8 v[88:91], v[120:123], v[180:183], v[88:91]
	v_mfma_i32_16x16x64_i8 v[60:63], v[112:115], v[188:191], v[60:63]
	v_mfma_i32_16x16x64_i8 v[56:59], v[120:123], v[188:191], v[56:59]
	v_mfma_i32_16x16x64_i8 v[28:31], v[112:115], v[196:199], v[28:31]
	v_mfma_i32_16x16x64_i8 v[24:27], v[120:123], v[196:199], v[24:27]
	v_mfma_i32_16x16x64_i8 v[140:143], v[116:119], v[176:179], v[140:143]
	v_mfma_i32_16x16x64_i8 v[132:135], v[144:147], v[176:179], v[132:135]
	v_mfma_i32_16x16x64_i8 v[96:99], v[116:119], v[184:187], v[92:95]
	v_mfma_i32_16x16x64_i8 v[88:91], v[144:147], v[184:187], v[88:91]
	v_mfma_i32_16x16x64_i8 v[60:63], v[116:119], v[192:195], v[60:63]
	v_mfma_i32_16x16x64_i8 v[56:59], v[144:147], v[192:195], v[56:59]
	v_mfma_i32_16x16x64_i8 v[28:31], v[116:119], v[200:203], v[28:31]
	v_mfma_i32_16x16x64_i8 v[24:27], v[144:147], v[200:203], v[24:27]
	v_mfma_i32_16x16x64_i8 v[92:95], v[150:153], v[172:175], v[124:127]
	v_mfma_i32_16x16x64_i8 v[124:127], v[160:163], v[176:179], v[92:95]
	v_mfma_i32_16x16x64_i8 v[92:95], v[164:167], v[172:175], v[108:111]
	v_mfma_i32_16x16x64_i8 v[76:79], v[150:153], v[180:183], v[76:79]
	v_mfma_i32_16x16x64_i8 v[72:75], v[164:167], v[180:183], v[72:75]
	v_mfma_i32_16x16x64_i8 v[44:47], v[150:153], v[188:191], v[44:47]
	v_mfma_i32_16x16x64_i8 v[40:43], v[164:167], v[188:191], v[40:43]
	v_mfma_i32_16x16x64_i8 v[12:15], v[150:153], v[196:199], v[12:15]
	v_mfma_i32_16x16x64_i8 v[8:11], v[164:167], v[196:199], v[8:11]
	v_mfma_i32_16x16x64_i8 v[108:111], v[168:171], v[176:179], v[92:95]
	v_mfma_i32_16x16x64_i8 v[76:79], v[160:163], v[184:187], v[76:79]
	v_mfma_i32_16x16x64_i8 v[72:75], v[168:171], v[184:187], v[72:75]
	v_mfma_i32_16x16x64_i8 v[44:47], v[160:163], v[192:195], v[44:47]
	v_mfma_i32_16x16x64_i8 v[40:43], v[168:171], v[192:195], v[40:43]
	v_mfma_i32_16x16x64_i8 v[12:15], v[160:163], v[200:203], v[12:15]
	v_mfma_i32_16x16x64_i8 v[8:11], v[168:171], v[200:203], v[8:11]
	s_setprio 0
	s_waitcnt vmcnt(8)
	s_barrier
; #define G_STAGE(bufoff, gbase, voff) do { _Pragma("unroll") for (int _i = 0; _i < 2; ++_i) \
;         __builtin_amdgcn_global_load_lds((const unsigned*)((const char*)(gbase) + (voff)[_i]), (LAS unsigned*)(lds + (bufoff) + ldsw + _i * 8192), 16, 0, 0); } while (0)
; #define G_LDA(dst, b, h) do { _Pragma("unroll") for (int m = 0; m < 4; ++m) G_LD8(dst[m], lds + G_SA(b, h) + aoff + m * 2048); } while (0)
; #define G_WAIT_V(n) asm volatile("s_waitcnt vmcnt(" #n ")" ::: "memory")
; #define G_WAIT_L(n) asm volatile("s_waitcnt lgkmcnt(" #n ")" ::: "memory")
; #define G_BAR __builtin_amdgcn_s_barrier()
; #define G_SCHED __builtin_amdgcn_sched_barrier(0)
;     ...
;             G_LDA(At, 1, 1); G_STAGE(G_SB(1, 0), b02 + kstep, voffB); G_STAGE(G_SB(1, 1), b12 + kstep, voffB); G_STAGE(G_SA(1, 0), a02 + kstep, vA0);
;             G_WAIT_L(0); G_BAR; G_MMA(1, 0, At, B0); G_MMA(1, 1, At, B1); G_WAIT_V(8); G_BAR; G_SCHED;
;         }
	s_add_i32 s64, s66, s97
	v_lshl_add_u64 v[200:201], v[208:209], 0, s[38:39]
	s_mov_b32 m0, s64
	s_nop 0
	global_load_lds_dwordx4 v[200:201], off
	v_lshl_add_u64 v[200:201], v[210:211], 0, s[38:39]
	s_add_i32 m0, s64, 0x2000
	s_add_i32 s64, s67, s97
	global_load_lds_dwordx4 v[200:201], off
	v_lshl_add_u64 v[200:201], v[212:213], 0, s[38:39]
	s_mov_b32 m0, s64
	s_nop 0
	global_load_lds_dwordx4 v[200:201], off
	v_lshl_add_u64 v[200:201], v[204:205], 0, s[38:39]
	s_add_i32 m0, s64, 0x2000
	s_nop 0
	global_load_lds_dwordx4 v[200:201], off
	v_lshl_add_u64 v[200:201], v[206:207], 0, s[38:39]
	s_mov_b32 m0, s21
	s_nop 0
	global_load_lds_dwordx4 v[200:201], off
	v_lshl_add_u64 v[200:201], v[214:215], 0, s[38:39]
	s_mov_b32 m0, s22
	s_nop 0
	global_load_lds_dwordx4 v[200:201], off
	ds_read_b128 v[92:95], v158 offset:49152
	ds_read_b128 v[172:175], v158 offset:50176
	ds_read_b128 v[176:179], v158 offset:51200
	ds_read_b128 v[180:183], v158 offset:52224
	ds_read_b128 v[184:187], v158 offset:53248
	ds_read_b128 v[188:191], v158 offset:54272
	ds_read_b128 v[192:195], v158 offset:55296
	ds_read_b128 v[196:199], v158 offset:56320
	s_waitcnt lgkmcnt(0)
	s_barrier
	s_setprio 1
	s_waitcnt lgkmcnt(0)
	v_mfma_i32_16x16x64_i8 v[136:139], v[112:115], v[92:95], v[136:139]
	v_mfma_i32_16x16x64_i8 v[128:131], v[120:123], v[92:95], v[128:131]
	v_mfma_i32_16x16x64_i8 v[84:87], v[112:115], v[176:179], v[84:87]
	v_mfma_i32_16x16x64_i8 v[80:83], v[120:123], v[176:179], v[80:83]
	v_mfma_i32_16x16x64_i8 v[52:55], v[112:115], v[184:187], v[52:55]
	v_mfma_i32_16x16x64_i8 v[48:51], v[120:123], v[184:187], v[48:51]
	v_mfma_i32_16x16x64_i8 v[20:23], v[112:115], v[192:195], v[20:23]
	v_mfma_i32_16x16x64_i8 v[16:19], v[120:123], v[192:195], v[16:19]
	v_mfma_i32_16x16x64_i8 v[136:139], v[116:119], v[172:175], v[136:139]
	v_mfma_i32_16x16x64_i8 v[128:131], v[144:147], v[172:175], v[128:131]
	v_mfma_i32_16x16x64_i8 v[84:87], v[116:119], v[180:183], v[84:87]
	v_mfma_i32_16x16x64_i8 v[80:83], v[144:147], v[180:183], v[80:83]
	v_mfma_i32_16x16x64_i8 v[52:55], v[116:119], v[188:191], v[52:55]
	v_mfma_i32_16x16x64_i8 v[48:51], v[144:147], v[188:191], v[48:51]
	v_mfma_i32_16x16x64_i8 v[20:23], v[116:119], v[196:199], v[20:23]
	v_mfma_i32_16x16x64_i8 v[16:19], v[144:147], v[196:199], v[16:19]
	v_mfma_i32_16x16x64_i8 v[100:103], v[150:153], v[92:95], v[100:103]
	v_mfma_i32_16x16x64_i8 v[92:95], v[164:167], v[92:95], v[104:107]
	v_mfma_i32_16x16x64_i8 v[68:71], v[150:153], v[176:179], v[68:71]
	v_mfma_i32_16x16x64_i8 v[64:67], v[164:167], v[176:179], v[64:67]
	v_mfma_i32_16x16x64_i8 v[36:39], v[150:153], v[184:187], v[36:39]
	v_mfma_i32_16x16x64_i8 v[32:35], v[164:167], v[184:187], v[32:35]
	v_mfma_i32_16x16x64_i8 v[4:7], v[150:153], v[192:195], v[4:7]
	v_mfma_i32_16x16x64_i8 v[0:3], v[164:167], v[192:195], v[0:3]
	v_mfma_i32_16x16x64_i8 v[116:119], v[160:163], v[172:175], v[100:103]
	v_mfma_i32_16x16x64_i8 v[104:107], v[168:171], v[172:175], v[92:95]
	v_mfma_i32_16x16x64_i8 v[68:71], v[160:163], v[180:183], v[68:71]
	v_mfma_i32_16x16x64_i8 v[64:67], v[168:171], v[180:183], v[64:67]
	v_mfma_i32_16x16x64_i8 v[36:39], v[160:163], v[188:191], v[36:39]
	v_mfma_i32_16x16x64_i8 v[32:35], v[168:171], v[188:191], v[32:35]
	v_mfma_i32_16x16x64_i8 v[4:7], v[160:163], v[196:199], v[4:7]
	v_mfma_i32_16x16x64_i8 v[0:3], v[168:171], v[196:199], v[0:3]
	s_setprio 0
	s_waitcnt vmcnt(8)
	s_barrier
	s_add_u32 s45, s45, 0x100
	s_addc_u32 s59, s59, 0
	s_add_u32 s61, s61, 0x100
	s_addc_u32 s70, s70, 0
	s_add_u32 s71, s71, 0x100
	s_addc_u32 s75, s75, 0
	s_add_u32 s62, s62, 0x100
	s_addc_u32 s63, s63, 0
	s_cmp_ge_i32 s76, s3
	s_mov_b32 s64, s76
	s_cbranch_scc0 .LBB0_284
	v_readlane_b32 s78, v255, 11
	v_readlane_b32 s79, v255, 13
	s_branch .LBB0_289

; #define G_STAGE(bufoff, gbase, voff) do { _Pragma("unroll") for (int _i = 0; _i < 2; ++_i) \
;         __builtin_amdgcn_global_load_lds((const unsigned*)((const char*)(gbase) + (voff)[_i]), (LAS unsigned*)(lds + (bufoff) + ldsw + _i * 8192), 16, 0, 0); } while (0)
; #define G_LDA(dst, b, h) do { _Pragma("unroll") for (int m = 0; m < 4; ++m) G_LD8(dst[m], lds + G_SA(b, h) + aoff + m * 2048); } while (0)
; #define G_LDB(dst, b, h) do { _Pragma("unroll") for (int n = 0; n < 2; ++n) G_LD8(dst[n], lds + G_SB(b, h) + boff + n * 2048); } while (0)
; #define G_WAIT_V(n) asm volatile("s_waitcnt vmcnt(" #n ")" ::: "memory")
; #define G_WAIT_L(n) asm volatile("s_waitcnt lgkmcnt(" #n ")" ::: "memory")
; #define G_BAR __builtin_amdgcn_s_barrier()
; #define G_SCHED __builtin_amdgcn_sched_barrier(0)
;     __device__ __forceinline__ unsigned row_off(const Unit& u, int r, LAS unsigned char* lds) const { return (unsigned)((const LAS int*)(lds + LDS_STAGE + u.q * 4096))[r] * (unsigned)rowbytes; }
;     ...
;             const char* a11 = cur.a1 + (size_t)(t + 1) * kstep;
;             const char* a02 = last ? nxt.a0 : cur.a0 + (size_t)(t + 2) * kstep; const char* a12 = last ? nxt.a1 : cur.a1 + (size_t)(t + 2) * kstep;
;             const char* b02 = last ? nxt.b0 : cur.b0 + (size_t)(t + 2) * kstep; const char* b12 = last ? nxt.b1 : cur.b1 + (size_t)(t + 2) * kstep;
;             G_LDB(B0, 0, 0); G_LDB(B1, 0, 1); G_SCHED; G_LDA(At, 0, 0); G_STAGE(G_SA(1, 1), a11, vA1);
;             if constexpr (GATHER) { if (last) { int tz = tid; asm volatile("" : "+v"(tz));
; #pragma unroll
;                 for (int i = 0; i < 2; ++i) { int R, C; stage_rc(tz * 16 + i * 8192, R, C); gc0[i] = S.row_off(nxt, R, lds) + (unsigned)C * 2u; gc1[i] = S.row_off(nxt, 128 + R, lds) + (unsigned)C * 2u; } } }
;             G_WAIT_L(0); G_BAR; G_MMA(0, 0, At, B0); G_MMA(0, 1, At, B1); G_WAIT_V(8); G_BAR; G_SCHED;
;             G_LDA(At, 0, 1); G_STAGE(G_SB(0, 0), b02, voffB); G_STAGE(G_SB(0, 1), b12, voffB); G_STAGE(G_SA(0, 0), a02, vA0);
.LBB0_522:
	s_add_i32 s79, s56, 2
	s_add_u32 s80, s54, 0x80
	s_addc_u32 s57, s55, 0
	s_add_i32 s82, s72, s20
	s_add_i32 m0, s27, 0xc000
	s_add_i32 s81, s27, 0xe000
	s_add_i32 s83, s82, 0x2000
	s_cmp_eq_u32 s71, s56
	s_cselect_b32 s56, s48, s80
	s_cselect_b32 s59, s51, s78
	s_cselect_b32 s58, s50, s77
	s_cselect_b32 s61, s45, s63
	s_cselect_b32 s60, s44, s62
	s_cselect_b32 s57, s49, s57
	global_load_lds_dwordx4 v240, s[54:55]
	s_mov_b32 m0, s81
	s_nop 0
	global_load_lds_dwordx4 v242, s[54:55]
	ds_read_b128 v[142:145], v138
	ds_read_b128 v[146:149], v138 offset:1024
	ds_read_b128 v[150:153], v138 offset:2048
	ds_read_b128 v[154:157], v138 offset:3072
	ds_read_b128 v[158:161], v139
	ds_read_b128 v[162:165], v139 offset:1024
	ds_read_b128 v[166:169], v139 offset:2048
	ds_read_b128 v[170:173], v139 offset:3072
	ds_read_b128 v[174:177], v140
	ds_read_b128 v[178:181], v140 offset:1024
	ds_read_b128 v[182:185], v140 offset:2048
	ds_read_b128 v[186:189], v140 offset:3072
	ds_read_b128 v[190:193], v140 offset:4096
	ds_read_b128 v[194:197], v140 offset:5120
	ds_read_b128 v[198:201], v140 offset:6144
	ds_read_b128 v[202:205], v140 offset:7168
	s_waitcnt lgkmcnt(0)
	v_mov_b32_e32 v131, v129
	s_barrier
	s_setprio 1
	s_waitcnt lgkmcnt(0)
	v_mfma_f32_16x16x32_bf16 v[124:127], v[142:145], v[174:177], v[124:127]
	v_mfma_f32_16x16x32_bf16 v[120:123], v[150:153], v[174:177], v[120:123]
	v_mfma_f32_16x16x32_bf16 v[92:95], v[142:145], v[182:185], v[92:95]
	v_mfma_f32_16x16x32_bf16 v[88:91], v[150:153], v[182:185], v[88:91]
	v_mfma_f32_16x16x32_bf16 v[60:63], v[142:145], v[190:193], v[60:63]
	v_mfma_f32_16x16x32_bf16 v[56:59], v[150:153], v[190:193], v[56:59]
	v_mfma_f32_16x16x32_bf16 v[28:31], v[142:145], v[198:201], v[28:31]
	v_mfma_f32_16x16x32_bf16 v[24:27], v[150:153], v[198:201], v[24:27]
	v_mfma_f32_16x16x32_bf16 v[124:127], v[146:149], v[178:181], v[124:127]
	v_mfma_f32_16x16x32_bf16 v[120:123], v[154:157], v[178:181], v[120:123]
	v_mfma_f32_16x16x32_bf16 v[92:95], v[146:149], v[186:189], v[92:95]
	v_mfma_f32_16x16x32_bf16 v[88:91], v[154:157], v[186:189], v[88:91]
	v_mfma_f32_16x16x32_bf16 v[60:63], v[146:149], v[194:197], v[60:63]
	v_mfma_f32_16x16x32_bf16 v[56:59], v[154:157], v[194:197], v[56:59]
	v_mfma_f32_16x16x32_bf16 v[28:31], v[146:149], v[202:205], v[28:31]
	v_mfma_f32_16x16x32_bf16 v[24:27], v[154:157], v[202:205], v[24:27]
	v_mfma_f32_16x16x32_bf16 v[112:115], v[158:161], v[174:177], v[112:115]
	v_mfma_f32_16x16x32_bf16 v[104:107], v[166:169], v[174:177], v[104:107]
	v_mfma_f32_16x16x32_bf16 v[80:83], v[158:161], v[182:185], v[80:83]
	v_mfma_f32_16x16x32_bf16 v[72:75], v[166:169], v[182:185], v[72:75]
	v_mfma_f32_16x16x32_bf16 v[48:51], v[158:161], v[190:193], v[48:51]
	v_mfma_f32_16x16x32_bf16 v[40:43], v[166:169], v[190:193], v[40:43]
	v_mfma_f32_16x16x32_bf16 v[16:19], v[158:161], v[198:201], v[16:19]
	v_mfma_f32_16x16x32_bf16 v[8:11], v[166:169], v[198:201], v[8:11]
	v_mfma_f32_16x16x32_bf16 v[112:115], v[162:165], v[178:181], v[112:115]
	v_mfma_f32_16x16x32_bf16 v[104:107], v[170:173], v[178:181], v[104:107]
	v_mfma_f32_16x16x32_bf16 v[80:83], v[162:165], v[186:189], v[80:83]
	v_mfma_f32_16x16x32_bf16 v[72:75], v[170:173], v[186:189], v[72:75]
	v_mfma_f32_16x16x32_bf16 v[48:51], v[162:165], v[194:197], v[48:51]
	v_mfma_f32_16x16x32_bf16 v[40:43], v[170:173], v[194:197], v[40:43]
	v_mfma_f32_16x16x32_bf16 v[16:19], v[162:165], v[202:205], v[16:19]
	v_mfma_f32_16x16x32_bf16 v[8:11], v[170:173], v[202:205], v[8:11]
	s_setprio 0
	s_waitcnt vmcnt(8)
	s_barrier
	s_mov_b32 m0, s82
	v_mov_b32_e32 v133, v129
	global_load_lds_dwordx4 v244, s[60:61]
	v_mov_b32_e32 v207, v129
	s_mov_b32 m0, s83
	v_lshl_add_u64 v[208:209], s[60:61], 0, v[244:245]
	v_lshl_add_u64 v[210:211], s[60:61], 0, v[246:247]
	global_load_lds_dwordx4 v246, s[60:61]
	s_cselect_b32 s61, s47, s75
	s_cselect_b32 s60, s46, s64
	s_add_i32 s80, s73, s20
	s_mov_b32 m0, s80
	v_lshl_add_u64 v[212:213], s[60:61], 0, v[244:245]
	global_load_lds_dwordx4 v244, s[60:61]
	s_add_i32 m0, s80, 0x2000
	v_lshl_add_u64 v[214:215], s[60:61], 0, v[246:247]
	global_load_lds_dwordx4 v246, s[60:61]
	s_mov_b32 m0, s27
	v_lshl_add_u64 v[206:207], s[58:59], 0, v[240:241]
	global_load_lds_dwordx4 v240, s[58:59]
	s_mov_b32 m0, s33
	v_lshl_add_u64 v[216:217], s[58:59], 0, v[242:243]
	global_load_lds_dwordx4 v242, s[58:59]
	ds_read_b128 v[174:177], v140 offset:16384
	ds_read_b128 v[178:181], v140 offset:17408
	ds_read_b128 v[182:185], v140 offset:18432
	ds_read_b128 v[186:189], v140 offset:19456
	ds_read_b128 v[190:193], v140 offset:20480
	ds_read_b128 v[194:197], v140 offset:21504
	ds_read_b128 v[198:201], v140 offset:22528
	ds_read_b128 v[202:205], v140 offset:23552
	s_waitcnt lgkmcnt(0)
	s_barrier
; #define G_STAGE(bufoff, gbase, voff) do { _Pragma("unroll") for (int _i = 0; _i < 2; ++_i) \
;         __builtin_amdgcn_global_load_lds((const unsigned*)((const char*)(gbase) + (voff)[_i]), (LAS unsigned*)(lds + (bufoff) + ldsw + _i * 8192), 16, 0, 0); } while (0)
; #define G_LDA(dst, b, h) do { _Pragma("unroll") for (int m = 0; m < 4; ++m) G_LD8(dst[m], lds + G_SA(b, h) + aoff + m * 2048); } while (0)
; #define G_LDB(dst, b, h) do { _Pragma("unroll") for (int n = 0; n < 2; ++n) G_LD8(dst[n], lds + G_SB(b, h) + boff + n * 2048); } while (0)
; #define G_WAIT_V(n) asm volatile("s_waitcnt vmcnt(" #n ")" ::: "memory")
; #define G_WAIT_L(n) asm volatile("s_waitcnt lgkmcnt(" #n ")" ::: "memory")
; #define G_BAR __builtin_amdgcn_s_barrier()
; #define G_SCHED __builtin_amdgcn_sched_barrier(0)
;     ...
;             G_WAIT_L(0); G_BAR; G_MMA(1, 0, At, B0); G_MMA(1, 1, At, B1); G_WAIT_V(8); G_BAR; G_SCHED;
;             G_LDB(B0, 1, 0); G_LDB(B1, 1, 1); G_SCHED; G_LDA(At, 1, 0); G_STAGE(G_SA(0, 1), a12, vA1);
;             G_WAIT_L(0); G_BAR; G_MMA(0, 0, At, B0); G_MMA(0, 1, At, B1); G_WAIT_V(8); G_BAR; G_SCHED;
	s_setprio 1
	s_waitcnt lgkmcnt(0)
	v_mfma_f32_16x16x32_bf16 v[116:119], v[142:145], v[174:177], v[116:119]
	v_mfma_f32_16x16x32_bf16 v[108:111], v[150:153], v[174:177], v[108:111]
	v_mfma_f32_16x16x32_bf16 v[84:87], v[142:145], v[182:185], v[84:87]
	v_mfma_f32_16x16x32_bf16 v[76:79], v[150:153], v[182:185], v[76:79]
	v_mfma_f32_16x16x32_bf16 v[52:55], v[142:145], v[190:193], v[52:55]
	v_mfma_f32_16x16x32_bf16 v[44:47], v[150:153], v[190:193], v[44:47]
	v_mfma_f32_16x16x32_bf16 v[20:23], v[142:145], v[198:201], v[20:23]
	v_mfma_f32_16x16x32_bf16 v[12:15], v[150:153], v[198:201], v[12:15]
	v_mfma_f32_16x16x32_bf16 v[116:119], v[146:149], v[178:181], v[116:119]
	v_mfma_f32_16x16x32_bf16 v[108:111], v[154:157], v[178:181], v[108:111]
	v_mfma_f32_16x16x32_bf16 v[84:87], v[146:149], v[186:189], v[84:87]
	v_mfma_f32_16x16x32_bf16 v[76:79], v[154:157], v[186:189], v[76:79]
	v_mfma_f32_16x16x32_bf16 v[52:55], v[146:149], v[194:197], v[52:55]
	v_mfma_f32_16x16x32_bf16 v[44:47], v[154:157], v[194:197], v[44:47]
	v_mfma_f32_16x16x32_bf16 v[20:23], v[146:149], v[202:205], v[20:23]
	v_mfma_f32_16x16x32_bf16 v[12:15], v[154:157], v[202:205], v[12:15]
	v_mfma_f32_16x16x32_bf16 v[100:103], v[158:161], v[174:177], v[100:103]
	v_mfma_f32_16x16x32_bf16 v[96:99], v[166:169], v[174:177], v[96:99]
	v_mfma_f32_16x16x32_bf16 v[68:71], v[158:161], v[182:185], v[68:71]
	v_mfma_f32_16x16x32_bf16 v[64:67], v[166:169], v[182:185], v[64:67]
	v_mfma_f32_16x16x32_bf16 v[36:39], v[158:161], v[190:193], v[36:39]
	v_mfma_f32_16x16x32_bf16 v[32:35], v[166:169], v[190:193], v[32:35]
	v_mfma_f32_16x16x32_bf16 v[4:7], v[158:161], v[198:201], v[4:7]
	v_mfma_f32_16x16x32_bf16 v[0:3], v[166:169], v[198:201], v[0:3]
	v_mfma_f32_16x16x32_bf16 v[100:103], v[162:165], v[178:181], v[100:103]
	v_mfma_f32_16x16x32_bf16 v[96:99], v[170:173], v[178:181], v[96:99]
	v_mfma_f32_16x16x32_bf16 v[68:71], v[162:165], v[186:189], v[68:71]
	v_mfma_f32_16x16x32_bf16 v[64:67], v[170:173], v[186:189], v[64:67]
	v_mfma_f32_16x16x32_bf16 v[36:39], v[162:165], v[194:197], v[36:39]
	v_mfma_f32_16x16x32_bf16 v[32:35], v[170:173], v[194:197], v[32:35]
	v_mfma_f32_16x16x32_bf16 v[4:7], v[162:165], v[202:205], v[4:7]
	v_mfma_f32_16x16x32_bf16 v[0:3], v[170:173], v[202:205], v[0:3]
	s_setprio 0
	s_waitcnt vmcnt(8)
	s_barrier
	s_add_i32 s58, 0, 0x18000
	s_add_i32 s59, 0, 0x1c000
	s_mov_b32 m0, s66
	s_nop 0
	global_load_lds_dwordx4 v240, s[56:57]
	s_mov_b32 m0, s67
	s_nop 0
	global_load_lds_dwordx4 v242, s[56:57]
	v_add_u32_e32 v131, s58, v137
	ds_read_b128 v[142:145], v131
	ds_read_b128 v[146:149], v131 offset:1024
	ds_read_b128 v[150:153], v131 offset:2048
	ds_read_b128 v[154:157], v131 offset:3072
	v_add_u32_e32 v131, s59, v137
	ds_read_b128 v[158:161], v131
	ds_read_b128 v[162:165], v131 offset:1024
	ds_read_b128 v[166:169], v131 offset:2048
	ds_read_b128 v[170:173], v131 offset:3072
	ds_read_b128 v[174:177], v140 offset:32768
	ds_read_b128 v[178:181], v140 offset:33792
	ds_read_b128 v[182:185], v140 offset:34816
	ds_read_b128 v[186:189], v140 offset:35840
	ds_read_b128 v[190:193], v140 offset:36864
	ds_read_b128 v[194:197], v140 offset:37888
	ds_read_b128 v[198:201], v140 offset:38912
	ds_read_b128 v[202:205], v140 offset:39936
	s_waitcnt lgkmcnt(0)
	s_barrier
	s_setprio 1
	s_waitcnt lgkmcnt(0)
	v_mfma_f32_16x16x32_bf16 v[124:127], v[142:145], v[174:177], v[124:127]
	v_mfma_f32_16x16x32_bf16 v[120:123], v[150:153], v[174:177], v[120:123]
	v_mfma_f32_16x16x32_bf16 v[92:95], v[142:145], v[182:185], v[92:95]
	v_mfma_f32_16x16x32_bf16 v[88:91], v[150:153], v[182:185], v[88:91]
	v_mfma_f32_16x16x32_bf16 v[60:63], v[142:145], v[190:193], v[60:63]
	v_mfma_f32_16x16x32_bf16 v[56:59], v[150:153], v[190:193], v[56:59]
	v_mfma_f32_16x16x32_bf16 v[28:31], v[142:145], v[198:201], v[28:31]
	v_mfma_f32_16x16x32_bf16 v[24:27], v[150:153], v[198:201], v[24:27]
	v_mfma_f32_16x16x32_bf16 v[124:127], v[146:149], v[178:181], v[124:127]
	v_mfma_f32_16x16x32_bf16 v[120:123], v[154:157], v[178:181], v[120:123]
	v_mfma_f32_16x16x32_bf16 v[92:95], v[146:149], v[186:189], v[92:95]
	v_mfma_f32_16x16x32_bf16 v[88:91], v[154:157], v[186:189], v[88:91]
	v_mfma_f32_16x16x32_bf16 v[60:63], v[146:149], v[194:197], v[60:63]
	v_mfma_f32_16x16x32_bf16 v[56:59], v[154:157], v[194:197], v[56:59]
	v_mfma_f32_16x16x32_bf16 v[28:31], v[146:149], v[202:205], v[28:31]
	v_mfma_f32_16x16x32_bf16 v[24:27], v[154:157], v[202:205], v[24:27]
	v_mfma_f32_16x16x32_bf16 v[112:115], v[158:161], v[174:177], v[112:115]
	v_mfma_f32_16x16x32_bf16 v[104:107], v[166:169], v[174:177], v[104:107]
	v_mfma_f32_16x16x32_bf16 v[80:83], v[158:161], v[182:185], v[80:83]
	v_mfma_f32_16x16x32_bf16 v[72:75], v[166:169], v[182:185], v[72:75]
	v_mfma_f32_16x16x32_bf16 v[48:51], v[158:161], v[190:193], v[48:51]
	v_mfma_f32_16x16x32_bf16 v[40:43], v[166:169], v[190:193], v[40:43]
	v_mfma_f32_16x16x32_bf16 v[16:19], v[158:161], v[198:201], v[16:19]
	v_mfma_f32_16x16x32_bf16 v[8:11], v[166:169], v[198:201], v[8:11]
	v_mfma_f32_16x16x32_bf16 v[112:115], v[162:165], v[178:181], v[112:115]
	v_mfma_f32_16x16x32_bf16 v[104:107], v[170:173], v[178:181], v[104:107]
	v_mfma_f32_16x16x32_bf16 v[80:83], v[162:165], v[186:189], v[80:83]
	v_mfma_f32_16x16x32_bf16 v[72:75], v[170:173], v[186:189], v[72:75]
	v_mfma_f32_16x16x32_bf16 v[48:51], v[162:165], v[194:197], v[48:51]
	v_mfma_f32_16x16x32_bf16 v[40:43], v[170:173], v[194:197], v[40:43]
	v_mfma_f32_16x16x32_bf16 v[16:19], v[162:165], v[202:205], v[16:19]
	v_mfma_f32_16x16x32_bf16 v[8:11], v[170:173], v[202:205], v[8:11]
	s_setprio 0
	s_waitcnt vmcnt(8)
	s_barrier
; #define G_STAGE(bufoff, gbase, voff) do { _Pragma("unroll") for (int _i = 0; _i < 2; ++_i) \
;         __builtin_amdgcn_global_load_lds((const unsigned*)((const char*)(gbase) + (voff)[_i]), (LAS unsigned*)(lds + (bufoff) + ldsw + _i * 8192), 16, 0, 0); } while (0)
; #define G_LDA(dst, b, h) do { _Pragma("unroll") for (int m = 0; m < 4; ++m) G_LD8(dst[m], lds + G_SA(b, h) + aoff + m * 2048); } while (0)
; #define G_WAIT_V(n) asm volatile("s_waitcnt vmcnt(" #n ")" ::: "memory")
; #define G_WAIT_L(n) asm volatile("s_waitcnt lgkmcnt(" #n ")" ::: "memory")
; #define G_BAR __builtin_amdgcn_s_barrier()
; #define G_SCHED __builtin_amdgcn_sched_barrier(0)
;     ...
;             G_LDA(At, 1, 1); G_STAGE(G_SB(1, 0), b02 + kstep, voffB); G_STAGE(G_SB(1, 1), b12 + kstep, voffB); G_STAGE(G_SA(1, 0), a02 + kstep, vA0);
;             G_WAIT_L(0); G_BAR; G_MMA(1, 0, At, B0); G_MMA(1, 1, At, B1); G_WAIT_V(8); G_BAR; G_SCHED;
;         }
	s_add_i32 s56, s58, s20
	v_lshl_add_u64 v[202:203], v[208:209], 0, s[40:41]
	s_mov_b32 m0, s56
	s_nop 0
	global_load_lds_dwordx4 v[202:203], off
	v_lshl_add_u64 v[202:203], v[210:211], 0, s[40:41]
	s_add_i32 m0, s56, 0x2000
	s_add_i32 s56, s59, s20
	global_load_lds_dwordx4 v[202:203], off
	v_lshl_add_u64 v[202:203], v[212:213], 0, s[40:41]
	s_mov_b32 m0, s56
	s_nop 0
	global_load_lds_dwordx4 v[202:203], off
	v_lshl_add_u64 v[202:203], v[214:215], 0, s[40:41]
	s_add_i32 m0, s56, 0x2000
	s_nop 0
	global_load_lds_dwordx4 v[202:203], off
	v_lshl_add_u64 v[202:203], v[206:207], 0, s[40:41]
	s_mov_b32 m0, s69
	s_nop 0
	global_load_lds_dwordx4 v[202:203], off
	v_lshl_add_u64 v[202:203], v[216:217], 0, s[40:41]
	s_mov_b32 m0, s70
	s_nop 0
	global_load_lds_dwordx4 v[202:203], off
	ds_read_b128 v[130:133], v140 offset:49152
	ds_read_b128 v[174:177], v140 offset:50176
	ds_read_b128 v[178:181], v140 offset:51200
	ds_read_b128 v[182:185], v140 offset:52224
	ds_read_b128 v[186:189], v140 offset:53248
	ds_read_b128 v[190:193], v140 offset:54272
	ds_read_b128 v[194:197], v140 offset:55296
	ds_read_b128 v[198:201], v140 offset:56320
	s_waitcnt lgkmcnt(0)
	s_barrier
	s_setprio 1
	s_waitcnt lgkmcnt(0)
	v_mfma_f32_16x16x32_bf16 v[116:119], v[142:145], v[130:133], v[116:119]
	v_mfma_f32_16x16x32_bf16 v[108:111], v[150:153], v[130:133], v[108:111]
	v_mfma_f32_16x16x32_bf16 v[84:87], v[142:145], v[178:181], v[84:87]
	v_mfma_f32_16x16x32_bf16 v[76:79], v[150:153], v[178:181], v[76:79]
	v_mfma_f32_16x16x32_bf16 v[52:55], v[142:145], v[186:189], v[52:55]
	v_mfma_f32_16x16x32_bf16 v[44:47], v[150:153], v[186:189], v[44:47]
	v_mfma_f32_16x16x32_bf16 v[20:23], v[142:145], v[194:197], v[20:23]
	v_mfma_f32_16x16x32_bf16 v[12:15], v[150:153], v[194:197], v[12:15]
	v_mfma_f32_16x16x32_bf16 v[116:119], v[146:149], v[174:177], v[116:119]
	v_mfma_f32_16x16x32_bf16 v[108:111], v[154:157], v[174:177], v[108:111]
	v_mfma_f32_16x16x32_bf16 v[84:87], v[146:149], v[182:185], v[84:87]
	v_mfma_f32_16x16x32_bf16 v[76:79], v[154:157], v[182:185], v[76:79]
	v_mfma_f32_16x16x32_bf16 v[52:55], v[146:149], v[190:193], v[52:55]
	v_mfma_f32_16x16x32_bf16 v[44:47], v[154:157], v[190:193], v[44:47]
	v_mfma_f32_16x16x32_bf16 v[20:23], v[146:149], v[198:201], v[20:23]
	v_mfma_f32_16x16x32_bf16 v[12:15], v[154:157], v[198:201], v[12:15]
	v_mfma_f32_16x16x32_bf16 v[100:103], v[158:161], v[130:133], v[100:103]
	v_mfma_f32_16x16x32_bf16 v[96:99], v[166:169], v[130:133], v[96:99]
	v_mfma_f32_16x16x32_bf16 v[68:71], v[158:161], v[178:181], v[68:71]
	v_mfma_f32_16x16x32_bf16 v[64:67], v[166:169], v[178:181], v[64:67]
	v_mfma_f32_16x16x32_bf16 v[36:39], v[158:161], v[186:189], v[36:39]
	v_mfma_f32_16x16x32_bf16 v[32:35], v[166:169], v[186:189], v[32:35]
	v_mfma_f32_16x16x32_bf16 v[4:7], v[158:161], v[194:197], v[4:7]
	v_mfma_f32_16x16x32_bf16 v[0:3], v[166:169], v[194:197], v[0:3]
	v_mfma_f32_16x16x32_bf16 v[100:103], v[162:165], v[174:177], v[100:103]
	v_mfma_f32_16x16x32_bf16 v[96:99], v[170:173], v[174:177], v[96:99]
	v_mfma_f32_16x16x32_bf16 v[68:71], v[162:165], v[182:185], v[68:71]
	v_mfma_f32_16x16x32_bf16 v[64:67], v[170:173], v[182:185], v[64:67]
	v_mfma_f32_16x16x32_bf16 v[36:39], v[162:165], v[190:193], v[36:39]
	v_mfma_f32_16x16x32_bf16 v[32:35], v[170:173], v[190:193], v[32:35]
	v_mfma_f32_16x16x32_bf16 v[4:7], v[162:165], v[198:201], v[4:7]
	v_mfma_f32_16x16x32_bf16 v[0:3], v[170:173], v[198:201], v[0:3]
	s_setprio 0
	s_waitcnt vmcnt(8)
	s_barrier
	s_add_u32 s62, s62, 0x100
	s_addc_u32 s63, s63, 0
	s_add_u32 s64, s64, 0x100
	s_addc_u32 s75, s75, 0
	s_add_u32 s77, s77, 0x100
	s_addc_u32 s78, s78, 0
	s_add_u32 s54, s54, 0x100
	s_addc_u32 s55, s55, 0
	s_cmp_ge_i32 s79, s0
	s_mov_b32 s56, s79
	s_cbranch_scc0 .LBB0_522
	v_readlane_b32 s78, v255, 11
	v_readlane_b32 s79, v255, 13
	s_and_b64 vcc, exec, s[42:43]
	s_cbranch_vccz .LBB0_525

; #define G_STAGE(bufoff, gbase, voff) do { _Pragma("unroll") for (int _i = 0; _i < 2; ++_i) \
;         __builtin_amdgcn_global_load_lds((const unsigned*)((const char*)(gbase) + (voff)[_i]), (LAS unsigned*)(lds + (bufoff) + ldsw + _i * 8192), 16, 0, 0); } while (0)
; #define G_LDA(dst, b, h) do { _Pragma("unroll") for (int m = 0; m < 4; ++m) G_LD8(dst[m], lds + G_SA(b, h) + aoff + m * 2048); } while (0)
; #define G_LDB(dst, b, h) do { _Pragma("unroll") for (int n = 0; n < 2; ++n) G_LD8(dst[n], lds + G_SB(b, h) + boff + n * 2048); } while (0)
; #define G_WAIT_V(n) asm volatile("s_waitcnt vmcnt(" #n ")" ::: "memory")
; #define G_WAIT_L(n) asm volatile("s_waitcnt lgkmcnt(" #n ")" ::: "memory")
; #define G_BAR __builtin_amdgcn_s_barrier()
; #define G_SCHED __builtin_amdgcn_sched_barrier(0)
;     __device__ __forceinline__ unsigned row_off(const Unit& u, int r, LAS unsigned char* lds) const { return (unsigned)((const LAS int*)(lds + LDS_STAGE + u.q * 4096))[r] * (unsigned)rowbytes; }
;     ...
;             const char* a11 = cur.a1 + (size_t)(t + 1) * kstep;
;             const char* a02 = last ? nxt.a0 : cur.a0 + (size_t)(t + 2) * kstep; const char* a12 = last ? nxt.a1 : cur.a1 + (size_t)(t + 2) * kstep;
;             const char* b02 = last ? nxt.b0 : cur.b0 + (size_t)(t + 2) * kstep; const char* b12 = last ? nxt.b1 : cur.b1 + (size_t)(t + 2) * kstep;
;             G_LDB(B0, 0, 0); G_LDB(B1, 0, 1); G_SCHED; G_LDA(At, 0, 0); G_STAGE(G_SA(1, 1), a11, vA1);
;             if constexpr (GATHER) { if (last) { int tz = tid; asm volatile("" : "+v"(tz));
; #pragma unroll
;                 for (int i = 0; i < 2; ++i) { int R, C; stage_rc(tz * 16 + i * 8192, R, C); gc0[i] = S.row_off(nxt, R, lds) + (unsigned)C * 2u; gc1[i] = S.row_off(nxt, 128 + R, lds) + (unsigned)C * 2u; } } }
;             G_WAIT_L(0); G_BAR; G_MMA(0, 0, At, B0); G_MMA(0, 1, At, B1); G_WAIT_V(8); G_BAR; G_SCHED;
;             G_LDA(At, 0, 1); G_STAGE(G_SB(0, 0), b02, voffB); G_STAGE(G_SB(0, 1), b12, voffB); G_STAGE(G_SA(0, 0), a02, vA0);
.LBB0_549:
	s_add_i32 s80, s58, 2
	s_add_u32 s81, s56, 0x80
	s_addc_u32 s59, s57, 0
	s_add_i32 s83, s75, s20
	s_add_i32 m0, s67, 0xc000
	s_add_i32 s82, s67, 0xe000
	s_add_i32 s84, s83, 0x2000
	s_cmp_eq_u32 s74, s58
	s_cselect_b32 s58, s44, s81
	s_cselect_b32 s61, s43, s79
	s_cselect_b32 s60, s42, s65
	s_cselect_b32 s63, s47, s53
	s_cselect_b32 s62, s46, s41
	s_cselect_b32 s59, s45, s59
	global_load_lds_dwordx4 v240, s[56:57]
	s_mov_b32 m0, s82
	v_mov_b32_e32 v205, v129
	global_load_lds_dwordx4 v242, s[56:57]
	ds_read_b128 v[130:133], v138
	ds_read_b128 v[142:145], v138 offset:1024
	ds_read_b128 v[146:149], v138 offset:2048
	ds_read_b128 v[150:153], v138 offset:3072
	ds_read_b128 v[154:157], v139
	ds_read_b128 v[158:161], v139 offset:1024
	ds_read_b128 v[162:165], v139 offset:2048
	ds_read_b128 v[166:169], v139 offset:3072
	ds_read_b128 v[170:173], v140
	ds_read_b128 v[174:177], v140 offset:1024
	ds_read_b128 v[178:181], v140 offset:2048
	ds_read_b128 v[182:185], v140 offset:3072
	ds_read_b128 v[186:189], v140 offset:4096
	ds_read_b128 v[190:193], v140 offset:5120
	ds_read_b128 v[194:197], v140 offset:6144
	ds_read_b128 v[198:201], v140 offset:7168
	s_waitcnt lgkmcnt(0)
	s_barrier
	s_setprio 1
	s_waitcnt lgkmcnt(0)
	v_mfma_f32_16x16x32_bf16 v[124:127], v[130:133], v[170:173], v[124:127]
	v_mfma_f32_16x16x32_bf16 v[120:123], v[146:149], v[170:173], v[120:123]
	v_mfma_f32_16x16x32_bf16 v[108:111], v[130:133], v[178:181], v[108:111]
	v_mfma_f32_16x16x32_bf16 v[104:107], v[146:149], v[178:181], v[104:107]
	v_mfma_f32_16x16x32_bf16 v[92:95], v[130:133], v[186:189], v[92:95]
	v_mfma_f32_16x16x32_bf16 v[88:91], v[146:149], v[186:189], v[88:91]
	v_mfma_f32_16x16x32_bf16 v[76:79], v[130:133], v[194:197], v[76:79]
	v_mfma_f32_16x16x32_bf16 v[72:75], v[146:149], v[194:197], v[72:75]
	v_mfma_f32_16x16x32_bf16 v[124:127], v[142:145], v[174:177], v[124:127]
	v_mfma_f32_16x16x32_bf16 v[120:123], v[150:153], v[174:177], v[120:123]
	v_mfma_f32_16x16x32_bf16 v[108:111], v[142:145], v[182:185], v[108:111]
	v_mfma_f32_16x16x32_bf16 v[104:107], v[150:153], v[182:185], v[104:107]
	v_mfma_f32_16x16x32_bf16 v[92:95], v[142:145], v[190:193], v[92:95]
	v_mfma_f32_16x16x32_bf16 v[88:91], v[150:153], v[190:193], v[88:91]
	v_mfma_f32_16x16x32_bf16 v[76:79], v[142:145], v[198:201], v[76:79]
	v_mfma_f32_16x16x32_bf16 v[72:75], v[150:153], v[198:201], v[72:75]
	v_mfma_f32_16x16x32_bf16 v[116:119], v[154:157], v[170:173], v[116:119]
	v_mfma_f32_16x16x32_bf16 v[112:115], v[162:165], v[170:173], v[112:115]
	v_mfma_f32_16x16x32_bf16 v[100:103], v[154:157], v[178:181], v[100:103]
	v_mfma_f32_16x16x32_bf16 v[96:99], v[162:165], v[178:181], v[96:99]
	v_mfma_f32_16x16x32_bf16 v[84:87], v[154:157], v[186:189], v[84:87]
	v_mfma_f32_16x16x32_bf16 v[80:83], v[162:165], v[186:189], v[80:83]
	v_mfma_f32_16x16x32_bf16 v[68:71], v[154:157], v[194:197], v[68:71]
	v_mfma_f32_16x16x32_bf16 v[64:67], v[162:165], v[194:197], v[64:67]
	v_mfma_f32_16x16x32_bf16 v[116:119], v[158:161], v[174:177], v[116:119]
	v_mfma_f32_16x16x32_bf16 v[112:115], v[166:169], v[174:177], v[112:115]
	v_mfma_f32_16x16x32_bf16 v[100:103], v[158:161], v[182:185], v[100:103]
	v_mfma_f32_16x16x32_bf16 v[96:99], v[166:169], v[182:185], v[96:99]
	v_mfma_f32_16x16x32_bf16 v[84:87], v[158:161], v[190:193], v[84:87]
	v_mfma_f32_16x16x32_bf16 v[80:83], v[166:169], v[190:193], v[80:83]
	v_mfma_f32_16x16x32_bf16 v[68:71], v[158:161], v[198:201], v[68:71]
	v_mfma_f32_16x16x32_bf16 v[64:67], v[166:169], v[198:201], v[64:67]
	s_setprio 0
	s_waitcnt vmcnt(8)
	s_barrier
	s_mov_b32 m0, s83
	s_nop 0
	global_load_lds_dwordx4 v244, s[62:63]
	s_mov_b32 m0, s84
	s_cselect_b32 s83, s49, s64
	s_cselect_b32 s82, s48, s55
	s_add_i32 s81, s76, s20
	global_load_lds_dwordx4 v246, s[62:63]
	s_mov_b32 m0, s81
	v_mov_b32_e32 v203, v129
	global_load_lds_dwordx4 v244, s[82:83]
	s_add_i32 m0, s81, 0x2000
	v_mov_b32_e32 v207, v129
	global_load_lds_dwordx4 v246, s[82:83]
	s_mov_b32 m0, s67
	v_lshl_add_u64 v[208:209], s[62:63], 0, v[244:245]
	global_load_lds_dwordx4 v240, s[60:61]
	s_mov_b32 m0, s68
	v_lshl_add_u64 v[210:211], s[62:63], 0, v[246:247]
	global_load_lds_dwordx4 v242, s[60:61]
	ds_read_b128 v[170:173], v140 offset:16384
	ds_read_b128 v[174:177], v140 offset:17408
	ds_read_b128 v[178:181], v140 offset:18432
	ds_read_b128 v[182:185], v140 offset:19456
	ds_read_b128 v[186:189], v140 offset:20480
	ds_read_b128 v[190:193], v140 offset:21504
	ds_read_b128 v[194:197], v140 offset:22528
	ds_read_b128 v[198:201], v140 offset:23552
	s_waitcnt lgkmcnt(0)
	v_lshl_add_u64 v[202:203], s[82:83], 0, v[244:245]
	v_lshl_add_u64 v[206:207], s[82:83], 0, v[246:247]
	v_lshl_add_u64 v[212:213], s[60:61], 0, v[240:241]
	v_lshl_add_u64 v[214:215], s[60:61], 0, v[242:243]
	s_barrier
; #define G_STAGE(bufoff, gbase, voff) do { _Pragma("unroll") for (int _i = 0; _i < 2; ++_i) \
;         __builtin_amdgcn_global_load_lds((const unsigned*)((const char*)(gbase) + (voff)[_i]), (LAS unsigned*)(lds + (bufoff) + ldsw + _i * 8192), 16, 0, 0); } while (0)
; #define G_LDA(dst, b, h) do { _Pragma("unroll") for (int m = 0; m < 4; ++m) G_LD8(dst[m], lds + G_SA(b, h) + aoff + m * 2048); } while (0)
; #define G_LDB(dst, b, h) do { _Pragma("unroll") for (int n = 0; n < 2; ++n) G_LD8(dst[n], lds + G_SB(b, h) + boff + n * 2048); } while (0)
; #define G_WAIT_V(n) asm volatile("s_waitcnt vmcnt(" #n ")" ::: "memory")
; #define G_WAIT_L(n) asm volatile("s_waitcnt lgkmcnt(" #n ")" ::: "memory")
; #define G_BAR __builtin_amdgcn_s_barrier()
; #define G_SCHED __builtin_amdgcn_sched_barrier(0)
;     ...
;             G_WAIT_L(0); G_BAR; G_MMA(1, 0, At, B0); G_MMA(1, 1, At, B1); G_WAIT_V(8); G_BAR; G_SCHED;
;             G_LDB(B0, 1, 0); G_LDB(B1, 1, 1); G_SCHED; G_LDA(At, 1, 0); G_STAGE(G_SA(0, 1), a12, vA1);
;             G_WAIT_L(0); G_BAR; G_MMA(0, 0, At, B0); G_MMA(0, 1, At, B1); G_WAIT_V(8); G_BAR; G_SCHED;
	s_setprio 1
	s_waitcnt lgkmcnt(0)
	v_mfma_f32_16x16x32_bf16 v[60:63], v[130:133], v[170:173], v[60:63]
	v_mfma_f32_16x16x32_bf16 v[56:59], v[146:149], v[170:173], v[56:59]
	v_mfma_f32_16x16x32_bf16 v[44:47], v[130:133], v[178:181], v[44:47]
	v_mfma_f32_16x16x32_bf16 v[40:43], v[146:149], v[178:181], v[40:43]
	v_mfma_f32_16x16x32_bf16 v[28:31], v[130:133], v[186:189], v[28:31]
	v_mfma_f32_16x16x32_bf16 v[24:27], v[146:149], v[186:189], v[24:27]
	v_mfma_f32_16x16x32_bf16 v[12:15], v[130:133], v[194:197], v[12:15]
	v_mfma_f32_16x16x32_bf16 v[8:11], v[146:149], v[194:197], v[8:11]
	v_mfma_f32_16x16x32_bf16 v[60:63], v[142:145], v[174:177], v[60:63]
	v_mfma_f32_16x16x32_bf16 v[56:59], v[150:153], v[174:177], v[56:59]
	v_mfma_f32_16x16x32_bf16 v[44:47], v[142:145], v[182:185], v[44:47]
	v_mfma_f32_16x16x32_bf16 v[40:43], v[150:153], v[182:185], v[40:43]
	v_mfma_f32_16x16x32_bf16 v[28:31], v[142:145], v[190:193], v[28:31]
	v_mfma_f32_16x16x32_bf16 v[24:27], v[150:153], v[190:193], v[24:27]
	v_mfma_f32_16x16x32_bf16 v[12:15], v[142:145], v[198:201], v[12:15]
	v_mfma_f32_16x16x32_bf16 v[8:11], v[150:153], v[198:201], v[8:11]
	v_mfma_f32_16x16x32_bf16 v[52:55], v[154:157], v[170:173], v[52:55]
	v_mfma_f32_16x16x32_bf16 v[48:51], v[162:165], v[170:173], v[48:51]
	v_mfma_f32_16x16x32_bf16 v[36:39], v[154:157], v[178:181], v[36:39]
	v_mfma_f32_16x16x32_bf16 v[32:35], v[162:165], v[178:181], v[32:35]
	v_mfma_f32_16x16x32_bf16 v[20:23], v[154:157], v[186:189], v[20:23]
	v_mfma_f32_16x16x32_bf16 v[16:19], v[162:165], v[186:189], v[16:19]
	v_mfma_f32_16x16x32_bf16 v[4:7], v[154:157], v[194:197], v[4:7]
	v_mfma_f32_16x16x32_bf16 v[0:3], v[162:165], v[194:197], v[0:3]
	v_mfma_f32_16x16x32_bf16 v[52:55], v[158:161], v[174:177], v[52:55]
	v_mfma_f32_16x16x32_bf16 v[48:51], v[166:169], v[174:177], v[48:51]
	v_mfma_f32_16x16x32_bf16 v[36:39], v[158:161], v[182:185], v[36:39]
	v_mfma_f32_16x16x32_bf16 v[32:35], v[166:169], v[182:185], v[32:35]
	v_mfma_f32_16x16x32_bf16 v[20:23], v[158:161], v[190:193], v[20:23]
	v_mfma_f32_16x16x32_bf16 v[16:19], v[166:169], v[190:193], v[16:19]
	v_mfma_f32_16x16x32_bf16 v[4:7], v[158:161], v[198:201], v[4:7]
	v_mfma_f32_16x16x32_bf16 v[0:3], v[166:169], v[198:201], v[0:3]
	s_setprio 0
	s_waitcnt vmcnt(8)
	s_barrier
	s_add_i32 s60, 0, 0x18000
	s_add_i32 s61, 0, 0x1c000
	s_mov_b32 m0, s69
	s_nop 0
	global_load_lds_dwordx4 v240, s[58:59]
	s_mov_b32 m0, s70
	s_nop 0
	global_load_lds_dwordx4 v242, s[58:59]
	v_add_u32_e32 v141, s60, v137
	ds_read_b128 v[130:133], v141
	ds_read_b128 v[142:145], v141 offset:1024
	ds_read_b128 v[146:149], v141 offset:2048
	ds_read_b128 v[150:153], v141 offset:3072
	v_add_u32_e32 v141, s61, v137
	ds_read_b128 v[154:157], v141
	ds_read_b128 v[158:161], v141 offset:1024
	ds_read_b128 v[162:165], v141 offset:2048
	ds_read_b128 v[166:169], v141 offset:3072
	ds_read_b128 v[170:173], v140 offset:32768
	ds_read_b128 v[174:177], v140 offset:33792
	ds_read_b128 v[178:181], v140 offset:34816
	ds_read_b128 v[182:185], v140 offset:35840
	ds_read_b128 v[186:189], v140 offset:36864
	ds_read_b128 v[190:193], v140 offset:37888
	ds_read_b128 v[194:197], v140 offset:38912
	ds_read_b128 v[198:201], v140 offset:39936
	s_waitcnt lgkmcnt(0)
	s_barrier
	s_setprio 1
	s_waitcnt lgkmcnt(0)
	v_mfma_f32_16x16x32_bf16 v[124:127], v[130:133], v[170:173], v[124:127]
	v_mfma_f32_16x16x32_bf16 v[120:123], v[146:149], v[170:173], v[120:123]
	v_mfma_f32_16x16x32_bf16 v[108:111], v[130:133], v[178:181], v[108:111]
	v_mfma_f32_16x16x32_bf16 v[104:107], v[146:149], v[178:181], v[104:107]
	v_mfma_f32_16x16x32_bf16 v[92:95], v[130:133], v[186:189], v[92:95]
	v_mfma_f32_16x16x32_bf16 v[88:91], v[146:149], v[186:189], v[88:91]
	v_mfma_f32_16x16x32_bf16 v[76:79], v[130:133], v[194:197], v[76:79]
	v_mfma_f32_16x16x32_bf16 v[72:75], v[146:149], v[194:197], v[72:75]
	v_mfma_f32_16x16x32_bf16 v[124:127], v[142:145], v[174:177], v[124:127]
	v_mfma_f32_16x16x32_bf16 v[120:123], v[150:153], v[174:177], v[120:123]
	v_mfma_f32_16x16x32_bf16 v[108:111], v[142:145], v[182:185], v[108:111]
	v_mfma_f32_16x16x32_bf16 v[104:107], v[150:153], v[182:185], v[104:107]
	v_mfma_f32_16x16x32_bf16 v[92:95], v[142:145], v[190:193], v[92:95]
	v_mfma_f32_16x16x32_bf16 v[88:91], v[150:153], v[190:193], v[88:91]
	v_mfma_f32_16x16x32_bf16 v[76:79], v[142:145], v[198:201], v[76:79]
	v_mfma_f32_16x16x32_bf16 v[72:75], v[150:153], v[198:201], v[72:75]
	v_mfma_f32_16x16x32_bf16 v[116:119], v[154:157], v[170:173], v[116:119]
	v_mfma_f32_16x16x32_bf16 v[112:115], v[162:165], v[170:173], v[112:115]
	v_mfma_f32_16x16x32_bf16 v[100:103], v[154:157], v[178:181], v[100:103]
	v_mfma_f32_16x16x32_bf16 v[96:99], v[162:165], v[178:181], v[96:99]
	v_mfma_f32_16x16x32_bf16 v[84:87], v[154:157], v[186:189], v[84:87]
	v_mfma_f32_16x16x32_bf16 v[80:83], v[162:165], v[186:189], v[80:83]
	v_mfma_f32_16x16x32_bf16 v[68:71], v[154:157], v[194:197], v[68:71]
	v_mfma_f32_16x16x32_bf16 v[64:67], v[162:165], v[194:197], v[64:67]
	v_mfma_f32_16x16x32_bf16 v[116:119], v[158:161], v[174:177], v[116:119]
	v_mfma_f32_16x16x32_bf16 v[112:115], v[166:169], v[174:177], v[112:115]
	v_mfma_f32_16x16x32_bf16 v[100:103], v[158:161], v[182:185], v[100:103]
	v_mfma_f32_16x16x32_bf16 v[96:99], v[166:169], v[182:185], v[96:99]
	v_mfma_f32_16x16x32_bf16 v[84:87], v[158:161], v[190:193], v[84:87]
	v_mfma_f32_16x16x32_bf16 v[80:83], v[166:169], v[190:193], v[80:83]
	v_mfma_f32_16x16x32_bf16 v[68:71], v[158:161], v[198:201], v[68:71]
	v_mfma_f32_16x16x32_bf16 v[64:67], v[166:169], v[198:201], v[64:67]
	s_setprio 0
	s_waitcnt vmcnt(8)
	s_barrier
; #define G_STAGE(bufoff, gbase, voff) do { _Pragma("unroll") for (int _i = 0; _i < 2; ++_i) \
;         __builtin_amdgcn_global_load_lds((const unsigned*)((const char*)(gbase) + (voff)[_i]), (LAS unsigned*)(lds + (bufoff) + ldsw + _i * 8192), 16, 0, 0); } while (0)
; #define G_LDA(dst, b, h) do { _Pragma("unroll") for (int m = 0; m < 4; ++m) G_LD8(dst[m], lds + G_SA(b, h) + aoff + m * 2048); } while (0)
; #define G_WAIT_V(n) asm volatile("s_waitcnt vmcnt(" #n ")" ::: "memory")
; #define G_WAIT_L(n) asm volatile("s_waitcnt lgkmcnt(" #n ")" ::: "memory")
; #define G_BAR __builtin_amdgcn_s_barrier()
; #define G_SCHED __builtin_amdgcn_sched_barrier(0)
;     ...
;             G_LDA(At, 1, 1); G_STAGE(G_SB(1, 0), b02 + kstep, voffB); G_STAGE(G_SB(1, 1), b12 + kstep, voffB); G_STAGE(G_SA(1, 0), a02 + kstep, vA0);
;             G_WAIT_L(0); G_BAR; G_MMA(1, 0, At, B0); G_MMA(1, 1, At, B1); G_WAIT_V(8); G_BAR; G_SCHED;
;         }
	s_add_i32 s58, s60, s20
	v_lshl_add_u64 v[204:205], v[208:209], 0, s[8:9]
	s_mov_b32 m0, s58
	s_nop 0
	global_load_lds_dwordx4 v[204:205], off
	v_lshl_add_u64 v[204:205], v[210:211], 0, s[8:9]
	s_add_i32 m0, s58, 0x2000
	s_add_i32 s58, s61, s20
	global_load_lds_dwordx4 v[204:205], off
	v_lshl_add_u64 v[202:203], v[202:203], 0, s[8:9]
	s_mov_b32 m0, s58
	s_nop 0
	global_load_lds_dwordx4 v[202:203], off
	v_lshl_add_u64 v[202:203], v[206:207], 0, s[8:9]
	s_add_i32 m0, s58, 0x2000
	s_nop 0
	global_load_lds_dwordx4 v[202:203], off
	v_lshl_add_u64 v[202:203], v[212:213], 0, s[8:9]
	s_mov_b32 m0, s72
	s_nop 0
	global_load_lds_dwordx4 v[202:203], off
	v_lshl_add_u64 v[202:203], v[214:215], 0, s[8:9]
	s_mov_b32 m0, s73
	s_nop 0
	global_load_lds_dwordx4 v[202:203], off
	ds_read_b128 v[170:173], v140 offset:49152
	ds_read_b128 v[174:177], v140 offset:50176
	ds_read_b128 v[178:181], v140 offset:51200
	ds_read_b128 v[182:185], v140 offset:52224
	ds_read_b128 v[186:189], v140 offset:53248
	ds_read_b128 v[190:193], v140 offset:54272
	ds_read_b128 v[194:197], v140 offset:55296
	ds_read_b128 v[198:201], v140 offset:56320
	s_waitcnt lgkmcnt(0)
	s_barrier
	s_setprio 1
	s_waitcnt lgkmcnt(0)
	v_mfma_f32_16x16x32_bf16 v[60:63], v[130:133], v[170:173], v[60:63]
	v_mfma_f32_16x16x32_bf16 v[56:59], v[146:149], v[170:173], v[56:59]
	v_mfma_f32_16x16x32_bf16 v[44:47], v[130:133], v[178:181], v[44:47]
	v_mfma_f32_16x16x32_bf16 v[40:43], v[146:149], v[178:181], v[40:43]
	v_mfma_f32_16x16x32_bf16 v[28:31], v[130:133], v[186:189], v[28:31]
	v_mfma_f32_16x16x32_bf16 v[24:27], v[146:149], v[186:189], v[24:27]
	v_mfma_f32_16x16x32_bf16 v[12:15], v[130:133], v[194:197], v[12:15]
	v_mfma_f32_16x16x32_bf16 v[8:11], v[146:149], v[194:197], v[8:11]
	v_mfma_f32_16x16x32_bf16 v[60:63], v[142:145], v[174:177], v[60:63]
	v_mfma_f32_16x16x32_bf16 v[56:59], v[150:153], v[174:177], v[56:59]
	v_mfma_f32_16x16x32_bf16 v[44:47], v[142:145], v[182:185], v[44:47]
	v_mfma_f32_16x16x32_bf16 v[40:43], v[150:153], v[182:185], v[40:43]
	v_mfma_f32_16x16x32_bf16 v[28:31], v[142:145], v[190:193], v[28:31]
	v_mfma_f32_16x16x32_bf16 v[24:27], v[150:153], v[190:193], v[24:27]
	v_mfma_f32_16x16x32_bf16 v[12:15], v[142:145], v[198:201], v[12:15]
	v_mfma_f32_16x16x32_bf16 v[8:11], v[150:153], v[198:201], v[8:11]
	v_mfma_f32_16x16x32_bf16 v[52:55], v[154:157], v[170:173], v[52:55]
	v_mfma_f32_16x16x32_bf16 v[48:51], v[162:165], v[170:173], v[48:51]
	v_mfma_f32_16x16x32_bf16 v[36:39], v[154:157], v[178:181], v[36:39]
	v_mfma_f32_16x16x32_bf16 v[32:35], v[162:165], v[178:181], v[32:35]
	v_mfma_f32_16x16x32_bf16 v[20:23], v[154:157], v[186:189], v[20:23]
	v_mfma_f32_16x16x32_bf16 v[16:19], v[162:165], v[186:189], v[16:19]
	v_mfma_f32_16x16x32_bf16 v[4:7], v[154:157], v[194:197], v[4:7]
	v_mfma_f32_16x16x32_bf16 v[0:3], v[162:165], v[194:197], v[0:3]
	v_mfma_f32_16x16x32_bf16 v[52:55], v[158:161], v[174:177], v[52:55]
	v_mfma_f32_16x16x32_bf16 v[48:51], v[166:169], v[174:177], v[48:51]
	v_mfma_f32_16x16x32_bf16 v[36:39], v[158:161], v[182:185], v[36:39]
	v_mfma_f32_16x16x32_bf16 v[32:35], v[166:169], v[182:185], v[32:35]
	v_mfma_f32_16x16x32_bf16 v[20:23], v[158:161], v[190:193], v[20:23]
	v_mfma_f32_16x16x32_bf16 v[16:19], v[166:169], v[190:193], v[16:19]
	v_mfma_f32_16x16x32_bf16 v[4:7], v[158:161], v[198:201], v[4:7]
	v_mfma_f32_16x16x32_bf16 v[0:3], v[166:169], v[198:201], v[0:3]
	s_setprio 0
	s_waitcnt vmcnt(8)
	s_barrier
	s_add_u32 s41, s41, 0x100
	s_addc_u32 s53, s53, 0
	s_add_u32 s55, s55, 0x100
	s_addc_u32 s64, s64, 0
	s_add_u32 s65, s65, 0x100
	s_addc_u32 s79, s79, 0
	s_add_u32 s56, s56, 0x100
	s_addc_u32 s57, s57, 0
	s_cmp_ge_i32 s80, s0
	s_mov_b32 s58, s80
	s_cbranch_scc0 .LBB0_549
	v_readlane_b32 s79, v255, 13
	s_and_b64 vcc, exec, s[38:39]
	s_cbranch_vccz .LBB0_552

; #define G_STAGE(bufoff, gbase, voff) do { _Pragma("unroll") for (int _i = 0; _i < 2; ++_i) \
;         __builtin_amdgcn_global_load_lds((const unsigned*)((const char*)(gbase) + (voff)[_i]), (LAS unsigned*)(lds + (bufoff) + ldsw + _i * 8192), 16, 0, 0); } while (0)
; #define G_LDA(dst, b, h) do { _Pragma("unroll") for (int m = 0; m < 4; ++m) G_LD8(dst[m], lds + G_SA(b, h) + aoff + m * 2048); } while (0)
; #define G_LDB(dst, b, h) do { _Pragma("unroll") for (int n = 0; n < 2; ++n) G_LD8(dst[n], lds + G_SB(b, h) + boff + n * 2048); } while (0)
; #define G_WAIT_V(n) asm volatile("s_waitcnt vmcnt(" #n ")" ::: "memory")
; #define G_WAIT_L(n) asm volatile("s_waitcnt lgkmcnt(" #n ")" ::: "memory")
; #define G_BAR __builtin_amdgcn_s_barrier()
; #define G_SCHED __builtin_amdgcn_sched_barrier(0)
;     __device__ __forceinline__ unsigned row_off(const Unit& u, int r, LAS unsigned char* lds) const { return (unsigned)((const LAS int*)(lds + LDS_STAGE + u.q * 4096))[r] * (unsigned)rowbytes; }
;     ...
;             const char* a11 = cur.a1 + (size_t)(t + 1) * kstep;
;             const char* a02 = last ? nxt.a0 : cur.a0 + (size_t)(t + 2) * kstep; const char* a12 = last ? nxt.a1 : cur.a1 + (size_t)(t + 2) * kstep;
;             const char* b02 = last ? nxt.b0 : cur.b0 + (size_t)(t + 2) * kstep; const char* b12 = last ? nxt.b1 : cur.b1 + (size_t)(t + 2) * kstep;
;             G_LDB(B0, 0, 0); G_LDB(B1, 0, 1); G_SCHED; G_LDA(At, 0, 0); G_STAGE(G_SA(1, 1), a11, vA1);
;             if constexpr (GATHER) { if (last) { int tz = tid; asm volatile("" : "+v"(tz));
; #pragma unroll
;                 for (int i = 0; i < 2; ++i) { int R, C; stage_rc(tz * 16 + i * 8192, R, C); gc0[i] = S.row_off(nxt, R, lds) + (unsigned)C * 2u; gc1[i] = S.row_off(nxt, 128 + R, lds) + (unsigned)C * 2u; } } }
;             G_WAIT_L(0); G_BAR; G_MMA(0, 0, At, B0); G_MMA(0, 1, At, B1); G_WAIT_V(8); G_BAR; G_SCHED;
;             G_LDA(At, 0, 1); G_STAGE(G_SB(0, 0), b02, voffB); G_STAGE(G_SB(0, 1), b12, voffB); G_STAGE(G_SA(0, 0), a02, vA0);
.LBB0_576:
	s_add_i32 s71, s52, 2
	s_add_u32 s72, s50, 0x80
	s_addc_u32 s53, s51, 0
	s_add_i32 s75, s22, s20
	s_add_i32 m0, s62, 0xc000
	s_add_i32 s74, s62, 0xe000
	s_add_i32 s76, s75, 0x2000
	s_cmp_eq_u32 s23, s52
	s_cselect_b32 s52, s38, s72
	s_cselect_b32 s55, s37, s70
	s_cselect_b32 s54, s36, s59
	s_cselect_b32 s57, s41, s45
	s_cselect_b32 s56, s40, s35
	s_cselect_b32 s53, s39, s53
	global_load_lds_dwordx4 v240, s[50:51]
	s_mov_b32 m0, s74
	v_mov_b32_e32 v205, v129
	global_load_lds_dwordx4 v242, s[50:51]
	ds_read_b128 v[138:141], v134
	ds_read_b128 v[142:145], v134 offset:1024
	ds_read_b128 v[146:149], v134 offset:2048
	ds_read_b128 v[150:153], v134 offset:3072
	ds_read_b128 v[154:157], v135
	ds_read_b128 v[158:161], v135 offset:1024
	ds_read_b128 v[162:165], v135 offset:2048
	ds_read_b128 v[166:169], v135 offset:3072
	ds_read_b128 v[170:173], v136
	ds_read_b128 v[174:177], v136 offset:1024
	ds_read_b128 v[178:181], v136 offset:2048
	ds_read_b128 v[182:185], v136 offset:3072
	ds_read_b128 v[186:189], v136 offset:4096
	ds_read_b128 v[190:193], v136 offset:5120
	ds_read_b128 v[194:197], v136 offset:6144
	ds_read_b128 v[198:201], v136 offset:7168
	s_waitcnt lgkmcnt(0)
	s_barrier
	s_setprio 1
	s_waitcnt lgkmcnt(0)
	v_mfma_f32_16x16x32_bf16 v[124:127], v[138:141], v[170:173], v[124:127]
	v_mfma_f32_16x16x32_bf16 v[120:123], v[146:149], v[170:173], v[120:123]
	v_mfma_f32_16x16x32_bf16 v[108:111], v[138:141], v[178:181], v[108:111]
	v_mfma_f32_16x16x32_bf16 v[104:107], v[146:149], v[178:181], v[104:107]
	v_mfma_f32_16x16x32_bf16 v[92:95], v[138:141], v[186:189], v[92:95]
	v_mfma_f32_16x16x32_bf16 v[88:91], v[146:149], v[186:189], v[88:91]
	v_mfma_f32_16x16x32_bf16 v[76:79], v[138:141], v[194:197], v[76:79]
	v_mfma_f32_16x16x32_bf16 v[72:75], v[146:149], v[194:197], v[72:75]
	v_mfma_f32_16x16x32_bf16 v[124:127], v[142:145], v[174:177], v[124:127]
	v_mfma_f32_16x16x32_bf16 v[120:123], v[150:153], v[174:177], v[120:123]
	v_mfma_f32_16x16x32_bf16 v[108:111], v[142:145], v[182:185], v[108:111]
	v_mfma_f32_16x16x32_bf16 v[104:107], v[150:153], v[182:185], v[104:107]
	v_mfma_f32_16x16x32_bf16 v[92:95], v[142:145], v[190:193], v[92:95]
	v_mfma_f32_16x16x32_bf16 v[88:91], v[150:153], v[190:193], v[88:91]
	v_mfma_f32_16x16x32_bf16 v[76:79], v[142:145], v[198:201], v[76:79]
	v_mfma_f32_16x16x32_bf16 v[72:75], v[150:153], v[198:201], v[72:75]
	v_mfma_f32_16x16x32_bf16 v[116:119], v[154:157], v[170:173], v[116:119]
	v_mfma_f32_16x16x32_bf16 v[112:115], v[162:165], v[170:173], v[112:115]
	v_mfma_f32_16x16x32_bf16 v[100:103], v[154:157], v[178:181], v[100:103]
	v_mfma_f32_16x16x32_bf16 v[96:99], v[162:165], v[178:181], v[96:99]
	v_mfma_f32_16x16x32_bf16 v[84:87], v[154:157], v[186:189], v[84:87]
	v_mfma_f32_16x16x32_bf16 v[80:83], v[162:165], v[186:189], v[80:83]
	v_mfma_f32_16x16x32_bf16 v[68:71], v[154:157], v[194:197], v[68:71]
	v_mfma_f32_16x16x32_bf16 v[64:67], v[162:165], v[194:197], v[64:67]
	v_mfma_f32_16x16x32_bf16 v[116:119], v[158:161], v[174:177], v[116:119]
	v_mfma_f32_16x16x32_bf16 v[112:115], v[166:169], v[174:177], v[112:115]
	v_mfma_f32_16x16x32_bf16 v[100:103], v[158:161], v[182:185], v[100:103]
	v_mfma_f32_16x16x32_bf16 v[96:99], v[166:169], v[182:185], v[96:99]
	v_mfma_f32_16x16x32_bf16 v[84:87], v[158:161], v[190:193], v[84:87]
	v_mfma_f32_16x16x32_bf16 v[80:83], v[166:169], v[190:193], v[80:83]
	v_mfma_f32_16x16x32_bf16 v[68:71], v[158:161], v[198:201], v[68:71]
	v_mfma_f32_16x16x32_bf16 v[64:67], v[166:169], v[198:201], v[64:67]
	s_setprio 0
	s_waitcnt vmcnt(8)
	s_barrier
	s_mov_b32 m0, s75
	s_nop 0
	global_load_lds_dwordx4 v244, s[56:57]
	s_mov_b32 m0, s76
	s_cselect_b32 s73, s43, s58
	s_cselect_b32 s72, s42, s49
	s_add_i32 s74, s24, s20
	global_load_lds_dwordx4 v246, s[56:57]
	s_mov_b32 m0, s74
	v_mov_b32_e32 v203, v129
	global_load_lds_dwordx4 v244, s[72:73]
	s_add_i32 m0, s74, 0x2000
	v_mov_b32_e32 v207, v129
	global_load_lds_dwordx4 v246, s[72:73]
	s_mov_b32 m0, s62
	v_lshl_add_u64 v[208:209], s[56:57], 0, v[244:245]
	global_load_lds_dwordx4 v240, s[54:55]
	s_mov_b32 m0, s63
	v_lshl_add_u64 v[210:211], s[56:57], 0, v[246:247]
	global_load_lds_dwordx4 v242, s[54:55]
	ds_read_b128 v[170:173], v136 offset:16384
	ds_read_b128 v[174:177], v136 offset:17408
	ds_read_b128 v[178:181], v136 offset:18432
	ds_read_b128 v[182:185], v136 offset:19456
	ds_read_b128 v[186:189], v136 offset:20480
	ds_read_b128 v[190:193], v136 offset:21504
	ds_read_b128 v[194:197], v136 offset:22528
	ds_read_b128 v[198:201], v136 offset:23552
	s_waitcnt lgkmcnt(0)
	v_lshl_add_u64 v[202:203], s[72:73], 0, v[244:245]
	v_lshl_add_u64 v[206:207], s[72:73], 0, v[246:247]
	v_lshl_add_u64 v[212:213], s[54:55], 0, v[240:241]
	v_lshl_add_u64 v[214:215], s[54:55], 0, v[242:243]
	s_barrier
; #define G_STAGE(bufoff, gbase, voff) do { _Pragma("unroll") for (int _i = 0; _i < 2; ++_i) \
;         __builtin_amdgcn_global_load_lds((const unsigned*)((const char*)(gbase) + (voff)[_i]), (LAS unsigned*)(lds + (bufoff) + ldsw + _i * 8192), 16, 0, 0); } while (0)
; #define G_LDA(dst, b, h) do { _Pragma("unroll") for (int m = 0; m < 4; ++m) G_LD8(dst[m], lds + G_SA(b, h) + aoff + m * 2048); } while (0)
; #define G_LDB(dst, b, h) do { _Pragma("unroll") for (int n = 0; n < 2; ++n) G_LD8(dst[n], lds + G_SB(b, h) + boff + n * 2048); } while (0)
; #define G_WAIT_V(n) asm volatile("s_waitcnt vmcnt(" #n ")" ::: "memory")
; #define G_WAIT_L(n) asm volatile("s_waitcnt lgkmcnt(" #n ")" ::: "memory")
; #define G_BAR __builtin_amdgcn_s_barrier()
; #define G_SCHED __builtin_amdgcn_sched_barrier(0)
;     ...
;             G_WAIT_L(0); G_BAR; G_MMA(1, 0, At, B0); G_MMA(1, 1, At, B1); G_WAIT_V(8); G_BAR; G_SCHED;
;             G_LDB(B0, 1, 0); G_LDB(B1, 1, 1); G_SCHED; G_LDA(At, 1, 0); G_STAGE(G_SA(0, 1), a12, vA1);
;             G_WAIT_L(0); G_BAR; G_MMA(0, 0, At, B0); G_MMA(0, 1, At, B1); G_WAIT_V(8); G_BAR; G_SCHED;
	s_setprio 1
	s_waitcnt lgkmcnt(0)
	v_mfma_f32_16x16x32_bf16 v[60:63], v[138:141], v[170:173], v[60:63]
	v_mfma_f32_16x16x32_bf16 v[56:59], v[146:149], v[170:173], v[56:59]
	v_mfma_f32_16x16x32_bf16 v[44:47], v[138:141], v[178:181], v[44:47]
	v_mfma_f32_16x16x32_bf16 v[40:43], v[146:149], v[178:181], v[40:43]
	v_mfma_f32_16x16x32_bf16 v[28:31], v[138:141], v[186:189], v[28:31]
	v_mfma_f32_16x16x32_bf16 v[24:27], v[146:149], v[186:189], v[24:27]
	v_mfma_f32_16x16x32_bf16 v[12:15], v[138:141], v[194:197], v[12:15]
	v_mfma_f32_16x16x32_bf16 v[8:11], v[146:149], v[194:197], v[8:11]
	v_mfma_f32_16x16x32_bf16 v[60:63], v[142:145], v[174:177], v[60:63]
	v_mfma_f32_16x16x32_bf16 v[56:59], v[150:153], v[174:177], v[56:59]
	v_mfma_f32_16x16x32_bf16 v[44:47], v[142:145], v[182:185], v[44:47]
	v_mfma_f32_16x16x32_bf16 v[40:43], v[150:153], v[182:185], v[40:43]
	v_mfma_f32_16x16x32_bf16 v[28:31], v[142:145], v[190:193], v[28:31]
	v_mfma_f32_16x16x32_bf16 v[24:27], v[150:153], v[190:193], v[24:27]
	v_mfma_f32_16x16x32_bf16 v[12:15], v[142:145], v[198:201], v[12:15]
	v_mfma_f32_16x16x32_bf16 v[8:11], v[150:153], v[198:201], v[8:11]
	v_mfma_f32_16x16x32_bf16 v[52:55], v[154:157], v[170:173], v[52:55]
	v_mfma_f32_16x16x32_bf16 v[48:51], v[162:165], v[170:173], v[48:51]
	v_mfma_f32_16x16x32_bf16 v[36:39], v[154:157], v[178:181], v[36:39]
	v_mfma_f32_16x16x32_bf16 v[32:35], v[162:165], v[178:181], v[32:35]
	v_mfma_f32_16x16x32_bf16 v[20:23], v[154:157], v[186:189], v[20:23]
	v_mfma_f32_16x16x32_bf16 v[16:19], v[162:165], v[186:189], v[16:19]
	v_mfma_f32_16x16x32_bf16 v[4:7], v[154:157], v[194:197], v[4:7]
	v_mfma_f32_16x16x32_bf16 v[0:3], v[162:165], v[194:197], v[0:3]
	v_mfma_f32_16x16x32_bf16 v[52:55], v[158:161], v[174:177], v[52:55]
	v_mfma_f32_16x16x32_bf16 v[48:51], v[166:169], v[174:177], v[48:51]
	v_mfma_f32_16x16x32_bf16 v[36:39], v[158:161], v[182:185], v[36:39]
	v_mfma_f32_16x16x32_bf16 v[32:35], v[166:169], v[182:185], v[32:35]
	v_mfma_f32_16x16x32_bf16 v[20:23], v[158:161], v[190:193], v[20:23]
	v_mfma_f32_16x16x32_bf16 v[16:19], v[166:169], v[190:193], v[16:19]
	v_mfma_f32_16x16x32_bf16 v[4:7], v[158:161], v[198:201], v[4:7]
	v_mfma_f32_16x16x32_bf16 v[0:3], v[166:169], v[198:201], v[0:3]
	s_setprio 0
	s_waitcnt vmcnt(8)
	s_barrier
	s_add_i32 s54, 0, 0x18000
	s_add_i32 s55, 0, 0x1c000
	s_mov_b32 m0, s64
	s_nop 0
	global_load_lds_dwordx4 v240, s[52:53]
	s_mov_b32 m0, s65
	s_nop 0
	global_load_lds_dwordx4 v242, s[52:53]
	v_add_u32_e32 v137, s54, v133
	ds_read_b128 v[138:141], v137
	ds_read_b128 v[142:145], v137 offset:1024
	ds_read_b128 v[146:149], v137 offset:2048
	ds_read_b128 v[150:153], v137 offset:3072
	v_add_u32_e32 v137, s55, v133
	ds_read_b128 v[154:157], v137
	ds_read_b128 v[158:161], v137 offset:1024
	ds_read_b128 v[162:165], v137 offset:2048
	ds_read_b128 v[166:169], v137 offset:3072
	ds_read_b128 v[170:173], v136 offset:32768
	ds_read_b128 v[174:177], v136 offset:33792
	ds_read_b128 v[178:181], v136 offset:34816
	ds_read_b128 v[182:185], v136 offset:35840
	ds_read_b128 v[186:189], v136 offset:36864
	ds_read_b128 v[190:193], v136 offset:37888
	ds_read_b128 v[194:197], v136 offset:38912
	ds_read_b128 v[198:201], v136 offset:39936
	s_waitcnt lgkmcnt(0)
	s_barrier
	s_setprio 1
	s_waitcnt lgkmcnt(0)
	v_mfma_f32_16x16x32_bf16 v[124:127], v[138:141], v[170:173], v[124:127]
	v_mfma_f32_16x16x32_bf16 v[120:123], v[146:149], v[170:173], v[120:123]
	v_mfma_f32_16x16x32_bf16 v[108:111], v[138:141], v[178:181], v[108:111]
	v_mfma_f32_16x16x32_bf16 v[104:107], v[146:149], v[178:181], v[104:107]
	v_mfma_f32_16x16x32_bf16 v[92:95], v[138:141], v[186:189], v[92:95]
	v_mfma_f32_16x16x32_bf16 v[88:91], v[146:149], v[186:189], v[88:91]
	v_mfma_f32_16x16x32_bf16 v[76:79], v[138:141], v[194:197], v[76:79]
	v_mfma_f32_16x16x32_bf16 v[72:75], v[146:149], v[194:197], v[72:75]
	v_mfma_f32_16x16x32_bf16 v[124:127], v[142:145], v[174:177], v[124:127]
	v_mfma_f32_16x16x32_bf16 v[120:123], v[150:153], v[174:177], v[120:123]
	v_mfma_f32_16x16x32_bf16 v[108:111], v[142:145], v[182:185], v[108:111]
	v_mfma_f32_16x16x32_bf16 v[104:107], v[150:153], v[182:185], v[104:107]
	v_mfma_f32_16x16x32_bf16 v[92:95], v[142:145], v[190:193], v[92:95]
	v_mfma_f32_16x16x32_bf16 v[88:91], v[150:153], v[190:193], v[88:91]
	v_mfma_f32_16x16x32_bf16 v[76:79], v[142:145], v[198:201], v[76:79]
	v_mfma_f32_16x16x32_bf16 v[72:75], v[150:153], v[198:201], v[72:75]
	v_mfma_f32_16x16x32_bf16 v[116:119], v[154:157], v[170:173], v[116:119]
	v_mfma_f32_16x16x32_bf16 v[112:115], v[162:165], v[170:173], v[112:115]
	v_mfma_f32_16x16x32_bf16 v[100:103], v[154:157], v[178:181], v[100:103]
	v_mfma_f32_16x16x32_bf16 v[96:99], v[162:165], v[178:181], v[96:99]
	v_mfma_f32_16x16x32_bf16 v[84:87], v[154:157], v[186:189], v[84:87]
	v_mfma_f32_16x16x32_bf16 v[80:83], v[162:165], v[186:189], v[80:83]
	v_mfma_f32_16x16x32_bf16 v[68:71], v[154:157], v[194:197], v[68:71]
	v_mfma_f32_16x16x32_bf16 v[64:67], v[162:165], v[194:197], v[64:67]
	v_mfma_f32_16x16x32_bf16 v[116:119], v[158:161], v[174:177], v[116:119]
	v_mfma_f32_16x16x32_bf16 v[112:115], v[166:169], v[174:177], v[112:115]
	v_mfma_f32_16x16x32_bf16 v[100:103], v[158:161], v[182:185], v[100:103]
	v_mfma_f32_16x16x32_bf16 v[96:99], v[166:169], v[182:185], v[96:99]
	v_mfma_f32_16x16x32_bf16 v[84:87], v[158:161], v[190:193], v[84:87]
	v_mfma_f32_16x16x32_bf16 v[80:83], v[166:169], v[190:193], v[80:83]
	v_mfma_f32_16x16x32_bf16 v[68:71], v[158:161], v[198:201], v[68:71]
	v_mfma_f32_16x16x32_bf16 v[64:67], v[166:169], v[198:201], v[64:67]
	s_setprio 0
	s_waitcnt vmcnt(8)
	s_barrier
; #define G_STAGE(bufoff, gbase, voff) do { _Pragma("unroll") for (int _i = 0; _i < 2; ++_i) \
;         __builtin_amdgcn_global_load_lds((const unsigned*)((const char*)(gbase) + (voff)[_i]), (LAS unsigned*)(lds + (bufoff) + ldsw + _i * 8192), 16, 0, 0); } while (0)
; #define G_LDA(dst, b, h) do { _Pragma("unroll") for (int m = 0; m < 4; ++m) G_LD8(dst[m], lds + G_SA(b, h) + aoff + m * 2048); } while (0)
; #define G_WAIT_V(n) asm volatile("s_waitcnt vmcnt(" #n ")" ::: "memory")
; #define G_WAIT_L(n) asm volatile("s_waitcnt lgkmcnt(" #n ")" ::: "memory")
; #define G_BAR __builtin_amdgcn_s_barrier()
; #define G_SCHED __builtin_amdgcn_sched_barrier(0)
;     ...
;             G_LDA(At, 1, 1); G_STAGE(G_SB(1, 0), b02 + kstep, voffB); G_STAGE(G_SB(1, 1), b12 + kstep, voffB); G_STAGE(G_SA(1, 0), a02 + kstep, vA0);
;             G_WAIT_L(0); G_BAR; G_MMA(1, 0, At, B0); G_MMA(1, 1, At, B1); G_WAIT_V(8); G_BAR; G_SCHED;
;         }
	s_add_i32 s52, s54, s20
	v_lshl_add_u64 v[204:205], v[208:209], 0, s[6:7]
	s_mov_b32 m0, s52
	s_nop 0
	global_load_lds_dwordx4 v[204:205], off
	v_lshl_add_u64 v[204:205], v[210:211], 0, s[6:7]
	s_add_i32 m0, s52, 0x2000
	s_add_i32 s52, s55, s20
	global_load_lds_dwordx4 v[204:205], off
	v_lshl_add_u64 v[202:203], v[202:203], 0, s[6:7]
	s_mov_b32 m0, s52
	s_nop 0
	global_load_lds_dwordx4 v[202:203], off
	v_lshl_add_u64 v[202:203], v[206:207], 0, s[6:7]
	s_add_i32 m0, s52, 0x2000
	s_nop 0
	global_load_lds_dwordx4 v[202:203], off
	v_lshl_add_u64 v[202:203], v[212:213], 0, s[6:7]
	s_mov_b32 m0, s25
	s_nop 0
	global_load_lds_dwordx4 v[202:203], off
	v_lshl_add_u64 v[202:203], v[214:215], 0, s[6:7]
	s_mov_b32 m0, s67
	s_nop 0
	global_load_lds_dwordx4 v[202:203], off
	ds_read_b128 v[170:173], v136 offset:49152
	ds_read_b128 v[174:177], v136 offset:50176
	ds_read_b128 v[178:181], v136 offset:51200
	ds_read_b128 v[182:185], v136 offset:52224
	ds_read_b128 v[186:189], v136 offset:53248
	ds_read_b128 v[190:193], v136 offset:54272
	ds_read_b128 v[194:197], v136 offset:55296
	ds_read_b128 v[198:201], v136 offset:56320
	s_waitcnt lgkmcnt(0)
	s_barrier
	s_setprio 1
	s_waitcnt lgkmcnt(0)
	v_mfma_f32_16x16x32_bf16 v[60:63], v[138:141], v[170:173], v[60:63]
	v_mfma_f32_16x16x32_bf16 v[56:59], v[146:149], v[170:173], v[56:59]
	v_mfma_f32_16x16x32_bf16 v[44:47], v[138:141], v[178:181], v[44:47]
	v_mfma_f32_16x16x32_bf16 v[40:43], v[146:149], v[178:181], v[40:43]
	v_mfma_f32_16x16x32_bf16 v[28:31], v[138:141], v[186:189], v[28:31]
	v_mfma_f32_16x16x32_bf16 v[24:27], v[146:149], v[186:189], v[24:27]
	v_mfma_f32_16x16x32_bf16 v[12:15], v[138:141], v[194:197], v[12:15]
	v_mfma_f32_16x16x32_bf16 v[8:11], v[146:149], v[194:197], v[8:11]
	v_mfma_f32_16x16x32_bf16 v[60:63], v[142:145], v[174:177], v[60:63]
	v_mfma_f32_16x16x32_bf16 v[56:59], v[150:153], v[174:177], v[56:59]
	v_mfma_f32_16x16x32_bf16 v[44:47], v[142:145], v[182:185], v[44:47]
	v_mfma_f32_16x16x32_bf16 v[40:43], v[150:153], v[182:185], v[40:43]
	v_mfma_f32_16x16x32_bf16 v[28:31], v[142:145], v[190:193], v[28:31]
	v_mfma_f32_16x16x32_bf16 v[24:27], v[150:153], v[190:193], v[24:27]
	v_mfma_f32_16x16x32_bf16 v[12:15], v[142:145], v[198:201], v[12:15]
	v_mfma_f32_16x16x32_bf16 v[8:11], v[150:153], v[198:201], v[8:11]
	v_mfma_f32_16x16x32_bf16 v[52:55], v[154:157], v[170:173], v[52:55]
	v_mfma_f32_16x16x32_bf16 v[48:51], v[162:165], v[170:173], v[48:51]
	v_mfma_f32_16x16x32_bf16 v[36:39], v[154:157], v[178:181], v[36:39]
	v_mfma_f32_16x16x32_bf16 v[32:35], v[162:165], v[178:181], v[32:35]
	v_mfma_f32_16x16x32_bf16 v[20:23], v[154:157], v[186:189], v[20:23]
	v_mfma_f32_16x16x32_bf16 v[16:19], v[162:165], v[186:189], v[16:19]
	v_mfma_f32_16x16x32_bf16 v[4:7], v[154:157], v[194:197], v[4:7]
	v_mfma_f32_16x16x32_bf16 v[0:3], v[162:165], v[194:197], v[0:3]
	v_mfma_f32_16x16x32_bf16 v[52:55], v[158:161], v[174:177], v[52:55]
	v_mfma_f32_16x16x32_bf16 v[48:51], v[166:169], v[174:177], v[48:51]
	v_mfma_f32_16x16x32_bf16 v[36:39], v[158:161], v[182:185], v[36:39]
	v_mfma_f32_16x16x32_bf16 v[32:35], v[166:169], v[182:185], v[32:35]
	v_mfma_f32_16x16x32_bf16 v[20:23], v[158:161], v[190:193], v[20:23]
	v_mfma_f32_16x16x32_bf16 v[16:19], v[166:169], v[190:193], v[16:19]
	v_mfma_f32_16x16x32_bf16 v[4:7], v[158:161], v[198:201], v[4:7]
	v_mfma_f32_16x16x32_bf16 v[0:3], v[166:169], v[198:201], v[0:3]
	s_setprio 0
	s_waitcnt vmcnt(8)
	s_barrier
	s_add_u32 s35, s35, 0x100
	s_addc_u32 s45, s45, 0
	s_add_u32 s49, s49, 0x100
	s_addc_u32 s58, s58, 0
	s_add_u32 s59, s59, 0x100
	s_addc_u32 s70, s70, 0
	s_add_u32 s50, s50, 0x100
	s_addc_u32 s51, s51, 0
	s_cmp_ge_i32 s71, s2
	s_mov_b32 s52, s71
	s_cbranch_scc0 .LBB0_576
	s_and_b64 vcc, exec, s[14:15]
	s_cbranch_vccz .LBB0_579

; #define G_STAGE(bufoff, gbase, voff) do { _Pragma("unroll") for (int _i = 0; _i < 2; ++_i) \
;         __builtin_amdgcn_global_load_lds((const unsigned*)((const char*)(gbase) + (voff)[_i]), (LAS unsigned*)(lds + (bufoff) + ldsw + _i * 8192), 16, 0, 0); } while (0)
; #define G_LDA(dst, b, h) do { _Pragma("unroll") for (int m = 0; m < 4; ++m) G_LD8(dst[m], lds + G_SA(b, h) + aoff + m * 2048); } while (0)
; #define G_LDB(dst, b, h) do { _Pragma("unroll") for (int n = 0; n < 2; ++n) G_LD8(dst[n], lds + G_SB(b, h) + boff + n * 2048); } while (0)
; #define G_WAIT_V(n) asm volatile("s_waitcnt vmcnt(" #n ")" ::: "memory")
; #define G_WAIT_L(n) asm volatile("s_waitcnt lgkmcnt(" #n ")" ::: "memory")
; #define G_BAR __builtin_amdgcn_s_barrier()
; #define G_SCHED __builtin_amdgcn_sched_barrier(0)
;     __device__ __forceinline__ unsigned row_off(const Unit& u, int r, LAS unsigned char* lds) const { return (unsigned)((const LAS int*)(lds + LDS_STAGE + u.q * 4096))[r] * (unsigned)rowbytes; }
;     ...
;             const char* a11 = cur.a1 + (size_t)(t + 1) * kstep;
;             const char* a02 = last ? nxt.a0 : cur.a0 + (size_t)(t + 2) * kstep; const char* a12 = last ? nxt.a1 : cur.a1 + (size_t)(t + 2) * kstep;
;             const char* b02 = last ? nxt.b0 : cur.b0 + (size_t)(t + 2) * kstep; const char* b12 = last ? nxt.b1 : cur.b1 + (size_t)(t + 2) * kstep;
;             G_LDB(B0, 0, 0); G_LDB(B1, 0, 1); G_SCHED; G_LDA(At, 0, 0); G_STAGE(G_SA(1, 1), a11, vA1);
;             if constexpr (GATHER) { if (last) { int tz = tid; asm volatile("" : "+v"(tz));
; #pragma unroll
;                 for (int i = 0; i < 2; ++i) { int R, C; stage_rc(tz * 16 + i * 8192, R, C); gc0[i] = S.row_off(nxt, R, lds) + (unsigned)C * 2u; gc1[i] = S.row_off(nxt, 128 + R, lds) + (unsigned)C * 2u; } } }
;             G_WAIT_L(0); G_BAR; G_MMA(0, 0, At, B0); G_MMA(0, 1, At, B1); G_WAIT_V(8); G_BAR; G_SCHED;
;             G_LDA(At, 0, 1); G_STAGE(G_SB(0, 0), b02, voffB); G_STAGE(G_SB(0, 1), b12, voffB); G_STAGE(G_SA(0, 0), a02, vA0);
.LBB0_812:
	s_add_i32 s74, s54, 2
	s_add_u32 s75, s52, 0x80
	s_addc_u32 s55, s53, 0
	s_add_i32 s78, s68, s20
	s_add_i32 m0, s22, 0xc000
	s_add_i32 s77, s22, 0xe000
	s_add_i32 s79, s78, 0x2000
	s_cmp_eq_u32 s67, s54
	s_cselect_b32 s54, s46, s75
	s_cselect_b32 s57, s49, s73
	s_cselect_b32 s56, s48, s72
	s_cselect_b32 s59, s43, s61
	s_cselect_b32 s58, s42, s60
	s_cselect_b32 s55, s47, s55
	global_load_lds_dwordx4 v240, s[52:53]
	s_mov_b32 m0, s77
	v_mov_b32_e32 v205, v129
	global_load_lds_dwordx4 v242, s[52:53]
	ds_read_b128 v[138:141], v134
	ds_read_b128 v[142:145], v134 offset:1024
	ds_read_b128 v[146:149], v134 offset:2048
	ds_read_b128 v[150:153], v134 offset:3072
	ds_read_b128 v[154:157], v135
	ds_read_b128 v[158:161], v135 offset:1024
	ds_read_b128 v[162:165], v135 offset:2048
	ds_read_b128 v[166:169], v135 offset:3072
	ds_read_b128 v[170:173], v136
	ds_read_b128 v[174:177], v136 offset:1024
	ds_read_b128 v[178:181], v136 offset:2048
	ds_read_b128 v[182:185], v136 offset:3072
	ds_read_b128 v[186:189], v136 offset:4096
	ds_read_b128 v[190:193], v136 offset:5120
	ds_read_b128 v[194:197], v136 offset:6144
	ds_read_b128 v[198:201], v136 offset:7168
	s_waitcnt lgkmcnt(0)
	s_barrier
	s_setprio 1
	s_waitcnt lgkmcnt(0)
	v_mfma_f32_16x16x32_bf16 v[124:127], v[138:141], v[170:173], v[124:127]
	v_mfma_f32_16x16x32_bf16 v[120:123], v[146:149], v[170:173], v[120:123]
	v_mfma_f32_16x16x32_bf16 v[108:111], v[138:141], v[178:181], v[108:111]
	v_mfma_f32_16x16x32_bf16 v[104:107], v[146:149], v[178:181], v[104:107]
	v_mfma_f32_16x16x32_bf16 v[92:95], v[138:141], v[186:189], v[92:95]
	v_mfma_f32_16x16x32_bf16 v[88:91], v[146:149], v[186:189], v[88:91]
	v_mfma_f32_16x16x32_bf16 v[76:79], v[138:141], v[194:197], v[76:79]
	v_mfma_f32_16x16x32_bf16 v[72:75], v[146:149], v[194:197], v[72:75]
	v_mfma_f32_16x16x32_bf16 v[124:127], v[142:145], v[174:177], v[124:127]
	v_mfma_f32_16x16x32_bf16 v[120:123], v[150:153], v[174:177], v[120:123]
	v_mfma_f32_16x16x32_bf16 v[108:111], v[142:145], v[182:185], v[108:111]
	v_mfma_f32_16x16x32_bf16 v[104:107], v[150:153], v[182:185], v[104:107]
	v_mfma_f32_16x16x32_bf16 v[92:95], v[142:145], v[190:193], v[92:95]
	v_mfma_f32_16x16x32_bf16 v[88:91], v[150:153], v[190:193], v[88:91]
	v_mfma_f32_16x16x32_bf16 v[76:79], v[142:145], v[198:201], v[76:79]
	v_mfma_f32_16x16x32_bf16 v[72:75], v[150:153], v[198:201], v[72:75]
	v_mfma_f32_16x16x32_bf16 v[116:119], v[154:157], v[170:173], v[116:119]
	v_mfma_f32_16x16x32_bf16 v[112:115], v[162:165], v[170:173], v[112:115]
	v_mfma_f32_16x16x32_bf16 v[100:103], v[154:157], v[178:181], v[100:103]
	v_mfma_f32_16x16x32_bf16 v[96:99], v[162:165], v[178:181], v[96:99]
	v_mfma_f32_16x16x32_bf16 v[84:87], v[154:157], v[186:189], v[84:87]
	v_mfma_f32_16x16x32_bf16 v[80:83], v[162:165], v[186:189], v[80:83]
	v_mfma_f32_16x16x32_bf16 v[68:71], v[154:157], v[194:197], v[68:71]
	v_mfma_f32_16x16x32_bf16 v[64:67], v[162:165], v[194:197], v[64:67]
	v_mfma_f32_16x16x32_bf16 v[116:119], v[158:161], v[174:177], v[116:119]
	v_mfma_f32_16x16x32_bf16 v[112:115], v[166:169], v[174:177], v[112:115]
	v_mfma_f32_16x16x32_bf16 v[100:103], v[158:161], v[182:185], v[100:103]
	v_mfma_f32_16x16x32_bf16 v[96:99], v[166:169], v[182:185], v[96:99]
	v_mfma_f32_16x16x32_bf16 v[84:87], v[158:161], v[190:193], v[84:87]
	v_mfma_f32_16x16x32_bf16 v[80:83], v[166:169], v[190:193], v[80:83]
	v_mfma_f32_16x16x32_bf16 v[68:71], v[158:161], v[198:201], v[68:71]
	v_mfma_f32_16x16x32_bf16 v[64:67], v[166:169], v[198:201], v[64:67]
	s_setprio 0
	s_waitcnt vmcnt(8)
	s_barrier
	s_mov_b32 m0, s78
	s_nop 0
	global_load_lds_dwordx4 v244, s[58:59]
	s_mov_b32 m0, s79
	s_cselect_b32 s79, s45, s71
	s_cselect_b32 s78, s44, s62
	s_add_i32 s75, s69, s20
	global_load_lds_dwordx4 v246, s[58:59]
	s_mov_b32 m0, s75
	v_mov_b32_e32 v203, v129
	global_load_lds_dwordx4 v244, s[78:79]
	s_add_i32 m0, s75, 0x2000
	v_mov_b32_e32 v207, v129
	global_load_lds_dwordx4 v246, s[78:79]
	s_mov_b32 m0, s22
	v_lshl_add_u64 v[208:209], s[58:59], 0, v[244:245]
	global_load_lds_dwordx4 v240, s[56:57]
	s_mov_b32 m0, s23
	v_lshl_add_u64 v[210:211], s[58:59], 0, v[246:247]
	global_load_lds_dwordx4 v242, s[56:57]
	ds_read_b128 v[170:173], v136 offset:16384
	ds_read_b128 v[174:177], v136 offset:17408
	ds_read_b128 v[178:181], v136 offset:18432
	ds_read_b128 v[182:185], v136 offset:19456
	ds_read_b128 v[186:189], v136 offset:20480
	ds_read_b128 v[190:193], v136 offset:21504
	ds_read_b128 v[194:197], v136 offset:22528
	ds_read_b128 v[198:201], v136 offset:23552
	s_waitcnt lgkmcnt(0)
	v_lshl_add_u64 v[202:203], s[78:79], 0, v[244:245]
	v_lshl_add_u64 v[206:207], s[78:79], 0, v[246:247]
	v_lshl_add_u64 v[212:213], s[56:57], 0, v[240:241]
	v_lshl_add_u64 v[214:215], s[56:57], 0, v[242:243]
	s_barrier
; #define G_STAGE(bufoff, gbase, voff) do { _Pragma("unroll") for (int _i = 0; _i < 2; ++_i) \
;         __builtin_amdgcn_global_load_lds((const unsigned*)((const char*)(gbase) + (voff)[_i]), (LAS unsigned*)(lds + (bufoff) + ldsw + _i * 8192), 16, 0, 0); } while (0)
; #define G_LDA(dst, b, h) do { _Pragma("unroll") for (int m = 0; m < 4; ++m) G_LD8(dst[m], lds + G_SA(b, h) + aoff + m * 2048); } while (0)
; #define G_LDB(dst, b, h) do { _Pragma("unroll") for (int n = 0; n < 2; ++n) G_LD8(dst[n], lds + G_SB(b, h) + boff + n * 2048); } while (0)
; #define G_WAIT_V(n) asm volatile("s_waitcnt vmcnt(" #n ")" ::: "memory")
; #define G_WAIT_L(n) asm volatile("s_waitcnt lgkmcnt(" #n ")" ::: "memory")
; #define G_BAR __builtin_amdgcn_s_barrier()
; #define G_SCHED __builtin_amdgcn_sched_barrier(0)
;     ...
;             G_WAIT_L(0); G_BAR; G_MMA(1, 0, At, B0); G_MMA(1, 1, At, B1); G_WAIT_V(8); G_BAR; G_SCHED;
;             G_LDB(B0, 1, 0); G_LDB(B1, 1, 1); G_SCHED; G_LDA(At, 1, 0); G_STAGE(G_SA(0, 1), a12, vA1);
;             G_WAIT_L(0); G_BAR; G_MMA(0, 0, At, B0); G_MMA(0, 1, At, B1); G_WAIT_V(8); G_BAR; G_SCHED;
	s_setprio 1
	s_waitcnt lgkmcnt(0)
	v_mfma_f32_16x16x32_bf16 v[60:63], v[138:141], v[170:173], v[60:63]
	v_mfma_f32_16x16x32_bf16 v[56:59], v[146:149], v[170:173], v[56:59]
	v_mfma_f32_16x16x32_bf16 v[44:47], v[138:141], v[178:181], v[44:47]
	v_mfma_f32_16x16x32_bf16 v[40:43], v[146:149], v[178:181], v[40:43]
	v_mfma_f32_16x16x32_bf16 v[28:31], v[138:141], v[186:189], v[28:31]
	v_mfma_f32_16x16x32_bf16 v[24:27], v[146:149], v[186:189], v[24:27]
	v_mfma_f32_16x16x32_bf16 v[12:15], v[138:141], v[194:197], v[12:15]
	v_mfma_f32_16x16x32_bf16 v[8:11], v[146:149], v[194:197], v[8:11]
	v_mfma_f32_16x16x32_bf16 v[60:63], v[142:145], v[174:177], v[60:63]
	v_mfma_f32_16x16x32_bf16 v[56:59], v[150:153], v[174:177], v[56:59]
	v_mfma_f32_16x16x32_bf16 v[44:47], v[142:145], v[182:185], v[44:47]
	v_mfma_f32_16x16x32_bf16 v[40:43], v[150:153], v[182:185], v[40:43]
	v_mfma_f32_16x16x32_bf16 v[28:31], v[142:145], v[190:193], v[28:31]
	v_mfma_f32_16x16x32_bf16 v[24:27], v[150:153], v[190:193], v[24:27]
	v_mfma_f32_16x16x32_bf16 v[12:15], v[142:145], v[198:201], v[12:15]
	v_mfma_f32_16x16x32_bf16 v[8:11], v[150:153], v[198:201], v[8:11]
	v_mfma_f32_16x16x32_bf16 v[52:55], v[154:157], v[170:173], v[52:55]
	v_mfma_f32_16x16x32_bf16 v[48:51], v[162:165], v[170:173], v[48:51]
	v_mfma_f32_16x16x32_bf16 v[36:39], v[154:157], v[178:181], v[36:39]
	v_mfma_f32_16x16x32_bf16 v[32:35], v[162:165], v[178:181], v[32:35]
	v_mfma_f32_16x16x32_bf16 v[20:23], v[154:157], v[186:189], v[20:23]
	v_mfma_f32_16x16x32_bf16 v[16:19], v[162:165], v[186:189], v[16:19]
	v_mfma_f32_16x16x32_bf16 v[4:7], v[154:157], v[194:197], v[4:7]
	v_mfma_f32_16x16x32_bf16 v[0:3], v[162:165], v[194:197], v[0:3]
	v_mfma_f32_16x16x32_bf16 v[52:55], v[158:161], v[174:177], v[52:55]
	v_mfma_f32_16x16x32_bf16 v[48:51], v[166:169], v[174:177], v[48:51]
	v_mfma_f32_16x16x32_bf16 v[36:39], v[158:161], v[182:185], v[36:39]
	v_mfma_f32_16x16x32_bf16 v[32:35], v[166:169], v[182:185], v[32:35]
	v_mfma_f32_16x16x32_bf16 v[20:23], v[158:161], v[190:193], v[20:23]
	v_mfma_f32_16x16x32_bf16 v[16:19], v[166:169], v[190:193], v[16:19]
	v_mfma_f32_16x16x32_bf16 v[4:7], v[158:161], v[198:201], v[4:7]
	v_mfma_f32_16x16x32_bf16 v[0:3], v[166:169], v[198:201], v[0:3]
	s_setprio 0
	s_waitcnt vmcnt(8)
	s_barrier
	s_add_i32 s56, 0, 0x18000
	s_add_i32 s57, 0, 0x1c000
	s_mov_b32 m0, s24
	s_nop 0
	global_load_lds_dwordx4 v240, s[54:55]
	s_mov_b32 m0, s25
	s_nop 0
	global_load_lds_dwordx4 v242, s[54:55]
	v_add_u32_e32 v137, s56, v133
	ds_read_b128 v[138:141], v137
	ds_read_b128 v[142:145], v137 offset:1024
	ds_read_b128 v[146:149], v137 offset:2048
	ds_read_b128 v[150:153], v137 offset:3072
	v_add_u32_e32 v137, s57, v133
	ds_read_b128 v[154:157], v137
	ds_read_b128 v[158:161], v137 offset:1024
	ds_read_b128 v[162:165], v137 offset:2048
	ds_read_b128 v[166:169], v137 offset:3072
	ds_read_b128 v[170:173], v136 offset:32768
	ds_read_b128 v[174:177], v136 offset:33792
	ds_read_b128 v[178:181], v136 offset:34816
	ds_read_b128 v[182:185], v136 offset:35840
	ds_read_b128 v[186:189], v136 offset:36864
	ds_read_b128 v[190:193], v136 offset:37888
	ds_read_b128 v[194:197], v136 offset:38912
	ds_read_b128 v[198:201], v136 offset:39936
	s_waitcnt lgkmcnt(0)
	s_barrier
	s_setprio 1
	s_waitcnt lgkmcnt(0)
	v_mfma_f32_16x16x32_bf16 v[124:127], v[138:141], v[170:173], v[124:127]
	v_mfma_f32_16x16x32_bf16 v[120:123], v[146:149], v[170:173], v[120:123]
	v_mfma_f32_16x16x32_bf16 v[108:111], v[138:141], v[178:181], v[108:111]
	v_mfma_f32_16x16x32_bf16 v[104:107], v[146:149], v[178:181], v[104:107]
	v_mfma_f32_16x16x32_bf16 v[92:95], v[138:141], v[186:189], v[92:95]
	v_mfma_f32_16x16x32_bf16 v[88:91], v[146:149], v[186:189], v[88:91]
	v_mfma_f32_16x16x32_bf16 v[76:79], v[138:141], v[194:197], v[76:79]
	v_mfma_f32_16x16x32_bf16 v[72:75], v[146:149], v[194:197], v[72:75]
	v_mfma_f32_16x16x32_bf16 v[124:127], v[142:145], v[174:177], v[124:127]
	v_mfma_f32_16x16x32_bf16 v[120:123], v[150:153], v[174:177], v[120:123]
	v_mfma_f32_16x16x32_bf16 v[108:111], v[142:145], v[182:185], v[108:111]
	v_mfma_f32_16x16x32_bf16 v[104:107], v[150:153], v[182:185], v[104:107]
	v_mfma_f32_16x16x32_bf16 v[92:95], v[142:145], v[190:193], v[92:95]
	v_mfma_f32_16x16x32_bf16 v[88:91], v[150:153], v[190:193], v[88:91]
	v_mfma_f32_16x16x32_bf16 v[76:79], v[142:145], v[198:201], v[76:79]
	v_mfma_f32_16x16x32_bf16 v[72:75], v[150:153], v[198:201], v[72:75]
	v_mfma_f32_16x16x32_bf16 v[116:119], v[154:157], v[170:173], v[116:119]
	v_mfma_f32_16x16x32_bf16 v[112:115], v[162:165], v[170:173], v[112:115]
	v_mfma_f32_16x16x32_bf16 v[100:103], v[154:157], v[178:181], v[100:103]
	v_mfma_f32_16x16x32_bf16 v[96:99], v[162:165], v[178:181], v[96:99]
	v_mfma_f32_16x16x32_bf16 v[84:87], v[154:157], v[186:189], v[84:87]
	v_mfma_f32_16x16x32_bf16 v[80:83], v[162:165], v[186:189], v[80:83]
	v_mfma_f32_16x16x32_bf16 v[68:71], v[154:157], v[194:197], v[68:71]
	v_mfma_f32_16x16x32_bf16 v[64:67], v[162:165], v[194:197], v[64:67]
	v_mfma_f32_16x16x32_bf16 v[116:119], v[158:161], v[174:177], v[116:119]
	v_mfma_f32_16x16x32_bf16 v[112:115], v[166:169], v[174:177], v[112:115]
	v_mfma_f32_16x16x32_bf16 v[100:103], v[158:161], v[182:185], v[100:103]
	v_mfma_f32_16x16x32_bf16 v[96:99], v[166:169], v[182:185], v[96:99]
	v_mfma_f32_16x16x32_bf16 v[84:87], v[158:161], v[190:193], v[84:87]
	v_mfma_f32_16x16x32_bf16 v[80:83], v[166:169], v[190:193], v[80:83]
	v_mfma_f32_16x16x32_bf16 v[68:71], v[158:161], v[198:201], v[68:71]
	v_mfma_f32_16x16x32_bf16 v[64:67], v[166:169], v[198:201], v[64:67]
	s_setprio 0
	s_waitcnt vmcnt(8)
	s_barrier
; #define G_STAGE(bufoff, gbase, voff) do { _Pragma("unroll") for (int _i = 0; _i < 2; ++_i) \
;         __builtin_amdgcn_global_load_lds((const unsigned*)((const char*)(gbase) + (voff)[_i]), (LAS unsigned*)(lds + (bufoff) + ldsw + _i * 8192), 16, 0, 0); } while (0)
; #define G_LDA(dst, b, h) do { _Pragma("unroll") for (int m = 0; m < 4; ++m) G_LD8(dst[m], lds + G_SA(b, h) + aoff + m * 2048); } while (0)
; #define G_WAIT_V(n) asm volatile("s_waitcnt vmcnt(" #n ")" ::: "memory")
; #define G_WAIT_L(n) asm volatile("s_waitcnt lgkmcnt(" #n ")" ::: "memory")
; #define G_BAR __builtin_amdgcn_s_barrier()
; #define G_SCHED __builtin_amdgcn_sched_barrier(0)
;     ...
;             G_LDA(At, 1, 1); G_STAGE(G_SB(1, 0), b02 + kstep, voffB); G_STAGE(G_SB(1, 1), b12 + kstep, voffB); G_STAGE(G_SA(1, 0), a02 + kstep, vA0);
;             G_WAIT_L(0); G_BAR; G_MMA(1, 0, At, B0); G_MMA(1, 1, At, B1); G_WAIT_V(8); G_BAR; G_SCHED;
;         }
	s_add_i32 s54, s56, s20
	v_lshl_add_u64 v[204:205], v[208:209], 0, s[36:37]
	s_mov_b32 m0, s54
	s_nop 0
	global_load_lds_dwordx4 v[204:205], off
	v_lshl_add_u64 v[204:205], v[210:211], 0, s[36:37]
	s_add_i32 m0, s54, 0x2000
	s_add_i32 s54, s57, s20
	global_load_lds_dwordx4 v[204:205], off
	v_lshl_add_u64 v[202:203], v[202:203], 0, s[36:37]
	s_mov_b32 m0, s54
	s_nop 0
	global_load_lds_dwordx4 v[202:203], off
	v_lshl_add_u64 v[202:203], v[206:207], 0, s[36:37]
	s_add_i32 m0, s54, 0x2000
	s_nop 0
	global_load_lds_dwordx4 v[202:203], off
	v_lshl_add_u64 v[202:203], v[212:213], 0, s[36:37]
	s_mov_b32 m0, s65
	s_nop 0
	global_load_lds_dwordx4 v[202:203], off
	v_lshl_add_u64 v[202:203], v[214:215], 0, s[36:37]
	s_mov_b32 m0, s66
	s_nop 0
	global_load_lds_dwordx4 v[202:203], off
	ds_read_b128 v[170:173], v136 offset:49152
	ds_read_b128 v[174:177], v136 offset:50176
	ds_read_b128 v[178:181], v136 offset:51200
	ds_read_b128 v[182:185], v136 offset:52224
	ds_read_b128 v[186:189], v136 offset:53248
	ds_read_b128 v[190:193], v136 offset:54272
	ds_read_b128 v[194:197], v136 offset:55296
	ds_read_b128 v[198:201], v136 offset:56320
	s_waitcnt lgkmcnt(0)
	s_barrier
	s_setprio 1
	s_waitcnt lgkmcnt(0)
	v_mfma_f32_16x16x32_bf16 v[60:63], v[138:141], v[170:173], v[60:63]
	v_mfma_f32_16x16x32_bf16 v[56:59], v[146:149], v[170:173], v[56:59]
	v_mfma_f32_16x16x32_bf16 v[44:47], v[138:141], v[178:181], v[44:47]
	v_mfma_f32_16x16x32_bf16 v[40:43], v[146:149], v[178:181], v[40:43]
	v_mfma_f32_16x16x32_bf16 v[28:31], v[138:141], v[186:189], v[28:31]
	v_mfma_f32_16x16x32_bf16 v[24:27], v[146:149], v[186:189], v[24:27]
	v_mfma_f32_16x16x32_bf16 v[12:15], v[138:141], v[194:197], v[12:15]
	v_mfma_f32_16x16x32_bf16 v[8:11], v[146:149], v[194:197], v[8:11]
	v_mfma_f32_16x16x32_bf16 v[60:63], v[142:145], v[174:177], v[60:63]
	v_mfma_f32_16x16x32_bf16 v[56:59], v[150:153], v[174:177], v[56:59]
	v_mfma_f32_16x16x32_bf16 v[44:47], v[142:145], v[182:185], v[44:47]
	v_mfma_f32_16x16x32_bf16 v[40:43], v[150:153], v[182:185], v[40:43]
	v_mfma_f32_16x16x32_bf16 v[28:31], v[142:145], v[190:193], v[28:31]
	v_mfma_f32_16x16x32_bf16 v[24:27], v[150:153], v[190:193], v[24:27]
	v_mfma_f32_16x16x32_bf16 v[12:15], v[142:145], v[198:201], v[12:15]
	v_mfma_f32_16x16x32_bf16 v[8:11], v[150:153], v[198:201], v[8:11]
	v_mfma_f32_16x16x32_bf16 v[52:55], v[154:157], v[170:173], v[52:55]
	v_mfma_f32_16x16x32_bf16 v[48:51], v[162:165], v[170:173], v[48:51]
	v_mfma_f32_16x16x32_bf16 v[36:39], v[154:157], v[178:181], v[36:39]
	v_mfma_f32_16x16x32_bf16 v[32:35], v[162:165], v[178:181], v[32:35]
	v_mfma_f32_16x16x32_bf16 v[20:23], v[154:157], v[186:189], v[20:23]
	v_mfma_f32_16x16x32_bf16 v[16:19], v[162:165], v[186:189], v[16:19]
	v_mfma_f32_16x16x32_bf16 v[4:7], v[154:157], v[194:197], v[4:7]
	v_mfma_f32_16x16x32_bf16 v[0:3], v[162:165], v[194:197], v[0:3]
	v_mfma_f32_16x16x32_bf16 v[52:55], v[158:161], v[174:177], v[52:55]
	v_mfma_f32_16x16x32_bf16 v[48:51], v[166:169], v[174:177], v[48:51]
	v_mfma_f32_16x16x32_bf16 v[36:39], v[158:161], v[182:185], v[36:39]
	v_mfma_f32_16x16x32_bf16 v[32:35], v[166:169], v[182:185], v[32:35]
	v_mfma_f32_16x16x32_bf16 v[20:23], v[158:161], v[190:193], v[20:23]
	v_mfma_f32_16x16x32_bf16 v[16:19], v[166:169], v[190:193], v[16:19]
	v_mfma_f32_16x16x32_bf16 v[4:7], v[158:161], v[198:201], v[4:7]
	v_mfma_f32_16x16x32_bf16 v[0:3], v[166:169], v[198:201], v[0:3]
	s_setprio 0
	s_waitcnt vmcnt(8)
	s_barrier
	s_add_u32 s60, s60, 0x100
	s_addc_u32 s61, s61, 0
	s_add_u32 s62, s62, 0x100
	s_addc_u32 s71, s71, 0
	s_add_u32 s72, s72, 0x100
	s_addc_u32 s73, s73, 0
	s_add_u32 s52, s52, 0x100
	s_addc_u32 s53, s53, 0
	s_cmp_ge_i32 s74, s0
	s_mov_b32 s54, s74
	s_cbranch_scc0 .LBB0_812
	v_readlane_b32 s78, v255, 11
	v_readlane_b32 s79, v255, 13
	s_and_b64 vcc, exec, s[40:41]
	s_cbranch_vccz .LBB0_815

; #define G_STAGE(bufoff, gbase, voff) do { _Pragma("unroll") for (int _i = 0; _i < 2; ++_i) \
;         __builtin_amdgcn_global_load_lds((const unsigned*)((const char*)(gbase) + (voff)[_i]), (LAS unsigned*)(lds + (bufoff) + ldsw + _i * 8192), 16, 0, 0); } while (0)
; #define G_LDA(dst, b, h) do { _Pragma("unroll") for (int m = 0; m < 4; ++m) G_LD8(dst[m], lds + G_SA(b, h) + aoff + m * 2048); } while (0)
; #define G_LDB(dst, b, h) do { _Pragma("unroll") for (int n = 0; n < 2; ++n) G_LD8(dst[n], lds + G_SB(b, h) + boff + n * 2048); } while (0)
; #define G_WAIT_V(n) asm volatile("s_waitcnt vmcnt(" #n ")" ::: "memory")
; #define G_WAIT_L(n) asm volatile("s_waitcnt lgkmcnt(" #n ")" ::: "memory")
; #define G_BAR __builtin_amdgcn_s_barrier()
; #define G_SCHED __builtin_amdgcn_sched_barrier(0)
;     __device__ __forceinline__ unsigned row_off(const Unit& u, int r, LAS unsigned char* lds) const { return (unsigned)((const LAS int*)(lds + LDS_STAGE + u.q * 4096))[r] * (unsigned)rowbytes; }
;     ...
;             const char* a11 = cur.a1 + (size_t)(t + 1) * kstep;
;             const char* a02 = last ? nxt.a0 : cur.a0 + (size_t)(t + 2) * kstep; const char* a12 = last ? nxt.a1 : cur.a1 + (size_t)(t + 2) * kstep;
;             const char* b02 = last ? nxt.b0 : cur.b0 + (size_t)(t + 2) * kstep; const char* b12 = last ? nxt.b1 : cur.b1 + (size_t)(t + 2) * kstep;
;             G_LDB(B0, 0, 0); G_LDB(B1, 0, 1); G_SCHED; G_LDA(At, 0, 0); G_STAGE(G_SA(1, 1), a11, vA1);
;             if constexpr (GATHER) { if (last) { int tz = tid; asm volatile("" : "+v"(tz));
; #pragma unroll
;                 for (int i = 0; i < 2; ++i) { int R, C; stage_rc(tz * 16 + i * 8192, R, C); gc0[i] = S.row_off(nxt, R, lds) + (unsigned)C * 2u; gc1[i] = S.row_off(nxt, 128 + R, lds) + (unsigned)C * 2u; } } }
;             G_WAIT_L(0); G_BAR; G_MMA(0, 0, At, B0); G_MMA(0, 1, At, B1); G_WAIT_V(8); G_BAR; G_SCHED;
;             G_LDA(At, 0, 1); G_STAGE(G_SB(0, 0), b02, voffB); G_STAGE(G_SB(0, 1), b12, voffB); G_STAGE(G_SA(0, 0), a02, vA0);
;             G_WAIT_L(0); G_BAR; G_MMA(1, 0, At, B0); G_MMA(1, 1, At, B1); G_WAIT_V(8); G_BAR; G_SCHED;
;             G_LDB(B0, 1, 0); G_LDB(B1, 1, 1); G_SCHED; G_LDA(At, 1, 0); G_STAGE(G_SA(0, 1), a12, vA1);
.LBB0_1023:
	s_add_i32 s78, s54, 2
	s_add_u32 s79, s52, 0x80
	s_addc_u32 s55, s53, 0
	s_add_i32 s81, s73, s20
	s_add_i32 m0, s23, 0xc000
	s_add_i32 s80, s23, 0xe000
	s_add_i32 s82, s81, 0x2000
	s_cmp_eq_u32 s72, s54
	s_cselect_b32 s54, s44, s79
	s_cselect_b32 s57, s43, s77
	s_cselect_b32 s56, s42, s75
	s_cselect_b32 s59, s49, s61
	s_cselect_b32 s58, s48, s60
	s_cselect_b32 s55, s45, s55
	global_load_lds_dwordx4 v240, s[52:53]
	s_mov_b32 m0, s80
	v_mov_b32_e32 v123, v65
	global_load_lds_dwordx4 v242, s[52:53]
	ds_read_b128 v[72:75], v70
	ds_read_b128 v[76:79], v70 offset:1024
	ds_read_b128 v[80:83], v70 offset:2048
	ds_read_b128 v[84:87], v70 offset:3072
	ds_read_b128 v[88:91], v71
	ds_read_b128 v[92:95], v71 offset:1024
	ds_read_b128 v[96:99], v71 offset:2048
	ds_read_b128 v[100:103], v71 offset:3072
	ds_read_b128 v[104:107], v71 offset:4096
	ds_read_b128 v[108:111], v71 offset:5120
	ds_read_b128 v[112:115], v71 offset:6144
	ds_read_b128 v[116:119], v71 offset:7168
	s_waitcnt lgkmcnt(0)
	s_barrier
	s_setprio 1
	s_waitcnt lgkmcnt(0)
	v_mfma_f32_16x16x32_bf16 v[60:63], v[72:75], v[88:91], v[60:63]
	v_mfma_f32_16x16x32_bf16 v[56:59], v[80:83], v[88:91], v[56:59]
	v_mfma_f32_16x16x32_bf16 v[52:55], v[72:75], v[96:99], v[52:55]
	v_mfma_f32_16x16x32_bf16 v[48:51], v[80:83], v[96:99], v[48:51]
	v_mfma_f32_16x16x32_bf16 v[44:47], v[72:75], v[104:107], v[44:47]
	v_mfma_f32_16x16x32_bf16 v[40:43], v[80:83], v[104:107], v[40:43]
	v_mfma_f32_16x16x32_bf16 v[36:39], v[72:75], v[112:115], v[36:39]
	v_mfma_f32_16x16x32_bf16 v[32:35], v[80:83], v[112:115], v[32:35]
	v_mfma_f32_16x16x32_bf16 v[60:63], v[76:79], v[92:95], v[60:63]
	v_mfma_f32_16x16x32_bf16 v[56:59], v[84:87], v[92:95], v[56:59]
	v_mfma_f32_16x16x32_bf16 v[52:55], v[76:79], v[100:103], v[52:55]
	v_mfma_f32_16x16x32_bf16 v[48:51], v[84:87], v[100:103], v[48:51]
	v_mfma_f32_16x16x32_bf16 v[44:47], v[76:79], v[108:111], v[44:47]
	v_mfma_f32_16x16x32_bf16 v[40:43], v[84:87], v[108:111], v[40:43]
	v_mfma_f32_16x16x32_bf16 v[36:39], v[76:79], v[116:119], v[36:39]
	v_mfma_f32_16x16x32_bf16 v[32:35], v[84:87], v[116:119], v[32:35]
	s_setprio 0
	s_waitcnt vmcnt(8)
	s_barrier
	s_mov_b32 m0, s81
	s_nop 0
	global_load_lds_dwordx4 v244, s[58:59]
	s_mov_b32 m0, s82
	s_cselect_b32 s81, s47, s74
	global_load_lds_dwordx4 v246, s[58:59]
	s_cselect_b32 s80, s46, s62
	s_mov_b32 m0, s24
	v_mov_b32_e32 v121, v65
	global_load_lds_dwordx4 v244, s[80:81]
	s_mov_b32 m0, s25
	v_mov_b32_e32 v125, v65
	global_load_lds_dwordx4 v246, s[80:81]
	s_mov_b32 m0, s23
	v_lshl_add_u64 v[126:127], s[58:59], 0, v[244:245]
	global_load_lds_dwordx4 v240, s[56:57]
	s_mov_b32 m0, s27
	v_lshl_add_u64 v[128:129], s[58:59], 0, v[246:247]
	global_load_lds_dwordx4 v242, s[56:57]
	ds_read_b128 v[88:91], v71 offset:16384
	ds_read_b128 v[92:95], v71 offset:17408
	ds_read_b128 v[96:99], v71 offset:18432
	ds_read_b128 v[100:103], v71 offset:19456
	ds_read_b128 v[104:107], v71 offset:20480
	ds_read_b128 v[108:111], v71 offset:21504
	ds_read_b128 v[112:115], v71 offset:22528
	ds_read_b128 v[116:119], v71 offset:23552
	s_waitcnt lgkmcnt(0)
	v_lshl_add_u64 v[120:121], s[80:81], 0, v[244:245]
	v_lshl_add_u64 v[124:125], s[80:81], 0, v[246:247]
	v_lshl_add_u64 v[130:131], s[56:57], 0, v[240:241]
	v_lshl_add_u64 v[132:133], s[56:57], 0, v[242:243]
	s_barrier
	s_setprio 1
	s_waitcnt lgkmcnt(0)
	v_mfma_f32_16x16x32_bf16 v[28:31], v[72:75], v[88:91], v[28:31]
	v_mfma_f32_16x16x32_bf16 v[24:27], v[80:83], v[88:91], v[24:27]
	v_mfma_f32_16x16x32_bf16 v[20:23], v[72:75], v[96:99], v[20:23]
	v_mfma_f32_16x16x32_bf16 v[16:19], v[80:83], v[96:99], v[16:19]
	v_mfma_f32_16x16x32_bf16 v[12:15], v[72:75], v[104:107], v[12:15]
	v_mfma_f32_16x16x32_bf16 v[8:11], v[80:83], v[104:107], v[8:11]
	v_mfma_f32_16x16x32_bf16 v[4:7], v[72:75], v[112:115], v[4:7]
	v_mfma_f32_16x16x32_bf16 v[0:3], v[80:83], v[112:115], v[0:3]
	v_mfma_f32_16x16x32_bf16 v[28:31], v[76:79], v[92:95], v[28:31]
	v_mfma_f32_16x16x32_bf16 v[24:27], v[84:87], v[92:95], v[24:27]
	v_mfma_f32_16x16x32_bf16 v[20:23], v[76:79], v[100:103], v[20:23]
	v_mfma_f32_16x16x32_bf16 v[16:19], v[84:87], v[100:103], v[16:19]
	v_mfma_f32_16x16x32_bf16 v[12:15], v[76:79], v[108:111], v[12:15]
	v_mfma_f32_16x16x32_bf16 v[8:11], v[84:87], v[108:111], v[8:11]
	v_mfma_f32_16x16x32_bf16 v[4:7], v[76:79], v[116:119], v[4:7]
	v_mfma_f32_16x16x32_bf16 v[0:3], v[84:87], v[116:119], v[0:3]
	s_setprio 0
	s_waitcnt vmcnt(8)
	s_barrier
	s_add_i32 s56, 0, 0x18000
	s_mov_b32 m0, s33
	s_nop 0
	global_load_lds_dwordx4 v240, s[54:55]
	s_mov_b32 m0, s41
	s_nop 0
	global_load_lds_dwordx4 v242, s[54:55]
	v_add_u32_e32 v84, s56, v69
	ds_read_b128 v[72:75], v84
	ds_read_b128 v[76:79], v84 offset:1024
	ds_read_b128 v[80:83], v84 offset:2048
	ds_read_b128 v[84:87], v84 offset:3072
	ds_read_b128 v[88:91], v71 offset:32768
	ds_read_b128 v[92:95], v71 offset:33792
	ds_read_b128 v[96:99], v71 offset:34816
	ds_read_b128 v[100:103], v71 offset:35840
	ds_read_b128 v[104:107], v71 offset:36864
	ds_read_b128 v[108:111], v71 offset:37888
	ds_read_b128 v[112:115], v71 offset:38912
	ds_read_b128 v[116:119], v71 offset:39936
	s_waitcnt lgkmcnt(0)
	s_barrier
; #define GAS __attribute__((address_space(1)))
; __device__ __forceinline__ v4u pack8(const f32x4 a, const f32x4 b) { v4u w; w.x = cvt_pk_bf16(a[0], a[1]); w.y = cvt_pk_bf16(a[2], a[3]); w.z = cvt_pk_bf16(b[0], b[1]); w.w = cvt_pk_bf16(b[2], b[3]); return w; }
; #define G_STAGE(bufoff, gbase, voff) do { _Pragma("unroll") for (int _i = 0; _i < 2; ++_i) \
;         __builtin_amdgcn_global_load_lds((const unsigned*)((const char*)(gbase) + (voff)[_i]), (LAS unsigned*)(lds + (bufoff) + ldsw + _i * 8192), 16, 0, 0); } while (0)
; #define G_LDA(dst, b, h) do { _Pragma("unroll") for (int m = 0; m < 4; ++m) G_LD8(dst[m], lds + G_SA(b, h) + aoff + m * 2048); } while (0)
; #define G_WAIT_V(n) asm volatile("s_waitcnt vmcnt(" #n ")" ::: "memory")
; #define G_WAIT_L(n) asm volatile("s_waitcnt lgkmcnt(" #n ")" ::: "memory")
; #define G_BAR __builtin_amdgcn_s_barrier()
; #define G_SCHED __builtin_amdgcn_sched_barrier(0)
; #define EPI_LOOP_AM for (int ai = 0; ai < 2; ++ai) _Pragma("unroll") for (int m = 0; m < 4; ++m)
;     ...
;             G_WAIT_L(0); G_BAR; G_MMA(0, 0, At, B0); G_MMA(0, 1, At, B1); G_WAIT_V(8); G_BAR; G_SCHED;
;             G_LDA(At, 1, 1); G_STAGE(G_SB(1, 0), b02 + kstep, voffB); G_STAGE(G_SB(1, 1), b12 + kstep, voffB); G_STAGE(G_SA(1, 0), a02 + kstep, vA0);
;             G_WAIT_L(0); G_BAR; G_MMA(1, 0, At, B0); G_MMA(1, 1, At, B1); G_WAIT_V(8); G_BAR; G_SCHED;
;         }
;     __device__ __forceinline__ void operator()(Acc& acc, const Unit& u, LAS unsigned char*, int wr, int wc, int fr, int fq) const {
;         const int l0 = wc * 32 + 8 * fq; const float norm = 6.9053396600248786e-4f;
; #pragma unroll
;         EPI_LOOP_AM { const int R = u.p0 * 256 + 128 * ai + 64 * wr + 16 * m + fr, k = R >> 3, g = R & 7;
;             *(GAS v4u*)(y + (size_t)k * D + g * 128 + l0) = pack8(acc[ai][0][m][0] * norm, acc[ai][0][m][1] * norm); }
	s_setprio 1
	s_waitcnt lgkmcnt(0)
	v_mfma_f32_16x16x32_bf16 v[60:63], v[72:75], v[88:91], v[60:63]
	v_mfma_f32_16x16x32_bf16 v[56:59], v[80:83], v[88:91], v[56:59]
	v_mfma_f32_16x16x32_bf16 v[52:55], v[72:75], v[96:99], v[52:55]
	v_mfma_f32_16x16x32_bf16 v[48:51], v[80:83], v[96:99], v[48:51]
	v_mfma_f32_16x16x32_bf16 v[44:47], v[72:75], v[104:107], v[44:47]
	v_mfma_f32_16x16x32_bf16 v[40:43], v[80:83], v[104:107], v[40:43]
	v_mfma_f32_16x16x32_bf16 v[36:39], v[72:75], v[112:115], v[36:39]
	v_mfma_f32_16x16x32_bf16 v[32:35], v[80:83], v[112:115], v[32:35]
	v_mfma_f32_16x16x32_bf16 v[60:63], v[76:79], v[92:95], v[60:63]
	v_mfma_f32_16x16x32_bf16 v[56:59], v[84:87], v[92:95], v[56:59]
	v_mfma_f32_16x16x32_bf16 v[52:55], v[76:79], v[100:103], v[52:55]
	v_mfma_f32_16x16x32_bf16 v[48:51], v[84:87], v[100:103], v[48:51]
	v_mfma_f32_16x16x32_bf16 v[44:47], v[76:79], v[108:111], v[44:47]
	v_mfma_f32_16x16x32_bf16 v[40:43], v[84:87], v[108:111], v[40:43]
	v_mfma_f32_16x16x32_bf16 v[36:39], v[76:79], v[116:119], v[36:39]
	v_mfma_f32_16x16x32_bf16 v[32:35], v[84:87], v[116:119], v[32:35]
	s_setprio 0
	s_waitcnt vmcnt(8)
	s_barrier
	s_add_i32 s54, s56, s20
	v_lshl_add_u64 v[122:123], v[126:127], 0, s[36:37]
	s_mov_b32 m0, s54
	s_nop 0
	global_load_lds_dwordx4 v[122:123], off
	v_lshl_add_u64 v[122:123], v[128:129], 0, s[36:37]
	s_add_i32 m0, s54, 0x2000
	v_lshl_add_u64 v[120:121], v[120:121], 0, s[36:37]
	global_load_lds_dwordx4 v[122:123], off
	s_mov_b32 m0, s69
	s_nop 0
	global_load_lds_dwordx4 v[120:121], off
	v_lshl_add_u64 v[120:121], v[124:125], 0, s[36:37]
	s_mov_b32 m0, s71
	s_nop 0
	global_load_lds_dwordx4 v[120:121], off
	v_lshl_add_u64 v[120:121], v[130:131], 0, s[36:37]
	s_mov_b32 m0, s66
	s_nop 0
	global_load_lds_dwordx4 v[120:121], off
	v_lshl_add_u64 v[120:121], v[132:133], 0, s[36:37]
	s_mov_b32 m0, s67
	s_nop 0
	global_load_lds_dwordx4 v[120:121], off
	ds_read_b128 v[88:91], v71 offset:49152
	ds_read_b128 v[92:95], v71 offset:50176
	ds_read_b128 v[96:99], v71 offset:51200
	ds_read_b128 v[100:103], v71 offset:52224
	ds_read_b128 v[104:107], v71 offset:53248
	ds_read_b128 v[108:111], v71 offset:54272
	ds_read_b128 v[112:115], v71 offset:55296
	ds_read_b128 v[116:119], v71 offset:56320
	s_waitcnt lgkmcnt(0)
	s_barrier
	s_setprio 1
	s_waitcnt lgkmcnt(0)
	v_mfma_f32_16x16x32_bf16 v[28:31], v[72:75], v[88:91], v[28:31]
	v_mfma_f32_16x16x32_bf16 v[24:27], v[80:83], v[88:91], v[24:27]
	v_mfma_f32_16x16x32_bf16 v[20:23], v[72:75], v[96:99], v[20:23]
	v_mfma_f32_16x16x32_bf16 v[16:19], v[80:83], v[96:99], v[16:19]
	v_mfma_f32_16x16x32_bf16 v[12:15], v[72:75], v[104:107], v[12:15]
	v_mfma_f32_16x16x32_bf16 v[8:11], v[80:83], v[104:107], v[8:11]
	v_mfma_f32_16x16x32_bf16 v[4:7], v[72:75], v[112:115], v[4:7]
	v_mfma_f32_16x16x32_bf16 v[0:3], v[80:83], v[112:115], v[0:3]
	v_mfma_f32_16x16x32_bf16 v[28:31], v[76:79], v[92:95], v[28:31]
	v_mfma_f32_16x16x32_bf16 v[24:27], v[84:87], v[92:95], v[24:27]
	v_mfma_f32_16x16x32_bf16 v[20:23], v[76:79], v[100:103], v[20:23]
	v_mfma_f32_16x16x32_bf16 v[16:19], v[84:87], v[100:103], v[16:19]
	v_mfma_f32_16x16x32_bf16 v[12:15], v[76:79], v[108:111], v[12:15]
	v_mfma_f32_16x16x32_bf16 v[8:11], v[84:87], v[108:111], v[8:11]
	v_mfma_f32_16x16x32_bf16 v[4:7], v[76:79], v[116:119], v[4:7]
	v_mfma_f32_16x16x32_bf16 v[0:3], v[84:87], v[116:119], v[0:3]
	s_setprio 0
	s_waitcnt vmcnt(8)
	s_barrier
	s_add_u32 s60, s60, 0x100
	s_addc_u32 s61, s61, 0
	s_add_u32 s62, s62, 0x100
	s_addc_u32 s74, s74, 0
	s_add_u32 s75, s75, 0x100
	s_addc_u32 s77, s77, 0
	s_add_u32 s52, s52, 0x100
	s_addc_u32 s53, s53, 0
	s_cmp_ge_i32 s78, s0
	s_mov_b32 s54, s78
	s_cbranch_scc0 .LBB0_1023
	v_pk_mul_f32 v[62:63], v[62:63], s[40:41] op_sel_hi:[1,0]
	v_pk_mul_f32 v[60:61], v[60:61], s[40:41] op_sel_hi:[1,0]
	v_pk_mul_f32 v[58:59], v[58:59], s[40:41] op_sel_hi:[1,0]
	v_pk_mul_f32 v[56:57], v[56:57], s[40:41] op_sel_hi:[1,0]
	v_pk_mul_f32 v[54:55], v[54:55], s[40:41] op_sel_hi:[1,0]
	v_pk_mul_f32 v[52:53], v[52:53], s[40:41] op_sel_hi:[1,0]
	v_pk_mul_f32 v[50:51], v[50:51], s[40:41] op_sel_hi:[1,0]
	v_pk_mul_f32 v[48:49], v[48:49], s[40:41] op_sel_hi:[1,0]
	v_pk_mul_f32 v[46:47], v[46:47], s[40:41] op_sel_hi:[1,0]
	v_pk_mul_f32 v[44:45], v[44:45], s[40:41] op_sel_hi:[1,0]
	v_pk_mul_f32 v[42:43], v[42:43], s[40:41] op_sel_hi:[1,0]
	v_pk_mul_f32 v[40:41], v[40:41], s[40:41] op_sel_hi:[1,0]
	v_pk_mul_f32 v[38:39], v[38:39], s[40:41] op_sel_hi:[1,0]
	v_pk_mul_f32 v[36:37], v[36:37], s[40:41] op_sel_hi:[1,0]
	v_pk_mul_f32 v[34:35], v[34:35], s[40:41] op_sel_hi:[1,0]
	v_pk_mul_f32 v[32:33], v[32:33], s[40:41] op_sel_hi:[1,0]
	v_pk_mul_f32 v[30:31], v[30:31], s[40:41] op_sel_hi:[1,0]
	v_pk_mul_f32 v[28:29], v[28:29], s[40:41] op_sel_hi:[1,0]
	v_pk_mul_f32 v[26:27], v[26:27], s[40:41] op_sel_hi:[1,0]
	v_pk_mul_f32 v[24:25], v[24:25], s[40:41] op_sel_hi:[1,0]
	v_pk_mul_f32 v[22:23], v[22:23], s[40:41] op_sel_hi:[1,0]
	v_pk_mul_f32 v[20:21], v[20:21], s[40:41] op_sel_hi:[1,0]
	v_pk_mul_f32 v[18:19], v[18:19], s[40:41] op_sel_hi:[1,0]
	v_pk_mul_f32 v[16:17], v[16:17], s[40:41] op_sel_hi:[1,0]
	v_pk_mul_f32 v[14:15], v[14:15], s[40:41] op_sel_hi:[1,0]
	v_pk_mul_f32 v[12:13], v[12:13], s[40:41] op_sel_hi:[1,0]
	v_pk_mul_f32 v[10:11], v[10:11], s[40:41] op_sel_hi:[1,0]
	v_pk_mul_f32 v[8:9], v[8:9], s[40:41] op_sel_hi:[1,0]
	v_pk_mul_f32 v[6:7], v[6:7], s[40:41] op_sel_hi:[1,0]
	v_pk_mul_f32 v[4:5], v[4:5], s[40:41] op_sel_hi:[1,0]
	v_pk_mul_f32 v[2:3], v[2:3], s[40:41] op_sel_hi:[1,0]
	v_pk_mul_f32 v[0:1], v[0:1], s[40:41] op_sel_hi:[1,0]
	v_readlane_b32 s78, v255, 11
	v_readlane_b32 s79, v255, 13
	s_and_b64 vcc, exec, s[38:39]
	s_cbranch_vccz .LBB0_1026

; #define G_STAGE(bufoff, gbase, voff) do { _Pragma("unroll") for (int _i = 0; _i < 2; ++_i) \
;         __builtin_amdgcn_global_load_lds((const unsigned*)((const char*)(gbase) + (voff)[_i]), (LAS unsigned*)(lds + (bufoff) + ldsw + _i * 8192), 16, 0, 0); } while (0)
; #define G_LDA(dst, b, h) do { _Pragma("unroll") for (int m = 0; m < 4; ++m) G_LD8(dst[m], lds + G_SA(b, h) + aoff + m * 2048); } while (0)
; #define G_LDB(dst, b, h) do { _Pragma("unroll") for (int n = 0; n < 2; ++n) G_LD8(dst[n], lds + G_SB(b, h) + boff + n * 2048); } while (0)
; #define G_WAIT_V(n) asm volatile("s_waitcnt vmcnt(" #n ")" ::: "memory")
; #define G_WAIT_L(n) asm volatile("s_waitcnt lgkmcnt(" #n ")" ::: "memory")
; #define G_BAR __builtin_amdgcn_s_barrier()
; #define G_SCHED __builtin_amdgcn_sched_barrier(0)
;     __device__ __forceinline__ unsigned row_off(const Unit& u, int r, LAS unsigned char* lds) const { return (unsigned)((const LAS int*)(lds + LDS_STAGE + u.q * 4096))[r] * (unsigned)rowbytes; }
;     ...
;             const char* a11 = cur.a1 + (size_t)(t + 1) * kstep;
;             const char* a02 = last ? nxt.a0 : cur.a0 + (size_t)(t + 2) * kstep; const char* a12 = last ? nxt.a1 : cur.a1 + (size_t)(t + 2) * kstep;
;             const char* b02 = last ? nxt.b0 : cur.b0 + (size_t)(t + 2) * kstep; const char* b12 = last ? nxt.b1 : cur.b1 + (size_t)(t + 2) * kstep;
;             G_LDB(B0, 0, 0); G_LDB(B1, 0, 1); G_SCHED; G_LDA(At, 0, 0); G_STAGE(G_SA(1, 1), a11, vA1);
;             if constexpr (GATHER) { if (last) { int tz = tid; asm volatile("" : "+v"(tz));
; #pragma unroll
;                 for (int i = 0; i < 2; ++i) { int R, C; stage_rc(tz * 16 + i * 8192, R, C); gc0[i] = S.row_off(nxt, R, lds) + (unsigned)C * 2u; gc1[i] = S.row_off(nxt, 128 + R, lds) + (unsigned)C * 2u; } } }
;             G_WAIT_L(0); G_BAR; G_MMA(0, 0, At, B0); G_MMA(0, 1, At, B1); G_WAIT_V(8); G_BAR; G_SCHED;
;             G_LDA(At, 0, 1); G_STAGE(G_SB(0, 0), b02, voffB); G_STAGE(G_SB(0, 1), b12, voffB); G_STAGE(G_SA(0, 0), a02, vA0);
.LBB0_1058:
	s_add_i32 s79, s54, 2
	s_add_u32 s80, s52, 0x80
	s_addc_u32 s55, s53, 0
	s_add_i32 s83, s71, s20
	s_add_i32 m0, s33, 0xc000
	s_add_i32 s82, s33, 0xe000
	s_add_i32 s84, s83, 0x2000
	s_cmp_eq_u32 s69, s54
	s_cselect_b32 s54, s44, s80
	s_cselect_b32 s57, s43, s78
	s_cselect_b32 s56, s42, s77
	s_cselect_b32 s59, s47, s41
	s_cselect_b32 s58, s46, s5
	s_cselect_b32 s55, s45, s55
	global_load_lds_dwordx4 v240, s[52:53]
	s_mov_b32 m0, s82
	v_mov_b32_e32 v207, v129
	global_load_lds_dwordx4 v242, s[52:53]
	ds_read_b128 v[130:133], v138
	ds_read_b128 v[144:147], v138 offset:1024
	ds_read_b128 v[148:151], v138 offset:2048
	ds_read_b128 v[152:155], v138 offset:3072
	ds_read_b128 v[156:159], v139
	ds_read_b128 v[160:163], v139 offset:1024
	ds_read_b128 v[164:167], v139 offset:2048
	ds_read_b128 v[168:171], v139 offset:3072
	ds_read_b128 v[172:175], v140
	ds_read_b128 v[176:179], v140 offset:1024
	ds_read_b128 v[180:183], v140 offset:2048
	ds_read_b128 v[184:187], v140 offset:3072
	ds_read_b128 v[188:191], v140 offset:4096
	ds_read_b128 v[192:195], v140 offset:5120
	ds_read_b128 v[196:199], v140 offset:6144
	ds_read_b128 v[200:203], v140 offset:7168
	s_waitcnt lgkmcnt(0)
	s_barrier
	s_setprio 1
	s_waitcnt lgkmcnt(0)
	v_mfma_f32_16x16x32_bf16 v[124:127], v[130:133], v[172:175], v[124:127]
	v_mfma_f32_16x16x32_bf16 v[120:123], v[148:151], v[172:175], v[120:123]
	v_mfma_f32_16x16x32_bf16 v[108:111], v[130:133], v[180:183], v[108:111]
	v_mfma_f32_16x16x32_bf16 v[104:107], v[148:151], v[180:183], v[104:107]
	v_mfma_f32_16x16x32_bf16 v[92:95], v[130:133], v[188:191], v[92:95]
	v_mfma_f32_16x16x32_bf16 v[88:91], v[148:151], v[188:191], v[88:91]
	v_mfma_f32_16x16x32_bf16 v[76:79], v[130:133], v[196:199], v[76:79]
	v_mfma_f32_16x16x32_bf16 v[72:75], v[148:151], v[196:199], v[72:75]
	v_mfma_f32_16x16x32_bf16 v[124:127], v[144:147], v[176:179], v[124:127]
	v_mfma_f32_16x16x32_bf16 v[120:123], v[152:155], v[176:179], v[120:123]
	v_mfma_f32_16x16x32_bf16 v[108:111], v[144:147], v[184:187], v[108:111]
	v_mfma_f32_16x16x32_bf16 v[104:107], v[152:155], v[184:187], v[104:107]
	v_mfma_f32_16x16x32_bf16 v[92:95], v[144:147], v[192:195], v[92:95]
	v_mfma_f32_16x16x32_bf16 v[88:91], v[152:155], v[192:195], v[88:91]
	v_mfma_f32_16x16x32_bf16 v[76:79], v[144:147], v[200:203], v[76:79]
	v_mfma_f32_16x16x32_bf16 v[72:75], v[152:155], v[200:203], v[72:75]
	v_mfma_f32_16x16x32_bf16 v[116:119], v[156:159], v[172:175], v[116:119]
	v_mfma_f32_16x16x32_bf16 v[112:115], v[164:167], v[172:175], v[112:115]
	v_mfma_f32_16x16x32_bf16 v[100:103], v[156:159], v[180:183], v[100:103]
	v_mfma_f32_16x16x32_bf16 v[96:99], v[164:167], v[180:183], v[96:99]
	v_mfma_f32_16x16x32_bf16 v[84:87], v[156:159], v[188:191], v[84:87]
	v_mfma_f32_16x16x32_bf16 v[80:83], v[164:167], v[188:191], v[80:83]
	v_mfma_f32_16x16x32_bf16 v[68:71], v[156:159], v[196:199], v[68:71]
	v_mfma_f32_16x16x32_bf16 v[64:67], v[164:167], v[196:199], v[64:67]
	v_mfma_f32_16x16x32_bf16 v[116:119], v[160:163], v[176:179], v[116:119]
	v_mfma_f32_16x16x32_bf16 v[112:115], v[168:171], v[176:179], v[112:115]
	v_mfma_f32_16x16x32_bf16 v[100:103], v[160:163], v[184:187], v[100:103]
	v_mfma_f32_16x16x32_bf16 v[96:99], v[168:171], v[184:187], v[96:99]
	v_mfma_f32_16x16x32_bf16 v[84:87], v[160:163], v[192:195], v[84:87]
	v_mfma_f32_16x16x32_bf16 v[80:83], v[168:171], v[192:195], v[80:83]
	v_mfma_f32_16x16x32_bf16 v[68:71], v[160:163], v[200:203], v[68:71]
	v_mfma_f32_16x16x32_bf16 v[64:67], v[168:171], v[200:203], v[64:67]
	s_setprio 0
	s_waitcnt vmcnt(8)
	s_barrier
	s_mov_b32 m0, s83
	s_nop 0
	global_load_lds_dwordx4 v244, s[58:59]
	s_mov_b32 m0, s84
	s_cselect_b32 s81, s49, s61
	s_cselect_b32 s80, s48, s60
	s_add_i32 s82, s72, s20
	global_load_lds_dwordx4 v246, s[58:59]
	s_mov_b32 m0, s82
	v_mov_b32_e32 v205, v129
	global_load_lds_dwordx4 v244, s[80:81]
	s_add_i32 m0, s82, 0x2000
	v_mov_b32_e32 v209, v129
	global_load_lds_dwordx4 v246, s[80:81]
	s_mov_b32 m0, s33
	v_lshl_add_u64 v[210:211], s[58:59], 0, v[244:245]
	global_load_lds_dwordx4 v240, s[56:57]
	s_mov_b32 m0, s62
	v_lshl_add_u64 v[212:213], s[58:59], 0, v[246:247]
	global_load_lds_dwordx4 v242, s[56:57]
	ds_read_b128 v[172:175], v140 offset:16384
	ds_read_b128 v[176:179], v140 offset:17408
	ds_read_b128 v[180:183], v140 offset:18432
	ds_read_b128 v[184:187], v140 offset:19456
	ds_read_b128 v[188:191], v140 offset:20480
	ds_read_b128 v[192:195], v140 offset:21504
	ds_read_b128 v[196:199], v140 offset:22528
	ds_read_b128 v[200:203], v140 offset:23552
	s_waitcnt lgkmcnt(0)
	v_lshl_add_u64 v[204:205], s[80:81], 0, v[244:245]
	v_lshl_add_u64 v[208:209], s[80:81], 0, v[246:247]
	v_lshl_add_u64 v[214:215], s[56:57], 0, v[240:241]
	v_lshl_add_u64 v[216:217], s[56:57], 0, v[242:243]
	s_barrier
; #define G_STAGE(bufoff, gbase, voff) do { _Pragma("unroll") for (int _i = 0; _i < 2; ++_i) \
;         __builtin_amdgcn_global_load_lds((const unsigned*)((const char*)(gbase) + (voff)[_i]), (LAS unsigned*)(lds + (bufoff) + ldsw + _i * 8192), 16, 0, 0); } while (0)
; #define G_LDA(dst, b, h) do { _Pragma("unroll") for (int m = 0; m < 4; ++m) G_LD8(dst[m], lds + G_SA(b, h) + aoff + m * 2048); } while (0)
; #define G_LDB(dst, b, h) do { _Pragma("unroll") for (int n = 0; n < 2; ++n) G_LD8(dst[n], lds + G_SB(b, h) + boff + n * 2048); } while (0)
; #define G_WAIT_V(n) asm volatile("s_waitcnt vmcnt(" #n ")" ::: "memory")
; #define G_WAIT_L(n) asm volatile("s_waitcnt lgkmcnt(" #n ")" ::: "memory")
; #define G_BAR __builtin_amdgcn_s_barrier()
; #define G_SCHED __builtin_amdgcn_sched_barrier(0)
;     ...
;             G_WAIT_L(0); G_BAR; G_MMA(1, 0, At, B0); G_MMA(1, 1, At, B1); G_WAIT_V(8); G_BAR; G_SCHED;
;             G_LDB(B0, 1, 0); G_LDB(B1, 1, 1); G_SCHED; G_LDA(At, 1, 0); G_STAGE(G_SA(0, 1), a12, vA1);
;             G_WAIT_L(0); G_BAR; G_MMA(0, 0, At, B0); G_MMA(0, 1, At, B1); G_WAIT_V(8); G_BAR; G_SCHED;
	s_setprio 1
	s_waitcnt lgkmcnt(0)
	v_mfma_f32_16x16x32_bf16 v[60:63], v[130:133], v[172:175], v[60:63]
	v_mfma_f32_16x16x32_bf16 v[56:59], v[148:151], v[172:175], v[56:59]
	v_mfma_f32_16x16x32_bf16 v[44:47], v[130:133], v[180:183], v[44:47]
	v_mfma_f32_16x16x32_bf16 v[40:43], v[148:151], v[180:183], v[40:43]
	v_mfma_f32_16x16x32_bf16 v[28:31], v[130:133], v[188:191], v[28:31]
	v_mfma_f32_16x16x32_bf16 v[24:27], v[148:151], v[188:191], v[24:27]
	v_mfma_f32_16x16x32_bf16 v[12:15], v[130:133], v[196:199], v[12:15]
	v_mfma_f32_16x16x32_bf16 v[8:11], v[148:151], v[196:199], v[8:11]
	v_mfma_f32_16x16x32_bf16 v[60:63], v[144:147], v[176:179], v[60:63]
	v_mfma_f32_16x16x32_bf16 v[56:59], v[152:155], v[176:179], v[56:59]
	v_mfma_f32_16x16x32_bf16 v[44:47], v[144:147], v[184:187], v[44:47]
	v_mfma_f32_16x16x32_bf16 v[40:43], v[152:155], v[184:187], v[40:43]
	v_mfma_f32_16x16x32_bf16 v[28:31], v[144:147], v[192:195], v[28:31]
	v_mfma_f32_16x16x32_bf16 v[24:27], v[152:155], v[192:195], v[24:27]
	v_mfma_f32_16x16x32_bf16 v[12:15], v[144:147], v[200:203], v[12:15]
	v_mfma_f32_16x16x32_bf16 v[8:11], v[152:155], v[200:203], v[8:11]
	v_mfma_f32_16x16x32_bf16 v[52:55], v[156:159], v[172:175], v[52:55]
	v_mfma_f32_16x16x32_bf16 v[48:51], v[164:167], v[172:175], v[48:51]
	v_mfma_f32_16x16x32_bf16 v[36:39], v[156:159], v[180:183], v[36:39]
	v_mfma_f32_16x16x32_bf16 v[32:35], v[164:167], v[180:183], v[32:35]
	v_mfma_f32_16x16x32_bf16 v[20:23], v[156:159], v[188:191], v[20:23]
	v_mfma_f32_16x16x32_bf16 v[16:19], v[164:167], v[188:191], v[16:19]
	v_mfma_f32_16x16x32_bf16 v[4:7], v[156:159], v[196:199], v[4:7]
	v_mfma_f32_16x16x32_bf16 v[0:3], v[164:167], v[196:199], v[0:3]
	v_mfma_f32_16x16x32_bf16 v[52:55], v[160:163], v[176:179], v[52:55]
	v_mfma_f32_16x16x32_bf16 v[48:51], v[168:171], v[176:179], v[48:51]
	v_mfma_f32_16x16x32_bf16 v[36:39], v[160:163], v[184:187], v[36:39]
	v_mfma_f32_16x16x32_bf16 v[32:35], v[168:171], v[184:187], v[32:35]
	v_mfma_f32_16x16x32_bf16 v[20:23], v[160:163], v[192:195], v[20:23]
	v_mfma_f32_16x16x32_bf16 v[16:19], v[168:171], v[192:195], v[16:19]
	v_mfma_f32_16x16x32_bf16 v[4:7], v[160:163], v[200:203], v[4:7]
	v_mfma_f32_16x16x32_bf16 v[0:3], v[168:171], v[200:203], v[0:3]
	s_setprio 0
	s_waitcnt vmcnt(8)
	s_barrier
	s_add_i32 s56, 0, 0x18000
	s_add_i32 s57, 0, 0x1c000
	s_mov_b32 m0, s63
	s_nop 0
	global_load_lds_dwordx4 v240, s[54:55]
	s_mov_b32 m0, s64
	s_nop 0
	global_load_lds_dwordx4 v242, s[54:55]
	v_add_u32_e32 v152, s56, v137
	v_add_u32_e32 v168, s57, v137
	ds_read_b128 v[130:133], v152
	ds_read_b128 v[144:147], v152 offset:1024
	ds_read_b128 v[148:151], v152 offset:2048
	ds_read_b128 v[152:155], v152 offset:3072
	ds_read_b128 v[156:159], v168
	ds_read_b128 v[160:163], v168 offset:1024
	ds_read_b128 v[164:167], v168 offset:2048
	ds_read_b128 v[168:171], v168 offset:3072
	ds_read_b128 v[172:175], v140 offset:32768
	ds_read_b128 v[176:179], v140 offset:33792
	ds_read_b128 v[180:183], v140 offset:34816
	ds_read_b128 v[184:187], v140 offset:35840
	ds_read_b128 v[188:191], v140 offset:36864
	ds_read_b128 v[192:195], v140 offset:37888
	ds_read_b128 v[196:199], v140 offset:38912
	ds_read_b128 v[200:203], v140 offset:39936
	s_waitcnt lgkmcnt(0)
	s_barrier
	s_setprio 1
	s_waitcnt lgkmcnt(0)
	v_mfma_f32_16x16x32_bf16 v[124:127], v[130:133], v[172:175], v[124:127]
	v_mfma_f32_16x16x32_bf16 v[120:123], v[148:151], v[172:175], v[120:123]
	v_mfma_f32_16x16x32_bf16 v[108:111], v[130:133], v[180:183], v[108:111]
	v_mfma_f32_16x16x32_bf16 v[104:107], v[148:151], v[180:183], v[104:107]
	v_mfma_f32_16x16x32_bf16 v[92:95], v[130:133], v[188:191], v[92:95]
	v_mfma_f32_16x16x32_bf16 v[88:91], v[148:151], v[188:191], v[88:91]
	v_mfma_f32_16x16x32_bf16 v[76:79], v[130:133], v[196:199], v[76:79]
	v_mfma_f32_16x16x32_bf16 v[72:75], v[148:151], v[196:199], v[72:75]
	v_mfma_f32_16x16x32_bf16 v[124:127], v[144:147], v[176:179], v[124:127]
	v_mfma_f32_16x16x32_bf16 v[120:123], v[152:155], v[176:179], v[120:123]
	v_mfma_f32_16x16x32_bf16 v[108:111], v[144:147], v[184:187], v[108:111]
	v_mfma_f32_16x16x32_bf16 v[104:107], v[152:155], v[184:187], v[104:107]
	v_mfma_f32_16x16x32_bf16 v[92:95], v[144:147], v[192:195], v[92:95]
	v_mfma_f32_16x16x32_bf16 v[88:91], v[152:155], v[192:195], v[88:91]
	v_mfma_f32_16x16x32_bf16 v[76:79], v[144:147], v[200:203], v[76:79]
	v_mfma_f32_16x16x32_bf16 v[72:75], v[152:155], v[200:203], v[72:75]
	v_mfma_f32_16x16x32_bf16 v[116:119], v[156:159], v[172:175], v[116:119]
	v_mfma_f32_16x16x32_bf16 v[112:115], v[164:167], v[172:175], v[112:115]
	v_mfma_f32_16x16x32_bf16 v[100:103], v[156:159], v[180:183], v[100:103]
	v_mfma_f32_16x16x32_bf16 v[96:99], v[164:167], v[180:183], v[96:99]
	v_mfma_f32_16x16x32_bf16 v[84:87], v[156:159], v[188:191], v[84:87]
	v_mfma_f32_16x16x32_bf16 v[80:83], v[164:167], v[188:191], v[80:83]
	v_mfma_f32_16x16x32_bf16 v[68:71], v[156:159], v[196:199], v[68:71]
	v_mfma_f32_16x16x32_bf16 v[64:67], v[164:167], v[196:199], v[64:67]
	v_mfma_f32_16x16x32_bf16 v[116:119], v[160:163], v[176:179], v[116:119]
	v_mfma_f32_16x16x32_bf16 v[112:115], v[168:171], v[176:179], v[112:115]
	v_mfma_f32_16x16x32_bf16 v[100:103], v[160:163], v[184:187], v[100:103]
	v_mfma_f32_16x16x32_bf16 v[96:99], v[168:171], v[184:187], v[96:99]
	v_mfma_f32_16x16x32_bf16 v[84:87], v[160:163], v[192:195], v[84:87]
	v_mfma_f32_16x16x32_bf16 v[80:83], v[168:171], v[192:195], v[80:83]
	v_mfma_f32_16x16x32_bf16 v[68:71], v[160:163], v[200:203], v[68:71]
	v_mfma_f32_16x16x32_bf16 v[64:67], v[168:171], v[200:203], v[64:67]
	s_setprio 0
	s_waitcnt vmcnt(8)
	s_barrier
; #define G_STAGE(bufoff, gbase, voff) do { _Pragma("unroll") for (int _i = 0; _i < 2; ++_i) \
;         __builtin_amdgcn_global_load_lds((const unsigned*)((const char*)(gbase) + (voff)[_i]), (LAS unsigned*)(lds + (bufoff) + ldsw + _i * 8192), 16, 0, 0); } while (0)
; #define G_LDA(dst, b, h) do { _Pragma("unroll") for (int m = 0; m < 4; ++m) G_LD8(dst[m], lds + G_SA(b, h) + aoff + m * 2048); } while (0)
; #define G_WAIT_V(n) asm volatile("s_waitcnt vmcnt(" #n ")" ::: "memory")
; #define G_WAIT_L(n) asm volatile("s_waitcnt lgkmcnt(" #n ")" ::: "memory")
; #define G_BAR __builtin_amdgcn_s_barrier()
; #define G_SCHED __builtin_amdgcn_sched_barrier(0)
;     ...
;             G_LDA(At, 1, 1); G_STAGE(G_SB(1, 0), b02 + kstep, voffB); G_STAGE(G_SB(1, 1), b12 + kstep, voffB); G_STAGE(G_SA(1, 0), a02 + kstep, vA0);
;             G_WAIT_L(0); G_BAR; G_MMA(1, 0, At, B0); G_MMA(1, 1, At, B1); G_WAIT_V(8); G_BAR; G_SCHED;
;         }
	s_add_i32 s54, s56, s20
	v_lshl_add_u64 v[206:207], v[210:211], 0, s[34:35]
	s_mov_b32 m0, s54
	s_nop 0
	global_load_lds_dwordx4 v[206:207], off
	v_lshl_add_u64 v[206:207], v[212:213], 0, s[34:35]
	s_add_i32 m0, s54, 0x2000
	s_add_i32 s54, s57, s20
	global_load_lds_dwordx4 v[206:207], off
	v_lshl_add_u64 v[204:205], v[204:205], 0, s[34:35]
	s_mov_b32 m0, s54
	s_nop 0
	global_load_lds_dwordx4 v[204:205], off
	v_lshl_add_u64 v[204:205], v[208:209], 0, s[34:35]
	s_add_i32 m0, s54, 0x2000
	s_nop 0
	global_load_lds_dwordx4 v[204:205], off
	v_lshl_add_u64 v[204:205], v[214:215], 0, s[34:35]
	s_mov_b32 m0, s66
	s_nop 0
	global_load_lds_dwordx4 v[204:205], off
	v_lshl_add_u64 v[204:205], v[216:217], 0, s[34:35]
	s_mov_b32 m0, s67
	s_nop 0
	global_load_lds_dwordx4 v[204:205], off
	ds_read_b128 v[172:175], v140 offset:49152
	ds_read_b128 v[176:179], v140 offset:50176
	ds_read_b128 v[180:183], v140 offset:51200
	ds_read_b128 v[184:187], v140 offset:52224
	ds_read_b128 v[188:191], v140 offset:53248
	ds_read_b128 v[192:195], v140 offset:54272
	ds_read_b128 v[196:199], v140 offset:55296
	ds_read_b128 v[200:203], v140 offset:56320
	s_waitcnt lgkmcnt(0)
	s_barrier
	s_setprio 1
	s_waitcnt lgkmcnt(0)
	v_mfma_f32_16x16x32_bf16 v[60:63], v[130:133], v[172:175], v[60:63]
	v_mfma_f32_16x16x32_bf16 v[56:59], v[148:151], v[172:175], v[56:59]
	v_mfma_f32_16x16x32_bf16 v[44:47], v[130:133], v[180:183], v[44:47]
	v_mfma_f32_16x16x32_bf16 v[40:43], v[148:151], v[180:183], v[40:43]
	v_mfma_f32_16x16x32_bf16 v[28:31], v[130:133], v[188:191], v[28:31]
	v_mfma_f32_16x16x32_bf16 v[24:27], v[148:151], v[188:191], v[24:27]
	v_mfma_f32_16x16x32_bf16 v[12:15], v[130:133], v[196:199], v[12:15]
	v_mfma_f32_16x16x32_bf16 v[8:11], v[148:151], v[196:199], v[8:11]
	v_mfma_f32_16x16x32_bf16 v[60:63], v[144:147], v[176:179], v[60:63]
	v_mfma_f32_16x16x32_bf16 v[56:59], v[152:155], v[176:179], v[56:59]
	v_mfma_f32_16x16x32_bf16 v[44:47], v[144:147], v[184:187], v[44:47]
	v_mfma_f32_16x16x32_bf16 v[40:43], v[152:155], v[184:187], v[40:43]
	v_mfma_f32_16x16x32_bf16 v[28:31], v[144:147], v[192:195], v[28:31]
	v_mfma_f32_16x16x32_bf16 v[24:27], v[152:155], v[192:195], v[24:27]
	v_mfma_f32_16x16x32_bf16 v[12:15], v[144:147], v[200:203], v[12:15]
	v_mfma_f32_16x16x32_bf16 v[8:11], v[152:155], v[200:203], v[8:11]
	v_mfma_f32_16x16x32_bf16 v[52:55], v[156:159], v[172:175], v[52:55]
	v_mfma_f32_16x16x32_bf16 v[48:51], v[164:167], v[172:175], v[48:51]
	v_mfma_f32_16x16x32_bf16 v[36:39], v[156:159], v[180:183], v[36:39]
	v_mfma_f32_16x16x32_bf16 v[32:35], v[164:167], v[180:183], v[32:35]
	v_mfma_f32_16x16x32_bf16 v[20:23], v[156:159], v[188:191], v[20:23]
	v_mfma_f32_16x16x32_bf16 v[16:19], v[164:167], v[188:191], v[16:19]
	v_mfma_f32_16x16x32_bf16 v[4:7], v[156:159], v[196:199], v[4:7]
	v_mfma_f32_16x16x32_bf16 v[0:3], v[164:167], v[196:199], v[0:3]
	v_mfma_f32_16x16x32_bf16 v[52:55], v[160:163], v[176:179], v[52:55]
	v_mfma_f32_16x16x32_bf16 v[48:51], v[168:171], v[176:179], v[48:51]
	v_mfma_f32_16x16x32_bf16 v[36:39], v[160:163], v[184:187], v[36:39]
	v_mfma_f32_16x16x32_bf16 v[32:35], v[168:171], v[184:187], v[32:35]
	v_mfma_f32_16x16x32_bf16 v[20:23], v[160:163], v[192:195], v[20:23]
	v_mfma_f32_16x16x32_bf16 v[16:19], v[168:171], v[192:195], v[16:19]
	v_mfma_f32_16x16x32_bf16 v[4:7], v[160:163], v[200:203], v[4:7]
	v_mfma_f32_16x16x32_bf16 v[0:3], v[168:171], v[200:203], v[0:3]
	s_setprio 0
	s_waitcnt vmcnt(8)
	s_barrier
	s_add_u32 s5, s5, 0x100
	s_addc_u32 s41, s41, 0
	s_add_u32 s60, s60, 0x100
	s_addc_u32 s61, s61, 0
	s_add_u32 s77, s77, 0x100
	s_addc_u32 s78, s78, 0
	s_add_u32 s52, s52, 0x100
	s_addc_u32 s53, s53, 0
	s_cmp_ge_i32 s79, s24
	s_mov_b32 s54, s79
	s_cbranch_scc0 .LBB0_1058
	v_readlane_b32 s78, v255, 11
	v_readlane_b32 s79, v255, 13
	s_and_b64 vcc, exec, s[38:39]
	s_cbranch_vccz .LBB0_1061

; #define G_STAGE(bufoff, gbase, voff) do { _Pragma("unroll") for (int _i = 0; _i < 2; ++_i) \
;         __builtin_amdgcn_global_load_lds((const unsigned*)((const char*)(gbase) + (voff)[_i]), (LAS unsigned*)(lds + (bufoff) + ldsw + _i * 8192), 16, 0, 0); } while (0)
; #define G_LDA(dst, b, h) do { _Pragma("unroll") for (int m = 0; m < 4; ++m) G_LD8(dst[m], lds + G_SA(b, h) + aoff + m * 2048); } while (0)
; #define G_LDB(dst, b, h) do { _Pragma("unroll") for (int n = 0; n < 2; ++n) G_LD8(dst[n], lds + G_SB(b, h) + boff + n * 2048); } while (0)
; #define G_WAIT_V(n) asm volatile("s_waitcnt vmcnt(" #n ")" ::: "memory")
; #define G_WAIT_L(n) asm volatile("s_waitcnt lgkmcnt(" #n ")" ::: "memory")
; #define G_BAR __builtin_amdgcn_s_barrier()
; #define G_SCHED __builtin_amdgcn_sched_barrier(0)
;     __device__ __forceinline__ unsigned row_off(const Unit& u, int r, LAS unsigned char* lds) const { return (unsigned)((const LAS int*)(lds + LDS_STAGE + u.q * 4096))[r] * (unsigned)rowbytes; }
;     ...
;             const char* a11 = cur.a1 + (size_t)(t + 1) * kstep;
;             const char* a02 = last ? nxt.a0 : cur.a0 + (size_t)(t + 2) * kstep; const char* a12 = last ? nxt.a1 : cur.a1 + (size_t)(t + 2) * kstep;
;             const char* b02 = last ? nxt.b0 : cur.b0 + (size_t)(t + 2) * kstep; const char* b12 = last ? nxt.b1 : cur.b1 + (size_t)(t + 2) * kstep;
;             G_LDB(B0, 0, 0); G_LDB(B1, 0, 1); G_SCHED; G_LDA(At, 0, 0); G_STAGE(G_SA(1, 1), a11, vA1);
;             if constexpr (GATHER) { if (last) { int tz = tid; asm volatile("" : "+v"(tz));
; #pragma unroll
;                 for (int i = 0; i < 2; ++i) { int R, C; stage_rc(tz * 16 + i * 8192, R, C); gc0[i] = S.row_off(nxt, R, lds) + (unsigned)C * 2u; gc1[i] = S.row_off(nxt, 128 + R, lds) + (unsigned)C * 2u; } } }
;             G_WAIT_L(0); G_BAR; G_MMA(0, 0, At, B0); G_MMA(0, 1, At, B1); G_WAIT_V(8); G_BAR; G_SCHED;
;             G_LDA(At, 0, 1); G_STAGE(G_SB(0, 0), b02, voffB); G_STAGE(G_SB(0, 1), b12, voffB); G_STAGE(G_SA(0, 0), a02, vA0);
.LBB0_1322:
	s_add_i32 vcc_lo, s66, 2
	s_add_u32 vcc_hi, s64, 0x80
	s_addc_u32 s67, s65, 0
	s_add_i32 s68, 0, 0x10000
	s_add_i32 s1, 0, 0x14000
	v_add_u32_e32 v146, s68, v172
	v_add_u32_e32 v162, s1, v172
	ds_read_b128 v[130:133], v146
	ds_read_b128 v[134:137], v146 offset:1024
	ds_read_b128 v[138:141], v146 offset:2048
	ds_read_b128 v[146:149], v146 offset:3072
	ds_read_b128 v[150:153], v162
	ds_read_b128 v[154:157], v162 offset:1024
	ds_read_b128 v[158:161], v162 offset:2048
	ds_read_b128 v[162:165], v162 offset:3072
	s_add_i32 s11, s68, s77
	s_add_i32 m0, s10, 0xc000
	s_add_i32 s33, s10, 0xe000
	s_add_i32 s21, s11, 0x2000
	s_cmp_eq_u32 s89, s66
	s_cselect_b32 s66, s54, vcc_hi
	s_cselect_b32 s69, s53, s97
	s_cselect_b32 s68, s52, s96
	s_cselect_b32 s71, s57, s93
	s_cselect_b32 s70, s56, s9
	s_cselect_b32 s67, s55, s67
	ds_read_b128 v[174:177], v173
	ds_read_b128 v[178:181], v173 offset:1024
	ds_read_b128 v[182:185], v173 offset:2048
	ds_read_b128 v[186:189], v173 offset:3072
	ds_read_b128 v[190:193], v173 offset:4096
	ds_read_b128 v[194:197], v173 offset:5120
	ds_read_b128 v[198:201], v173 offset:6144
	ds_read_b128 v[202:205], v173 offset:7168
	global_load_lds_dwordx4 v240, s[64:65]
	s_mov_b32 m0, s33
	s_nop 0
	global_load_lds_dwordx4 v242, s[64:65]
	s_waitcnt lgkmcnt(0)
	v_mov_b32_e32 v129, v145
	s_barrier
	s_setprio 1
	s_waitcnt lgkmcnt(0)
	v_mfma_f32_16x16x32_bf16 v[124:127], v[130:133], v[174:177], v[124:127]
	v_mfma_f32_16x16x32_bf16 v[120:123], v[138:141], v[174:177], v[120:123]
	v_mfma_f32_16x16x32_bf16 v[116:119], v[130:133], v[182:185], v[116:119]
	v_mfma_f32_16x16x32_bf16 v[112:115], v[138:141], v[182:185], v[112:115]
	v_mfma_f32_16x16x32_bf16 v[108:111], v[130:133], v[190:193], v[108:111]
	v_mfma_f32_16x16x32_bf16 v[104:107], v[138:141], v[190:193], v[104:107]
	v_mfma_f32_16x16x32_bf16 v[100:103], v[130:133], v[198:201], v[100:103]
	v_mfma_f32_16x16x32_bf16 v[96:99], v[138:141], v[198:201], v[96:99]
	v_mfma_f32_16x16x32_bf16 v[124:127], v[134:137], v[178:181], v[124:127]
	v_mfma_f32_16x16x32_bf16 v[120:123], v[146:149], v[178:181], v[120:123]
	v_mfma_f32_16x16x32_bf16 v[116:119], v[134:137], v[186:189], v[116:119]
	v_mfma_f32_16x16x32_bf16 v[112:115], v[146:149], v[186:189], v[112:115]
	v_mfma_f32_16x16x32_bf16 v[108:111], v[134:137], v[194:197], v[108:111]
	v_mfma_f32_16x16x32_bf16 v[104:107], v[146:149], v[194:197], v[104:107]
	v_mfma_f32_16x16x32_bf16 v[100:103], v[134:137], v[202:205], v[100:103]
	v_mfma_f32_16x16x32_bf16 v[96:99], v[146:149], v[202:205], v[96:99]
	v_mfma_f32_16x16x32_bf16 v[68:71], v[150:153], v[174:177], v[68:71]
	v_mfma_f32_16x16x32_bf16 v[60:63], v[158:161], v[174:177], v[60:63]
	v_mfma_f32_16x16x32_bf16 v[52:55], v[150:153], v[182:185], v[52:55]
	v_mfma_f32_16x16x32_bf16 v[48:51], v[158:161], v[182:185], v[48:51]
	v_mfma_f32_16x16x32_bf16 v[44:47], v[150:153], v[190:193], v[44:47]
	v_mfma_f32_16x16x32_bf16 v[40:43], v[158:161], v[190:193], v[40:43]
	v_mfma_f32_16x16x32_bf16 v[36:39], v[150:153], v[198:201], v[36:39]
	v_mfma_f32_16x16x32_bf16 v[32:35], v[158:161], v[198:201], v[32:35]
	v_mfma_f32_16x16x32_bf16 v[68:71], v[154:157], v[178:181], v[68:71]
	v_mfma_f32_16x16x32_bf16 v[60:63], v[162:165], v[178:181], v[60:63]
	v_mfma_f32_16x16x32_bf16 v[52:55], v[154:157], v[186:189], v[52:55]
	v_mfma_f32_16x16x32_bf16 v[48:51], v[162:165], v[186:189], v[48:51]
	v_mfma_f32_16x16x32_bf16 v[44:47], v[154:157], v[194:197], v[44:47]
	v_mfma_f32_16x16x32_bf16 v[40:43], v[162:165], v[194:197], v[40:43]
	v_mfma_f32_16x16x32_bf16 v[36:39], v[154:157], v[202:205], v[36:39]
	v_mfma_f32_16x16x32_bf16 v[32:35], v[162:165], v[202:205], v[32:35]
	s_setprio 0
	s_waitcnt vmcnt(8)
	s_barrier
	s_mov_b32 m0, s11
	v_mov_b32_e32 v143, v145
	global_load_lds_dwordx4 v244, s[70:71]
	v_mov_b32_e32 v207, v145
	s_mov_b32 m0, s21
	v_lshl_add_u64 v[208:209], s[70:71], 0, v[244:245]
	v_lshl_add_u64 v[210:211], s[70:71], 0, v[246:247]
	global_load_lds_dwordx4 v246, s[70:71]
	s_cselect_b32 s71, s59, s95
	s_cselect_b32 s70, s58, s94
	s_add_i32 s1, s1, s77
	s_mov_b32 m0, s1
	v_lshl_add_u64 v[212:213], s[70:71], 0, v[244:245]
	global_load_lds_dwordx4 v244, s[70:71]
	s_add_i32 m0, s1, 0x2000
	v_lshl_add_u64 v[142:143], s[70:71], 0, v[246:247]
	global_load_lds_dwordx4 v246, s[70:71]
	s_mov_b32 m0, s10
	v_lshl_add_u64 v[206:207], s[68:69], 0, v[240:241]
	global_load_lds_dwordx4 v240, s[68:69]
	s_mov_b32 m0, s63
	v_lshl_add_u64 v[214:215], s[68:69], 0, v[242:243]
	global_load_lds_dwordx4 v242, s[68:69]
	ds_read_b128 v[174:177], v173 offset:16384
	ds_read_b128 v[178:181], v173 offset:17408
	ds_read_b128 v[182:185], v173 offset:18432
	ds_read_b128 v[186:189], v173 offset:19456
	ds_read_b128 v[190:193], v173 offset:20480
	ds_read_b128 v[194:197], v173 offset:21504
	ds_read_b128 v[198:201], v173 offset:22528
	ds_read_b128 v[202:205], v173 offset:23552
	s_waitcnt lgkmcnt(0)
	s_barrier
; #define G_STAGE(bufoff, gbase, voff) do { _Pragma("unroll") for (int _i = 0; _i < 2; ++_i) \
;         __builtin_amdgcn_global_load_lds((const unsigned*)((const char*)(gbase) + (voff)[_i]), (LAS unsigned*)(lds + (bufoff) + ldsw + _i * 8192), 16, 0, 0); } while (0)
; #define G_LDA(dst, b, h) do { _Pragma("unroll") for (int m = 0; m < 4; ++m) G_LD8(dst[m], lds + G_SA(b, h) + aoff + m * 2048); } while (0)
; #define G_LDB(dst, b, h) do { _Pragma("unroll") for (int n = 0; n < 2; ++n) G_LD8(dst[n], lds + G_SB(b, h) + boff + n * 2048); } while (0)
; #define G_WAIT_V(n) asm volatile("s_waitcnt vmcnt(" #n ")" ::: "memory")
; #define G_WAIT_L(n) asm volatile("s_waitcnt lgkmcnt(" #n ")" ::: "memory")
; #define G_BAR __builtin_amdgcn_s_barrier()
; #define G_SCHED __builtin_amdgcn_sched_barrier(0)
;     ...
;             G_WAIT_L(0); G_BAR; G_MMA(1, 0, At, B0); G_MMA(1, 1, At, B1); G_WAIT_V(8); G_BAR; G_SCHED;
;             G_LDB(B0, 1, 0); G_LDB(B1, 1, 1); G_SCHED; G_LDA(At, 1, 0); G_STAGE(G_SA(0, 1), a12, vA1);
;             G_WAIT_L(0); G_BAR; G_MMA(0, 0, At, B0); G_MMA(0, 1, At, B1); G_WAIT_V(8); G_BAR; G_SCHED;
	s_setprio 1
	s_waitcnt lgkmcnt(0)
	v_mfma_f32_16x16x32_bf16 v[92:95], v[130:133], v[174:177], v[92:95]
	v_mfma_f32_16x16x32_bf16 v[88:91], v[138:141], v[174:177], v[88:91]
	v_mfma_f32_16x16x32_bf16 v[84:87], v[130:133], v[182:185], v[84:87]
	v_mfma_f32_16x16x32_bf16 v[80:83], v[138:141], v[182:185], v[80:83]
	v_mfma_f32_16x16x32_bf16 v[76:79], v[130:133], v[190:193], v[76:79]
	v_mfma_f32_16x16x32_bf16 v[72:75], v[138:141], v[190:193], v[72:75]
	v_mfma_f32_16x16x32_bf16 v[64:67], v[130:133], v[198:201], v[64:67]
	v_mfma_f32_16x16x32_bf16 v[56:59], v[138:141], v[198:201], v[56:59]
	v_mfma_f32_16x16x32_bf16 v[92:95], v[134:137], v[178:181], v[92:95]
	v_mfma_f32_16x16x32_bf16 v[88:91], v[146:149], v[178:181], v[88:91]
	v_mfma_f32_16x16x32_bf16 v[84:87], v[134:137], v[186:189], v[84:87]
	v_mfma_f32_16x16x32_bf16 v[80:83], v[146:149], v[186:189], v[80:83]
	v_mfma_f32_16x16x32_bf16 v[76:79], v[134:137], v[194:197], v[76:79]
	v_mfma_f32_16x16x32_bf16 v[72:75], v[146:149], v[194:197], v[72:75]
	v_mfma_f32_16x16x32_bf16 v[64:67], v[134:137], v[202:205], v[64:67]
	v_mfma_f32_16x16x32_bf16 v[56:59], v[146:149], v[202:205], v[56:59]
	v_mfma_f32_16x16x32_bf16 v[28:31], v[150:153], v[174:177], v[28:31]
	v_mfma_f32_16x16x32_bf16 v[24:27], v[158:161], v[174:177], v[24:27]
	v_mfma_f32_16x16x32_bf16 v[20:23], v[150:153], v[182:185], v[20:23]
	v_mfma_f32_16x16x32_bf16 v[16:19], v[158:161], v[182:185], v[16:19]
	v_mfma_f32_16x16x32_bf16 v[12:15], v[150:153], v[190:193], v[12:15]
	v_mfma_f32_16x16x32_bf16 v[8:11], v[158:161], v[190:193], v[8:11]
	v_mfma_f32_16x16x32_bf16 v[4:7], v[150:153], v[198:201], v[4:7]
	v_mfma_f32_16x16x32_bf16 v[0:3], v[158:161], v[198:201], v[0:3]
	v_mfma_f32_16x16x32_bf16 v[28:31], v[154:157], v[178:181], v[28:31]
	v_mfma_f32_16x16x32_bf16 v[24:27], v[162:165], v[178:181], v[24:27]
	v_mfma_f32_16x16x32_bf16 v[20:23], v[154:157], v[186:189], v[20:23]
	v_mfma_f32_16x16x32_bf16 v[16:19], v[162:165], v[186:189], v[16:19]
	v_mfma_f32_16x16x32_bf16 v[12:15], v[154:157], v[194:197], v[12:15]
	v_mfma_f32_16x16x32_bf16 v[8:11], v[162:165], v[194:197], v[8:11]
	v_mfma_f32_16x16x32_bf16 v[4:7], v[154:157], v[202:205], v[4:7]
	v_mfma_f32_16x16x32_bf16 v[0:3], v[162:165], v[202:205], v[0:3]
	s_setprio 0
	s_waitcnt vmcnt(8)
	s_barrier
	s_add_i32 s1, 0, 0x18000
	s_add_i32 s11, 0, 0x1c000
	s_mov_b32 m0, s72
	s_nop 0
	global_load_lds_dwordx4 v240, s[66:67]
	s_mov_b32 m0, s73
	s_nop 0
	global_load_lds_dwordx4 v242, s[66:67]
	v_add_u32_e32 v129, s1, v172
	ds_read_b128 v[130:133], v129
	ds_read_b128 v[134:137], v129 offset:1024
	ds_read_b128 v[138:141], v129 offset:2048
	ds_read_b128 v[146:149], v129 offset:3072
	v_add_u32_e32 v129, s11, v172
	ds_read_b128 v[150:153], v129
	ds_read_b128 v[154:157], v129 offset:1024
	ds_read_b128 v[158:161], v129 offset:2048
	ds_read_b128 v[162:165], v129 offset:3072
	ds_read_b128 v[174:177], v173 offset:32768
	ds_read_b128 v[178:181], v173 offset:33792
	ds_read_b128 v[182:185], v173 offset:34816
	ds_read_b128 v[186:189], v173 offset:35840
	ds_read_b128 v[190:193], v173 offset:36864
	ds_read_b128 v[194:197], v173 offset:37888
	ds_read_b128 v[198:201], v173 offset:38912
	ds_read_b128 v[202:205], v173 offset:39936
	s_waitcnt lgkmcnt(0)
	s_barrier
	s_setprio 1
	s_waitcnt lgkmcnt(0)
	v_mfma_f32_16x16x32_bf16 v[124:127], v[130:133], v[174:177], v[124:127]
	v_mfma_f32_16x16x32_bf16 v[120:123], v[138:141], v[174:177], v[120:123]
	v_mfma_f32_16x16x32_bf16 v[116:119], v[130:133], v[182:185], v[116:119]
	v_mfma_f32_16x16x32_bf16 v[112:115], v[138:141], v[182:185], v[112:115]
	v_mfma_f32_16x16x32_bf16 v[108:111], v[130:133], v[190:193], v[108:111]
	v_mfma_f32_16x16x32_bf16 v[104:107], v[138:141], v[190:193], v[104:107]
	v_mfma_f32_16x16x32_bf16 v[100:103], v[130:133], v[198:201], v[100:103]
	v_mfma_f32_16x16x32_bf16 v[96:99], v[138:141], v[198:201], v[96:99]
	v_mfma_f32_16x16x32_bf16 v[124:127], v[134:137], v[178:181], v[124:127]
	v_mfma_f32_16x16x32_bf16 v[120:123], v[146:149], v[178:181], v[120:123]
	v_mfma_f32_16x16x32_bf16 v[116:119], v[134:137], v[186:189], v[116:119]
	v_mfma_f32_16x16x32_bf16 v[112:115], v[146:149], v[186:189], v[112:115]
	v_mfma_f32_16x16x32_bf16 v[108:111], v[134:137], v[194:197], v[108:111]
	v_mfma_f32_16x16x32_bf16 v[104:107], v[146:149], v[194:197], v[104:107]
	v_mfma_f32_16x16x32_bf16 v[100:103], v[134:137], v[202:205], v[100:103]
	v_mfma_f32_16x16x32_bf16 v[96:99], v[146:149], v[202:205], v[96:99]
	v_mfma_f32_16x16x32_bf16 v[68:71], v[150:153], v[174:177], v[68:71]
	v_mfma_f32_16x16x32_bf16 v[60:63], v[158:161], v[174:177], v[60:63]
	v_mfma_f32_16x16x32_bf16 v[52:55], v[150:153], v[182:185], v[52:55]
	v_mfma_f32_16x16x32_bf16 v[48:51], v[158:161], v[182:185], v[48:51]
	v_mfma_f32_16x16x32_bf16 v[44:47], v[150:153], v[190:193], v[44:47]
	v_mfma_f32_16x16x32_bf16 v[40:43], v[158:161], v[190:193], v[40:43]
	v_mfma_f32_16x16x32_bf16 v[36:39], v[150:153], v[198:201], v[36:39]
	v_mfma_f32_16x16x32_bf16 v[32:35], v[158:161], v[198:201], v[32:35]
	v_mfma_f32_16x16x32_bf16 v[68:71], v[154:157], v[178:181], v[68:71]
	v_mfma_f32_16x16x32_bf16 v[60:63], v[162:165], v[178:181], v[60:63]
	v_mfma_f32_16x16x32_bf16 v[52:55], v[154:157], v[186:189], v[52:55]
	v_mfma_f32_16x16x32_bf16 v[48:51], v[162:165], v[186:189], v[48:51]
	v_mfma_f32_16x16x32_bf16 v[44:47], v[154:157], v[194:197], v[44:47]
	v_mfma_f32_16x16x32_bf16 v[40:43], v[162:165], v[194:197], v[40:43]
	v_mfma_f32_16x16x32_bf16 v[36:39], v[154:157], v[202:205], v[36:39]
	v_mfma_f32_16x16x32_bf16 v[32:35], v[162:165], v[202:205], v[32:35]
	s_setprio 0
	s_waitcnt vmcnt(8)
	s_barrier
; #define G_STAGE(bufoff, gbase, voff) do { _Pragma("unroll") for (int _i = 0; _i < 2; ++_i) \
;         __builtin_amdgcn_global_load_lds((const unsigned*)((const char*)(gbase) + (voff)[_i]), (LAS unsigned*)(lds + (bufoff) + ldsw + _i * 8192), 16, 0, 0); } while (0)
; #define G_LDA(dst, b, h) do { _Pragma("unroll") for (int m = 0; m < 4; ++m) G_LD8(dst[m], lds + G_SA(b, h) + aoff + m * 2048); } while (0)
; #define G_WAIT_V(n) asm volatile("s_waitcnt vmcnt(" #n ")" ::: "memory")
; #define G_WAIT_L(n) asm volatile("s_waitcnt lgkmcnt(" #n ")" ::: "memory")
; #define G_BAR __builtin_amdgcn_s_barrier()
; #define G_SCHED __builtin_amdgcn_sched_barrier(0)
;     ...
;             G_LDA(At, 1, 1); G_STAGE(G_SB(1, 0), b02 + kstep, voffB); G_STAGE(G_SB(1, 1), b12 + kstep, voffB); G_STAGE(G_SA(1, 0), a02 + kstep, vA0);
;             G_WAIT_L(0); G_BAR; G_MMA(1, 0, At, B0); G_MMA(1, 1, At, B1); G_WAIT_V(8); G_BAR; G_SCHED;
;         }
	s_add_i32 s1, s1, s77
	v_lshl_add_u64 v[128:129], v[208:209], 0, s[48:49]
	s_mov_b32 m0, s1
	s_nop 0
	global_load_lds_dwordx4 v[128:129], off
	v_lshl_add_u64 v[128:129], v[210:211], 0, s[48:49]
	s_add_i32 m0, s1, 0x2000
	s_add_i32 s1, s11, s77
	global_load_lds_dwordx4 v[128:129], off
	v_lshl_add_u64 v[128:129], v[212:213], 0, s[48:49]
	s_mov_b32 m0, s1
	s_nop 0
	global_load_lds_dwordx4 v[128:129], off
	v_lshl_add_u64 v[128:129], v[142:143], 0, s[48:49]
	s_add_i32 m0, s1, 0x2000
	s_nop 0
	global_load_lds_dwordx4 v[128:129], off
	v_lshl_add_u64 v[128:129], v[206:207], 0, s[48:49]
	s_mov_b32 m0, s75
	s_nop 0
	global_load_lds_dwordx4 v[128:129], off
	v_lshl_add_u64 v[128:129], v[214:215], 0, s[48:49]
	s_mov_b32 m0, s76
	s_nop 0
	global_load_lds_dwordx4 v[128:129], off
	ds_read_b128 v[174:177], v173 offset:49152
	ds_read_b128 v[178:181], v173 offset:50176
	ds_read_b128 v[182:185], v173 offset:51200
	ds_read_b128 v[186:189], v173 offset:52224
	ds_read_b128 v[190:193], v173 offset:53248
	ds_read_b128 v[194:197], v173 offset:54272
	ds_read_b128 v[198:201], v173 offset:55296
	ds_read_b128 v[202:205], v173 offset:56320
	s_waitcnt lgkmcnt(0)
	s_barrier
	s_setprio 1
	s_waitcnt lgkmcnt(0)
	v_mfma_f32_16x16x32_bf16 v[92:95], v[130:133], v[174:177], v[92:95]
	v_mfma_f32_16x16x32_bf16 v[88:91], v[138:141], v[174:177], v[88:91]
	v_mfma_f32_16x16x32_bf16 v[84:87], v[130:133], v[182:185], v[84:87]
	v_mfma_f32_16x16x32_bf16 v[80:83], v[138:141], v[182:185], v[80:83]
	v_mfma_f32_16x16x32_bf16 v[76:79], v[130:133], v[190:193], v[76:79]
	v_mfma_f32_16x16x32_bf16 v[72:75], v[138:141], v[190:193], v[72:75]
	v_mfma_f32_16x16x32_bf16 v[64:67], v[130:133], v[198:201], v[64:67]
	v_mfma_f32_16x16x32_bf16 v[56:59], v[138:141], v[198:201], v[56:59]
	v_mfma_f32_16x16x32_bf16 v[92:95], v[134:137], v[178:181], v[92:95]
	v_mfma_f32_16x16x32_bf16 v[88:91], v[146:149], v[178:181], v[88:91]
	v_mfma_f32_16x16x32_bf16 v[84:87], v[134:137], v[186:189], v[84:87]
	v_mfma_f32_16x16x32_bf16 v[80:83], v[146:149], v[186:189], v[80:83]
	v_mfma_f32_16x16x32_bf16 v[76:79], v[134:137], v[194:197], v[76:79]
	v_mfma_f32_16x16x32_bf16 v[72:75], v[146:149], v[194:197], v[72:75]
	v_mfma_f32_16x16x32_bf16 v[64:67], v[134:137], v[202:205], v[64:67]
	v_mfma_f32_16x16x32_bf16 v[56:59], v[146:149], v[202:205], v[56:59]
	v_mfma_f32_16x16x32_bf16 v[28:31], v[150:153], v[174:177], v[28:31]
	v_mfma_f32_16x16x32_bf16 v[24:27], v[158:161], v[174:177], v[24:27]
	v_mfma_f32_16x16x32_bf16 v[20:23], v[150:153], v[182:185], v[20:23]
	v_mfma_f32_16x16x32_bf16 v[16:19], v[158:161], v[182:185], v[16:19]
	v_mfma_f32_16x16x32_bf16 v[12:15], v[150:153], v[190:193], v[12:15]
	v_mfma_f32_16x16x32_bf16 v[8:11], v[158:161], v[190:193], v[8:11]
	v_mfma_f32_16x16x32_bf16 v[4:7], v[150:153], v[198:201], v[4:7]
	v_mfma_f32_16x16x32_bf16 v[0:3], v[158:161], v[198:201], v[0:3]
	v_mfma_f32_16x16x32_bf16 v[28:31], v[154:157], v[178:181], v[28:31]
	v_mfma_f32_16x16x32_bf16 v[24:27], v[162:165], v[178:181], v[24:27]
	v_mfma_f32_16x16x32_bf16 v[20:23], v[154:157], v[186:189], v[20:23]
	v_mfma_f32_16x16x32_bf16 v[16:19], v[162:165], v[186:189], v[16:19]
	v_mfma_f32_16x16x32_bf16 v[12:15], v[154:157], v[194:197], v[12:15]
	v_mfma_f32_16x16x32_bf16 v[8:11], v[162:165], v[194:197], v[8:11]
	v_mfma_f32_16x16x32_bf16 v[4:7], v[154:157], v[202:205], v[4:7]
	v_mfma_f32_16x16x32_bf16 v[0:3], v[162:165], v[202:205], v[0:3]
	s_setprio 0
	s_waitcnt vmcnt(8)
	s_barrier
	s_add_u32 s9, s9, 0x100
	s_addc_u32 s93, s93, 0
	s_add_u32 s94, s94, 0x100
	s_addc_u32 s95, s95, 0
	s_add_u32 s96, s96, 0x100
	s_addc_u32 s97, s97, 0
	s_add_u32 s64, s64, 0x100
	s_addc_u32 s65, s65, 0
	s_cmp_ge_i32 vcc_lo, s2
	s_mov_b32 s66, vcc_lo
	s_cbranch_scc0 .LBB0_1322
	v_readlane_b32 s64, v255, 9
	v_readlane_b32 s65, v255, 10
	s_load_dword s97, s[64:65], 0xa8
	s_and_b64 vcc, exec, s[46:47]
	s_cbranch_vccz .LBB0_1325

; #define G_STAGE(bufoff, gbase, voff) do { _Pragma("unroll") for (int _i = 0; _i < 2; ++_i) \
;         __builtin_amdgcn_global_load_lds((const unsigned*)((const char*)(gbase) + (voff)[_i]), (LAS unsigned*)(lds + (bufoff) + ldsw + _i * 8192), 16, 0, 0); } while (0)
; #define G_LDA(dst, b, h) do { _Pragma("unroll") for (int m = 0; m < 4; ++m) G_LD8(dst[m], lds + G_SA(b, h) + aoff + m * 2048); } while (0)
; #define G_LDB(dst, b, h) do { _Pragma("unroll") for (int n = 0; n < 2; ++n) G_LD8(dst[n], lds + G_SB(b, h) + boff + n * 2048); } while (0)
; #define G_WAIT_V(n) asm volatile("s_waitcnt vmcnt(" #n ")" ::: "memory")
; #define G_WAIT_L(n) asm volatile("s_waitcnt lgkmcnt(" #n ")" ::: "memory")
; #define G_BAR __builtin_amdgcn_s_barrier()
; #define G_SCHED __builtin_amdgcn_sched_barrier(0)
;     __device__ __forceinline__ unsigned row_off(const Unit& u, int r, LAS unsigned char* lds) const { return (unsigned)((const LAS int*)(lds + LDS_STAGE + u.q * 4096))[r] * (unsigned)rowbytes; }
;     ...
;             const char* a11 = cur.a1 + (size_t)(t + 1) * kstep;
;             const char* a02 = last ? nxt.a0 : cur.a0 + (size_t)(t + 2) * kstep; const char* a12 = last ? nxt.a1 : cur.a1 + (size_t)(t + 2) * kstep;
;             const char* b02 = last ? nxt.b0 : cur.b0 + (size_t)(t + 2) * kstep; const char* b12 = last ? nxt.b1 : cur.b1 + (size_t)(t + 2) * kstep;
;             G_LDB(B0, 0, 0); G_LDB(B1, 0, 1); G_SCHED; G_LDA(At, 0, 0); G_STAGE(G_SA(1, 1), a11, vA1);
;             if constexpr (GATHER) { if (last) { int tz = tid; asm volatile("" : "+v"(tz));
; #pragma unroll
;                 for (int i = 0; i < 2; ++i) { int R, C; stage_rc(tz * 16 + i * 8192, R, C); gc0[i] = S.row_off(nxt, R, lds) + (unsigned)C * 2u; gc1[i] = S.row_off(nxt, 128 + R, lds) + (unsigned)C * 2u; } } }
;             G_WAIT_L(0); G_BAR; G_MMA(0, 0, At, B0); G_MMA(0, 1, At, B1); G_WAIT_V(8); G_BAR; G_SCHED;
;             G_LDA(At, 0, 1); G_STAGE(G_SB(0, 0), b02, voffB); G_STAGE(G_SB(0, 1), b12, voffB); G_STAGE(G_SA(0, 0), a02, vA0);
;             G_WAIT_L(0); G_BAR; G_MMA(1, 0, At, B0); G_MMA(1, 1, At, B1); G_WAIT_V(8); G_BAR; G_SCHED;
.LBB0_1626:
	s_add_i32 s31, s31, 2
	s_add_u32 s78, s26, s74
	s_addc_u32 s79, s27, s75
	s_add_u32 s80, s62, s74
	s_addc_u32 s81, s63, s75
	s_add_u32 s82, s80, 0x100
	s_addc_u32 s83, s81, 0
	s_add_u32 s80, s36, s74
	s_addc_u32 s81, s37, s75
	s_add_u32 vcc_lo, s87, s74
	s_waitcnt lgkmcnt(0)
	s_addc_u32 vcc_hi, s90, s75
	s_and_b64 s[76:77], s[76:77], exec
	s_cselect_b32 s79, s57, s79
	s_cselect_b32 s78, s56, s78
	s_cselect_b32 s81, s51, s81
	s_cselect_b32 s80, s50, s80
	s_cselect_b32 s77, s55, s83
	s_cselect_b32 s76, s54, s82
	s_cselect_b32 s83, s53, vcc_hi
	s_cselect_b32 s82, s52, vcc_lo
	s_barrier
	s_setprio 1
	s_waitcnt lgkmcnt(0)
	v_mfma_i32_16x16x64_i8 v[156:159], v[88:91], v[184:187], v[156:159]
	v_mfma_i32_16x16x64_i8 v[148:151], v[96:99], v[184:187], v[148:151]
	v_mfma_i32_16x16x64_i8 v[140:143], v[88:91], v[176:179], v[140:143]
	v_mfma_i32_16x16x64_i8 v[132:135], v[96:99], v[176:179], v[132:135]
	v_mfma_i32_16x16x64_i8 v[124:127], v[88:91], v[168:171], v[124:127]
	v_mfma_i32_16x16x64_i8 v[116:119], v[96:99], v[168:171], v[116:119]
	v_mfma_i32_16x16x64_i8 v[108:111], v[88:91], v[160:163], v[108:111]
	v_mfma_i32_16x16x64_i8 v[84:87], v[96:99], v[160:163], v[84:87]
	v_mfma_i32_16x16x64_i8 v[156:159], v[92:95], v[188:191], v[156:159]
	v_mfma_i32_16x16x64_i8 v[148:151], v[100:103], v[188:191], v[148:151]
	v_mfma_i32_16x16x64_i8 v[140:143], v[92:95], v[180:183], v[140:143]
	v_mfma_i32_16x16x64_i8 v[132:135], v[100:103], v[180:183], v[132:135]
	v_mfma_i32_16x16x64_i8 v[124:127], v[92:95], v[172:175], v[124:127]
	v_mfma_i32_16x16x64_i8 v[116:119], v[100:103], v[172:175], v[116:119]
	v_mfma_i32_16x16x64_i8 v[108:111], v[92:95], v[164:167], v[108:111]
	v_mfma_i32_16x16x64_i8 v[84:87], v[100:103], v[164:167], v[84:87]
	v_mfma_i32_16x16x64_i8 v[152:155], v[64:67], v[184:187], v[152:155]
	v_mfma_i32_16x16x64_i8 v[144:147], v[72:75], v[184:187], v[144:147]
	v_mfma_i32_16x16x64_i8 v[136:139], v[64:67], v[176:179], v[136:139]
	v_mfma_i32_16x16x64_i8 v[128:131], v[72:75], v[176:179], v[128:131]
	v_mfma_i32_16x16x64_i8 v[120:123], v[64:67], v[168:171], v[120:123]
	v_mfma_i32_16x16x64_i8 v[112:115], v[72:75], v[168:171], v[112:115]
	v_mfma_i32_16x16x64_i8 v[104:107], v[64:67], v[160:163], v[104:107]
	v_mfma_i32_16x16x64_i8 v[80:83], v[72:75], v[160:163], v[80:83]
	v_mfma_i32_16x16x64_i8 v[152:155], v[68:71], v[188:191], v[152:155]
	v_mfma_i32_16x16x64_i8 v[144:147], v[76:79], v[188:191], v[144:147]
	v_mfma_i32_16x16x64_i8 v[136:139], v[68:71], v[180:183], v[136:139]
	v_mfma_i32_16x16x64_i8 v[128:131], v[76:79], v[180:183], v[128:131]
	v_mfma_i32_16x16x64_i8 v[120:123], v[68:71], v[172:175], v[120:123]
	v_mfma_i32_16x16x64_i8 v[112:115], v[76:79], v[172:175], v[112:115]
	v_mfma_i32_16x16x64_i8 v[104:107], v[68:71], v[164:167], v[104:107]
	v_mfma_i32_16x16x64_i8 v[80:83], v[76:79], v[164:167], v[80:83]
	s_setprio 0
	s_waitcnt vmcnt(8)
	s_barrier
	s_mov_b32 m0, s34
	s_nop 0
	global_load_lds_dwordx4 v244, s[80:81]
	s_mov_b32 m0, s35
	v_mov_b32_e32 v211, v193
	global_load_lds_dwordx4 v246, s[80:81]
	s_mov_b32 m0, s30
	v_mov_b32_e32 v213, v193
	global_load_lds_dwordx4 v244, s[82:83]
	s_mov_b32 m0, s0
	v_mov_b32_e32 v195, v193
	global_load_lds_dwordx4 v246, s[82:83]
	s_mov_b32 m0, s3
	v_mov_b32_e32 v197, v193
	global_load_lds_dwordx4 v194, s[78:79]
	s_mov_b32 m0, s40
	v_lshl_add_u64 v[214:215], s[80:81], 0, v[244:245]
	global_load_lds_dwordx4 v196, s[78:79]
	ds_read_b128 v[160:163], v208 offset:16384
	ds_read_b128 v[164:167], v208 offset:17408
	ds_read_b128 v[168:171], v208 offset:18432
	ds_read_b128 v[172:175], v208 offset:19456
	ds_read_b128 v[176:179], v208 offset:20480
	ds_read_b128 v[180:183], v208 offset:21504
	ds_read_b128 v[184:187], v208 offset:22528
	ds_read_b128 v[188:191], v208 offset:23552
	s_waitcnt lgkmcnt(0)
	v_lshl_add_u64 v[216:217], s[80:81], 0, v[246:247]
	v_lshl_add_u64 v[210:211], s[82:83], 0, v[244:245]
	v_lshl_add_u64 v[212:213], s[82:83], 0, v[246:247]
	v_lshl_add_u64 v[218:219], s[78:79], 0, v[194:195]
	v_lshl_add_u64 v[220:221], s[78:79], 0, v[196:197]
	s_barrier
	s_setprio 1
	s_waitcnt lgkmcnt(0)
	v_mfma_i32_16x16x64_i8 v[60:63], v[88:91], v[160:163], v[60:63]
	v_mfma_i32_16x16x64_i8 v[52:55], v[96:99], v[160:163], v[52:55]
	v_mfma_i32_16x16x64_i8 v[44:47], v[88:91], v[168:171], v[44:47]
	v_mfma_i32_16x16x64_i8 v[36:39], v[96:99], v[168:171], v[36:39]
	v_mfma_i32_16x16x64_i8 v[28:31], v[88:91], v[176:179], v[28:31]
	v_mfma_i32_16x16x64_i8 v[20:23], v[96:99], v[176:179], v[20:23]
	v_mfma_i32_16x16x64_i8 v[12:15], v[88:91], v[184:187], v[12:15]
	v_mfma_i32_16x16x64_i8 v[4:7], v[96:99], v[184:187], v[4:7]
	v_mfma_i32_16x16x64_i8 v[60:63], v[92:95], v[164:167], v[60:63]
	v_mfma_i32_16x16x64_i8 v[52:55], v[100:103], v[164:167], v[52:55]
	v_mfma_i32_16x16x64_i8 v[44:47], v[92:95], v[172:175], v[44:47]
	v_mfma_i32_16x16x64_i8 v[36:39], v[100:103], v[172:175], v[36:39]
	v_mfma_i32_16x16x64_i8 v[28:31], v[92:95], v[180:183], v[28:31]
	v_mfma_i32_16x16x64_i8 v[20:23], v[100:103], v[180:183], v[20:23]
	v_mfma_i32_16x16x64_i8 v[12:15], v[92:95], v[188:191], v[12:15]
	v_mfma_i32_16x16x64_i8 v[4:7], v[100:103], v[188:191], v[4:7]
	v_mfma_i32_16x16x64_i8 v[56:59], v[64:67], v[160:163], v[56:59]
	v_mfma_i32_16x16x64_i8 v[48:51], v[72:75], v[160:163], v[48:51]
	v_mfma_i32_16x16x64_i8 v[40:43], v[64:67], v[168:171], v[40:43]
	v_mfma_i32_16x16x64_i8 v[32:35], v[72:75], v[168:171], v[32:35]
	v_mfma_i32_16x16x64_i8 v[24:27], v[64:67], v[176:179], v[24:27]
	v_mfma_i32_16x16x64_i8 v[16:19], v[72:75], v[176:179], v[16:19]
	v_mfma_i32_16x16x64_i8 v[8:11], v[64:67], v[184:187], v[8:11]
	v_mfma_i32_16x16x64_i8 v[0:3], v[72:75], v[184:187], v[0:3]
	v_mfma_i32_16x16x64_i8 v[56:59], v[68:71], v[164:167], v[56:59]
	v_mfma_i32_16x16x64_i8 v[48:51], v[76:79], v[164:167], v[48:51]
	v_mfma_i32_16x16x64_i8 v[40:43], v[68:71], v[172:175], v[40:43]
	v_mfma_i32_16x16x64_i8 v[32:35], v[76:79], v[172:175], v[32:35]
	v_mfma_i32_16x16x64_i8 v[24:27], v[68:71], v[180:183], v[24:27]
	v_mfma_i32_16x16x64_i8 v[16:19], v[76:79], v[180:183], v[16:19]
	v_mfma_i32_16x16x64_i8 v[8:11], v[68:71], v[188:191], v[8:11]
	v_mfma_i32_16x16x64_i8 v[0:3], v[76:79], v[188:191], v[0:3]
	s_setprio 0
	s_waitcnt vmcnt(8)
	s_barrier
; #define G_STAGE(bufoff, gbase, voff) do { _Pragma("unroll") for (int _i = 0; _i < 2; ++_i) \
;         __builtin_amdgcn_global_load_lds((const unsigned*)((const char*)(gbase) + (voff)[_i]), (LAS unsigned*)(lds + (bufoff) + ldsw + _i * 8192), 16, 0, 0); } while (0)
; #define G_LDA(dst, b, h) do { _Pragma("unroll") for (int m = 0; m < 4; ++m) G_LD8(dst[m], lds + G_SA(b, h) + aoff + m * 2048); } while (0)
; #define G_LDB(dst, b, h) do { _Pragma("unroll") for (int n = 0; n < 2; ++n) G_LD8(dst[n], lds + G_SB(b, h) + boff + n * 2048); } while (0)
; #define G_WAIT_V(n) asm volatile("s_waitcnt vmcnt(" #n ")" ::: "memory")
; #define G_WAIT_L(n) asm volatile("s_waitcnt lgkmcnt(" #n ")" ::: "memory")
; #define G_BAR __builtin_amdgcn_s_barrier()
; #define G_SCHED __builtin_amdgcn_sched_barrier(0)
;     ...
;             G_LDB(B0, 1, 0); G_LDB(B1, 1, 1); G_SCHED; G_LDA(At, 1, 0); G_STAGE(G_SA(0, 1), a12, vA1);
;             G_WAIT_L(0); G_BAR; G_MMA(0, 0, At, B0); G_MMA(0, 1, At, B1); G_WAIT_V(8); G_BAR; G_SCHED;
;             G_LDA(At, 1, 1); G_STAGE(G_SB(1, 0), b02 + kstep, voffB); G_STAGE(G_SB(1, 1), b12 + kstep, voffB); G_STAGE(G_SA(1, 0), a02 + kstep, vA0);
;             G_WAIT_L(0); G_BAR; G_MMA(1, 0, At, B0); G_MMA(1, 1, At, B1); G_WAIT_V(8); G_BAR; G_SCHED;
;         }
	s_add_i32 s78, 0, 0x18000
	s_add_i32 s79, 0, 0x1c000
	s_mov_b32 m0, s41
	v_lshl_add_u64 v[222:223], s[76:77], 0, v[192:193]
	global_load_lds_dwordx4 v[222:223], off
	v_lshl_add_u64 v[222:223], s[76:77], 0, v[198:199]
	s_mov_b32 m0, s18
	s_nop 0
	global_load_lds_dwordx4 v[222:223], off
	v_add_u32_e32 v76, s78, v203
	v_add_u32_e32 v100, s79, v203
	ds_read_b128 v[64:67], v76
	ds_read_b128 v[68:71], v76 offset:1024
	ds_read_b128 v[72:75], v76 offset:2048
	ds_read_b128 v[76:79], v76 offset:3072
	ds_read_b128 v[88:91], v100
	ds_read_b128 v[92:95], v100 offset:1024
	ds_read_b128 v[96:99], v100 offset:2048
	ds_read_b128 v[100:103], v100 offset:3072
	ds_read_b128 v[160:163], v208 offset:32768
	ds_read_b128 v[164:167], v208 offset:33792
	ds_read_b128 v[168:171], v208 offset:34816
	ds_read_b128 v[172:175], v208 offset:35840
	ds_read_b128 v[176:179], v208 offset:36864
	ds_read_b128 v[180:183], v208 offset:37888
	ds_read_b128 v[184:187], v208 offset:38912
	ds_read_b128 v[188:191], v208 offset:39936
	s_waitcnt lgkmcnt(0)
	s_barrier
	s_setprio 1
	s_waitcnt lgkmcnt(0)
	v_mfma_i32_16x16x64_i8 v[156:159], v[64:67], v[160:163], v[156:159]
	v_mfma_i32_16x16x64_i8 v[148:151], v[72:75], v[160:163], v[148:151]
	v_mfma_i32_16x16x64_i8 v[140:143], v[64:67], v[168:171], v[140:143]
	v_mfma_i32_16x16x64_i8 v[132:135], v[72:75], v[168:171], v[132:135]
	v_mfma_i32_16x16x64_i8 v[124:127], v[64:67], v[176:179], v[124:127]
	v_mfma_i32_16x16x64_i8 v[116:119], v[72:75], v[176:179], v[116:119]
	v_mfma_i32_16x16x64_i8 v[108:111], v[64:67], v[184:187], v[108:111]
	v_mfma_i32_16x16x64_i8 v[84:87], v[72:75], v[184:187], v[84:87]
	v_mfma_i32_16x16x64_i8 v[156:159], v[68:71], v[164:167], v[156:159]
	v_mfma_i32_16x16x64_i8 v[148:151], v[76:79], v[164:167], v[148:151]
	v_mfma_i32_16x16x64_i8 v[140:143], v[68:71], v[172:175], v[140:143]
	v_mfma_i32_16x16x64_i8 v[132:135], v[76:79], v[172:175], v[132:135]
	v_mfma_i32_16x16x64_i8 v[124:127], v[68:71], v[180:183], v[124:127]
	v_mfma_i32_16x16x64_i8 v[116:119], v[76:79], v[180:183], v[116:119]
	v_mfma_i32_16x16x64_i8 v[108:111], v[68:71], v[188:191], v[108:111]
	v_mfma_i32_16x16x64_i8 v[84:87], v[76:79], v[188:191], v[84:87]
	v_mfma_i32_16x16x64_i8 v[152:155], v[88:91], v[160:163], v[152:155]
	v_mfma_i32_16x16x64_i8 v[144:147], v[96:99], v[160:163], v[144:147]
	v_mfma_i32_16x16x64_i8 v[136:139], v[88:91], v[168:171], v[136:139]
	v_mfma_i32_16x16x64_i8 v[128:131], v[96:99], v[168:171], v[128:131]
	v_mfma_i32_16x16x64_i8 v[120:123], v[88:91], v[176:179], v[120:123]
	v_mfma_i32_16x16x64_i8 v[112:115], v[96:99], v[176:179], v[112:115]
	v_mfma_i32_16x16x64_i8 v[104:107], v[88:91], v[184:187], v[104:107]
	v_mfma_i32_16x16x64_i8 v[80:83], v[96:99], v[184:187], v[80:83]
	v_mfma_i32_16x16x64_i8 v[152:155], v[92:95], v[164:167], v[152:155]
	v_mfma_i32_16x16x64_i8 v[144:147], v[100:103], v[164:167], v[144:147]
	v_mfma_i32_16x16x64_i8 v[136:139], v[92:95], v[172:175], v[136:139]
	v_mfma_i32_16x16x64_i8 v[128:131], v[100:103], v[172:175], v[128:131]
	v_mfma_i32_16x16x64_i8 v[120:123], v[92:95], v[180:183], v[120:123]
	v_mfma_i32_16x16x64_i8 v[112:115], v[100:103], v[180:183], v[112:115]
	v_mfma_i32_16x16x64_i8 v[104:107], v[92:95], v[188:191], v[104:107]
	v_mfma_i32_16x16x64_i8 v[80:83], v[100:103], v[188:191], v[80:83]
	s_setprio 0
	s_waitcnt vmcnt(8)
	s_barrier
	s_add_i32 s76, s78, s93
	v_lshl_add_u64 v[214:215], v[214:215], 0, s[44:45]
	s_mov_b32 m0, s76
	s_nop 0
	global_load_lds_dwordx4 v[214:215], off
	v_lshl_add_u64 v[214:215], v[216:217], 0, s[44:45]
	s_add_i32 m0, s76, 0x2000
	s_add_i32 s76, s79, s93
	global_load_lds_dwordx4 v[214:215], off
	v_lshl_add_u64 v[210:211], v[210:211], 0, s[44:45]
	s_mov_b32 m0, s76
	s_nop 0
	global_load_lds_dwordx4 v[210:211], off
	v_lshl_add_u64 v[210:211], v[212:213], 0, s[44:45]
	s_add_i32 m0, s76, 0x2000
	s_nop 0
	global_load_lds_dwordx4 v[210:211], off
	v_lshl_add_u64 v[210:211], v[218:219], 0, s[44:45]
	s_mov_b32 m0, s19
	s_nop 0
	global_load_lds_dwordx4 v[210:211], off
	v_lshl_add_u64 v[210:211], v[220:221], 0, s[44:45]
	s_mov_b32 m0, s89
	s_nop 0
	global_load_lds_dwordx4 v[210:211], off
	ds_read_b128 v[160:163], v208 offset:49152
	ds_read_b128 v[164:167], v208 offset:50176
	ds_read_b128 v[168:171], v208 offset:51200
	ds_read_b128 v[172:175], v208 offset:52224
	ds_read_b128 v[176:179], v208 offset:53248
	ds_read_b128 v[180:183], v208 offset:54272
	ds_read_b128 v[184:187], v208 offset:55296
	ds_read_b128 v[188:191], v208 offset:56320
	s_waitcnt lgkmcnt(0)
	s_barrier
	s_setprio 1
	s_waitcnt lgkmcnt(0)
	v_mfma_i32_16x16x64_i8 v[60:63], v[64:67], v[160:163], v[60:63]
	v_mfma_i32_16x16x64_i8 v[52:55], v[72:75], v[160:163], v[52:55]
	v_mfma_i32_16x16x64_i8 v[44:47], v[64:67], v[168:171], v[44:47]
	v_mfma_i32_16x16x64_i8 v[36:39], v[72:75], v[168:171], v[36:39]
	v_mfma_i32_16x16x64_i8 v[28:31], v[64:67], v[176:179], v[28:31]
	v_mfma_i32_16x16x64_i8 v[20:23], v[72:75], v[176:179], v[20:23]
	v_mfma_i32_16x16x64_i8 v[12:15], v[64:67], v[184:187], v[12:15]
	v_mfma_i32_16x16x64_i8 v[4:7], v[72:75], v[184:187], v[4:7]
	v_mfma_i32_16x16x64_i8 v[60:63], v[68:71], v[164:167], v[60:63]
	v_mfma_i32_16x16x64_i8 v[52:55], v[76:79], v[164:167], v[52:55]
	v_mfma_i32_16x16x64_i8 v[44:47], v[68:71], v[172:175], v[44:47]
	v_mfma_i32_16x16x64_i8 v[36:39], v[76:79], v[172:175], v[36:39]
	v_mfma_i32_16x16x64_i8 v[28:31], v[68:71], v[180:183], v[28:31]
	v_mfma_i32_16x16x64_i8 v[20:23], v[76:79], v[180:183], v[20:23]
	v_mfma_i32_16x16x64_i8 v[12:15], v[68:71], v[188:191], v[12:15]
	v_mfma_i32_16x16x64_i8 v[4:7], v[76:79], v[188:191], v[4:7]
	v_mfma_i32_16x16x64_i8 v[56:59], v[88:91], v[160:163], v[56:59]
	v_mfma_i32_16x16x64_i8 v[48:51], v[96:99], v[160:163], v[48:51]
	v_mfma_i32_16x16x64_i8 v[40:43], v[88:91], v[168:171], v[40:43]
	v_mfma_i32_16x16x64_i8 v[32:35], v[96:99], v[168:171], v[32:35]
	v_mfma_i32_16x16x64_i8 v[24:27], v[88:91], v[176:179], v[24:27]
	v_mfma_i32_16x16x64_i8 v[16:19], v[96:99], v[176:179], v[16:19]
	v_mfma_i32_16x16x64_i8 v[8:11], v[88:91], v[184:187], v[8:11]
	v_mfma_i32_16x16x64_i8 v[0:3], v[96:99], v[184:187], v[0:3]
	v_mfma_i32_16x16x64_i8 v[56:59], v[92:95], v[164:167], v[56:59]
	v_mfma_i32_16x16x64_i8 v[48:51], v[100:103], v[164:167], v[48:51]
	v_mfma_i32_16x16x64_i8 v[40:43], v[92:95], v[172:175], v[40:43]
	v_mfma_i32_16x16x64_i8 v[32:35], v[100:103], v[172:175], v[32:35]
	v_mfma_i32_16x16x64_i8 v[24:27], v[92:95], v[180:183], v[24:27]
	v_mfma_i32_16x16x64_i8 v[16:19], v[100:103], v[180:183], v[16:19]
	v_mfma_i32_16x16x64_i8 v[8:11], v[92:95], v[188:191], v[8:11]
	v_mfma_i32_16x16x64_i8 v[0:3], v[100:103], v[188:191], v[0:3]
	s_setprio 0
	s_waitcnt vmcnt(8)
	s_barrier
	s_add_u32 s74, s74, 0x100
	s_addc_u32 s75, s75, 0
	s_cmp_ge_i32 s31, s33
	s_cbranch_scc1 .LBB0_1639

; #define G_STAGE(bufoff, gbase, voff) do { _Pragma("unroll") for (int _i = 0; _i < 2; ++_i) \
;         __builtin_amdgcn_global_load_lds((const unsigned*)((const char*)(gbase) + (voff)[_i]), (LAS unsigned*)(lds + (bufoff) + ldsw + _i * 8192), 16, 0, 0); } while (0)
; #define G_LDA(dst, b, h) do { _Pragma("unroll") for (int m = 0; m < 4; ++m) G_LD8(dst[m], lds + G_SA(b, h) + aoff + m * 2048); } while (0)
; #define G_LDB(dst, b, h) do { _Pragma("unroll") for (int n = 0; n < 2; ++n) G_LD8(dst[n], lds + G_SB(b, h) + boff + n * 2048); } while (0)
; #define G_WAIT_V(n) asm volatile("s_waitcnt vmcnt(" #n ")" ::: "memory")
; #define G_WAIT_L(n) asm volatile("s_waitcnt lgkmcnt(" #n ")" ::: "memory")
; #define G_BAR __builtin_amdgcn_s_barrier()
; #define G_SCHED __builtin_amdgcn_sched_barrier(0)
;     __device__ __forceinline__ unsigned row_off(const Unit& u, int r, LAS unsigned char* lds) const { return (unsigned)((const LAS int*)(lds + LDS_STAGE + u.q * 4096))[r] * (unsigned)rowbytes; }
;     ...
;             const char* a11 = cur.a1 + (size_t)(t + 1) * kstep;
;             const char* a02 = last ? nxt.a0 : cur.a0 + (size_t)(t + 2) * kstep; const char* a12 = last ? nxt.a1 : cur.a1 + (size_t)(t + 2) * kstep;
;             const char* b02 = last ? nxt.b0 : cur.b0 + (size_t)(t + 2) * kstep; const char* b12 = last ? nxt.b1 : cur.b1 + (size_t)(t + 2) * kstep;
;             G_LDB(B0, 0, 0); G_LDB(B1, 0, 1); G_SCHED; G_LDA(At, 0, 0); G_STAGE(G_SA(1, 1), a11, vA1);
;             if constexpr (GATHER) { if (last) { int tz = tid; asm volatile("" : "+v"(tz));
; #pragma unroll
;                 for (int i = 0; i < 2; ++i) { int R, C; stage_rc(tz * 16 + i * 8192, R, C); gc0[i] = S.row_off(nxt, R, lds) + (unsigned)C * 2u; gc1[i] = S.row_off(nxt, 128 + R, lds) + (unsigned)C * 2u; } } }
;             G_WAIT_L(0); G_BAR; G_MMA(0, 0, At, B0); G_MMA(0, 1, At, B1); G_WAIT_V(8); G_BAR; G_SCHED;
;             G_LDA(At, 0, 1); G_STAGE(G_SB(0, 0), b02, voffB); G_STAGE(G_SB(0, 1), b12, voffB); G_STAGE(G_SA(0, 0), a02, vA0);
.LBB0_1733:
	s_add_i32 s81, s80, 2
	s_add_u32 s52, s78, s48
	s_addc_u32 s53, s79, s49
	s_add_u32 s58, s44, s48
	s_addc_u32 s59, s45, s49
	s_add_u32 s86, s58, 0x100
	v_add_u32_e32 v154, s66, v137
	v_add_u32_e32 v170, s67, v137
	s_addc_u32 s87, s59, 0
	ds_read_b128 v[142:145], v154
	ds_read_b128 v[146:149], v154 offset:1024
	ds_read_b128 v[150:153], v154 offset:2048
	ds_read_b128 v[154:157], v154 offset:3072
	ds_read_b128 v[158:161], v170
	ds_read_b128 v[162:165], v170 offset:1024
	ds_read_b128 v[166:169], v170 offset:2048
	ds_read_b128 v[170:173], v170 offset:3072
	s_add_u32 s56, s29, s48
	s_addc_u32 s57, s75, s49
	s_add_u32 s82, s76, s48
	s_addc_u32 s83, s77, s49
	s_add_i32 s90, s66, s22
	s_add_i32 m0, s23, 0xc000
	s_add_i32 s89, s23, 0xe000
	s_add_i32 s84, s90, 0x2000
	s_cmp_eq_u32 s65, s80
	s_cselect_b32 s55, s37, s53
	s_cselect_b32 s54, s36, s52
	s_cselect_b32 s57, s31, s57
	s_cselect_b32 s56, s30, s56
	s_cselect_b32 s53, s39, s87
	s_cselect_b32 s52, s38, s86
	v_lshl_add_u64 v[206:207], s[58:59], 0, v[128:129]
	v_lshl_add_u64 v[206:207], v[206:207], 0, s[10:11]
	ds_read_b128 v[174:177], v138
	ds_read_b128 v[178:181], v138 offset:1024
	ds_read_b128 v[182:185], v138 offset:2048
	ds_read_b128 v[186:189], v138 offset:3072
	ds_read_b128 v[190:193], v138 offset:4096
	ds_read_b128 v[194:197], v138 offset:5120
	ds_read_b128 v[198:201], v138 offset:6144
	ds_read_b128 v[202:205], v138 offset:7168
	global_load_lds_dwordx4 v[206:207], off
	v_lshl_add_u64 v[206:207], s[58:59], 0, v[130:131]
	v_lshl_add_u64 v[206:207], v[206:207], 0, s[10:11]
	s_mov_b32 m0, s89
	v_mov_b32_e32 v131, v129
	global_load_lds_dwordx4 v[206:207], off
	s_waitcnt lgkmcnt(0)
	s_barrier
	s_setprio 1
	s_waitcnt lgkmcnt(0)
	v_mfma_scale_f32_16x16x128_f8f6f4 v[124:127], v[142:149], v[174:181], v[124:127], v139, v139 op_sel_hi:[0,0,0]
	v_mfma_scale_f32_16x16x128_f8f6f4 v[120:123], v[150:157], v[174:181], v[120:123], v139, v139 op_sel_hi:[0,0,0]
	v_mfma_scale_f32_16x16x128_f8f6f4 v[116:119], v[142:149], v[182:189], v[116:119], v139, v139 op_sel_hi:[0,0,0]
	v_mfma_scale_f32_16x16x128_f8f6f4 v[112:115], v[150:157], v[182:189], v[112:115], v139, v139 op_sel_hi:[0,0,0]
	v_mfma_scale_f32_16x16x128_f8f6f4 v[108:111], v[142:149], v[190:197], v[108:111], v139, v139 op_sel_hi:[0,0,0]
	v_mfma_scale_f32_16x16x128_f8f6f4 v[104:107], v[150:157], v[190:197], v[104:107], v139, v139 op_sel_hi:[0,0,0]
	v_mfma_scale_f32_16x16x128_f8f6f4 v[100:103], v[142:149], v[198:205], v[100:103], v139, v139 op_sel_hi:[0,0,0]
	v_mfma_scale_f32_16x16x128_f8f6f4 v[96:99], v[150:157], v[198:205], v[96:99], v139, v139 op_sel_hi:[0,0,0]
	v_mfma_scale_f32_16x16x128_f8f6f4 v[206:209], v[158:165], v[174:181], v[60:63], v139, v139 op_sel_hi:[0,0,0]
	v_mfma_scale_f32_16x16x128_f8f6f4 v[174:177], v[166:173], v[174:181], v[56:59], v139, v139 op_sel_hi:[0,0,0]
	v_mfma_scale_f32_16x16x128_f8f6f4 v[178:181], v[158:165], v[182:189], v[52:55], v139, v139 op_sel_hi:[0,0,0]
	v_mfma_scale_f32_16x16x128_f8f6f4 v[182:185], v[166:173], v[182:189], v[48:51], v139, v139 op_sel_hi:[0,0,0]
	v_mfma_scale_f32_16x16x128_f8f6f4 v[186:189], v[158:165], v[190:197], v[44:47], v139, v139 op_sel_hi:[0,0,0]
	v_mfma_scale_f32_16x16x128_f8f6f4 v[190:193], v[166:173], v[190:197], v[40:43], v139, v139 op_sel_hi:[0,0,0]
	v_mfma_scale_f32_16x16x128_f8f6f4 v[194:197], v[158:165], v[198:205], v[36:39], v139, v139 op_sel_hi:[0,0,0]
	v_mfma_scale_f32_16x16x128_f8f6f4 v[198:201], v[166:173], v[198:205], v[32:35], v139, v139 op_sel_hi:[0,0,0]
	s_setprio 0
	s_waitcnt vmcnt(8)
	s_barrier
	s_mov_b32 m0, s90
	s_nop 3
	global_load_lds_dwordx4 v132, s[56:57]
	s_mov_b32 m0, s84
	s_cselect_b32 s59, s35, s83
	s_cselect_b32 s58, s34, s82
	s_add_i32 s80, s67, s22
	s_add_u32 s98, s56, 0x20000
	s_addc_u32 s99, s57, 0
	global_load_lds_dwordx4 v132, s[98:99]
	s_mov_b32 m0, s80
	v_mov_b32_e32 v133, v129
	global_load_lds_dwordx4 v132, s[58:59]
	s_add_i32 m0, s80, 0x2000
	s_add_u32 s100, s58, 0x20000
	s_addc_u32 s101, s59, 0
	global_load_lds_dwordx4 v132, s[100:101]
	s_mov_b32 m0, s23
	v_lshl_add_u64 v[246:247], s[56:57], 0, v[132:133]
	global_load_lds_dwordx4 v128, s[54:55]
	s_mov_b32 m0, s24
	v_lshl_add_u64 v[248:249], s[98:99], 0, v[132:133]
	global_load_lds_dwordx4 v130, s[54:55]
	ds_read_b128 v[32:35], v138 offset:16384
	ds_read_b128 v[36:39], v138 offset:17408
	ds_read_b128 v[40:43], v138 offset:18432
	ds_read_b128 v[44:47], v138 offset:19456
	ds_read_b128 v[48:51], v138 offset:20480
	ds_read_b128 v[52:55], v138 offset:21504
	ds_read_b128 v[56:59], v138 offset:22528
	ds_read_b128 v[60:63], v138 offset:23552
	s_waitcnt lgkmcnt(0)
	v_lshl_add_u64 v[250:251], s[100:101], 0, v[132:133]
	v_lshl_add_u64 v[252:253], s[54:55], 0, v[128:129]
	v_lshl_add_u64 v[134:135], s[54:55], 0, v[130:131]
	s_barrier
; #define G_STAGE(bufoff, gbase, voff) do { _Pragma("unroll") for (int _i = 0; _i < 2; ++_i) \
;         __builtin_amdgcn_global_load_lds((const unsigned*)((const char*)(gbase) + (voff)[_i]), (LAS unsigned*)(lds + (bufoff) + ldsw + _i * 8192), 16, 0, 0); } while (0)
; #define G_LDA(dst, b, h) do { _Pragma("unroll") for (int m = 0; m < 4; ++m) G_LD8(dst[m], lds + G_SA(b, h) + aoff + m * 2048); } while (0)
; #define G_LDB(dst, b, h) do { _Pragma("unroll") for (int n = 0; n < 2; ++n) G_LD8(dst[n], lds + G_SB(b, h) + boff + n * 2048); } while (0)
; #define G_WAIT_V(n) asm volatile("s_waitcnt vmcnt(" #n ")" ::: "memory")
; #define G_WAIT_L(n) asm volatile("s_waitcnt lgkmcnt(" #n ")" ::: "memory")
; #define G_BAR __builtin_amdgcn_s_barrier()
; #define G_SCHED __builtin_amdgcn_sched_barrier(0)
;     ...
;             G_WAIT_L(0); G_BAR; G_MMA(1, 0, At, B0); G_MMA(1, 1, At, B1); G_WAIT_V(8); G_BAR; G_SCHED;
;             G_LDB(B0, 1, 0); G_LDB(B1, 1, 1); G_SCHED; G_LDA(At, 1, 0); G_STAGE(G_SA(0, 1), a12, vA1);
;             G_WAIT_L(0); G_BAR; G_MMA(0, 0, At, B0); G_MMA(0, 1, At, B1); G_WAIT_V(8); G_BAR; G_SCHED;
	s_setprio 1
	s_waitcnt lgkmcnt(0)
	v_mfma_scale_f32_16x16x128_f8f6f4 v[92:95], v[142:149], v[32:39], v[92:95], v139, v139 op_sel_hi:[0,0,0]
	v_mfma_scale_f32_16x16x128_f8f6f4 v[88:91], v[150:157], v[32:39], v[88:91], v139, v139 op_sel_hi:[0,0,0]
	v_mfma_scale_f32_16x16x128_f8f6f4 v[84:87], v[142:149], v[40:47], v[84:87], v139, v139 op_sel_hi:[0,0,0]
	v_mfma_scale_f32_16x16x128_f8f6f4 v[80:83], v[150:157], v[40:47], v[80:83], v139, v139 op_sel_hi:[0,0,0]
	v_mfma_scale_f32_16x16x128_f8f6f4 v[76:79], v[142:149], v[48:55], v[76:79], v139, v139 op_sel_hi:[0,0,0]
	v_mfma_scale_f32_16x16x128_f8f6f4 v[72:75], v[150:157], v[48:55], v[72:75], v139, v139 op_sel_hi:[0,0,0]
	v_mfma_scale_f32_16x16x128_f8f6f4 v[202:205], v[142:149], v[56:63], v[68:71], v139, v139 op_sel_hi:[0,0,0]
	v_mfma_scale_f32_16x16x128_f8f6f4 v[210:213], v[150:157], v[56:63], v[64:67], v139, v139 op_sel_hi:[0,0,0]
	v_mfma_scale_f32_16x16x128_f8f6f4 v[214:217], v[158:165], v[32:39], v[28:31], v139, v139 op_sel_hi:[0,0,0]
	v_mfma_scale_f32_16x16x128_f8f6f4 v[218:221], v[166:173], v[32:39], v[24:27], v139, v139 op_sel_hi:[0,0,0]
	v_mfma_scale_f32_16x16x128_f8f6f4 v[222:225], v[158:165], v[40:47], v[20:23], v139, v139 op_sel_hi:[0,0,0]
	v_mfma_scale_f32_16x16x128_f8f6f4 v[226:229], v[166:173], v[40:47], v[16:19], v139, v139 op_sel_hi:[0,0,0]
	v_mfma_scale_f32_16x16x128_f8f6f4 v[230:233], v[158:165], v[48:55], v[12:15], v139, v139 op_sel_hi:[0,0,0]
	v_mfma_scale_f32_16x16x128_f8f6f4 v[234:237], v[166:173], v[48:55], v[8:11], v139, v139 op_sel_hi:[0,0,0]
	v_mfma_scale_f32_16x16x128_f8f6f4 v[238:241], v[158:165], v[56:63], v[4:7], v139, v139 op_sel_hi:[0,0,0]
	v_mfma_scale_f32_16x16x128_f8f6f4 v[242:245], v[166:173], v[56:63], v[0:3], v139, v139 op_sel_hi:[0,0,0]
	s_setprio 0
	s_waitcnt vmcnt(8)
	s_barrier
	s_add_i32 s54, 0, 0x18000
	s_add_i32 s55, 0, 0x1c000
	s_nop 0
	s_mov_b32 m0, s25
	s_nop 0
	global_load_lds_dwordx4 v128, s[52:53]
	s_mov_b32 m0, s26
	s_nop 0
	global_load_lds_dwordx4 v130, s[52:53]
	v_add_u32_e32 v12, s54, v137
	v_add_u32_e32 v16, s55, v137
	ds_read_b128 v[0:3], v12
	ds_read_b128 v[4:7], v12 offset:1024
	ds_read_b128 v[8:11], v12 offset:2048
	ds_read_b128 v[12:15], v12 offset:3072
	ds_read_b128 v[142:145], v16
	ds_read_b128 v[146:149], v16 offset:1024
	ds_read_b128 v[150:153], v16 offset:2048
	ds_read_b128 v[154:157], v16 offset:3072
	ds_read_b128 v[16:19], v138 offset:32768
	ds_read_b128 v[20:23], v138 offset:33792
	ds_read_b128 v[24:27], v138 offset:34816
	ds_read_b128 v[28:31], v138 offset:35840
	ds_read_b128 v[32:35], v138 offset:36864
	ds_read_b128 v[36:39], v138 offset:37888
	ds_read_b128 v[64:67], v138 offset:38912
	ds_read_b128 v[68:71], v138 offset:39936
	s_waitcnt lgkmcnt(0)
	s_barrier
	s_setprio 1
	s_waitcnt lgkmcnt(0)
	v_mfma_scale_f32_16x16x128_f8f6f4 v[124:127], v[0:7], v[16:23], v[124:127], v139, v139 op_sel_hi:[0,0,0]
	v_mfma_scale_f32_16x16x128_f8f6f4 v[120:123], v[8:15], v[16:23], v[120:123], v139, v139 op_sel_hi:[0,0,0]
	v_mfma_scale_f32_16x16x128_f8f6f4 v[116:119], v[0:7], v[24:31], v[116:119], v139, v139 op_sel_hi:[0,0,0]
	v_mfma_scale_f32_16x16x128_f8f6f4 v[112:115], v[8:15], v[24:31], v[112:115], v139, v139 op_sel_hi:[0,0,0]
	v_mfma_scale_f32_16x16x128_f8f6f4 v[108:111], v[0:7], v[32:39], v[108:111], v139, v139 op_sel_hi:[0,0,0]
	v_mfma_scale_f32_16x16x128_f8f6f4 v[104:107], v[8:15], v[32:39], v[104:107], v139, v139 op_sel_hi:[0,0,0]
	v_mfma_scale_f32_16x16x128_f8f6f4 v[100:103], v[0:7], v[64:71], v[100:103], v139, v139 op_sel_hi:[0,0,0]
	v_mfma_scale_f32_16x16x128_f8f6f4 v[96:99], v[8:15], v[64:71], v[96:99], v139, v139 op_sel_hi:[0,0,0]
	v_mfma_scale_f32_16x16x128_f8f6f4 v[60:63], v[142:149], v[16:23], v[206:209], v139, v139 op_sel_hi:[0,0,0]
	v_mfma_scale_f32_16x16x128_f8f6f4 v[56:59], v[150:157], v[16:23], v[174:177], v139, v139 op_sel_hi:[0,0,0]
	v_mfma_scale_f32_16x16x128_f8f6f4 v[52:55], v[142:149], v[24:31], v[178:181], v139, v139 op_sel_hi:[0,0,0]
	v_mfma_scale_f32_16x16x128_f8f6f4 v[48:51], v[150:157], v[24:31], v[182:185], v139, v139 op_sel_hi:[0,0,0]
	v_mfma_scale_f32_16x16x128_f8f6f4 v[44:47], v[142:149], v[32:39], v[186:189], v139, v139 op_sel_hi:[0,0,0]
	v_mfma_scale_f32_16x16x128_f8f6f4 v[40:43], v[150:157], v[32:39], v[190:193], v139, v139 op_sel_hi:[0,0,0]
	v_mfma_scale_f32_16x16x128_f8f6f4 v[36:39], v[142:149], v[64:71], v[194:197], v139, v139 op_sel_hi:[0,0,0]
	v_mfma_scale_f32_16x16x128_f8f6f4 v[32:35], v[150:157], v[64:71], v[198:201], v139, v139 op_sel_hi:[0,0,0]
	s_setprio 0
	s_waitcnt vmcnt(8)
	s_barrier
; #define G_STAGE(bufoff, gbase, voff) do { _Pragma("unroll") for (int _i = 0; _i < 2; ++_i) \
;         __builtin_amdgcn_global_load_lds((const unsigned*)((const char*)(gbase) + (voff)[_i]), (LAS unsigned*)(lds + (bufoff) + ldsw + _i * 8192), 16, 0, 0); } while (0)
; #define G_LDA(dst, b, h) do { _Pragma("unroll") for (int m = 0; m < 4; ++m) G_LD8(dst[m], lds + G_SA(b, h) + aoff + m * 2048); } while (0)
; #define G_WAIT_V(n) asm volatile("s_waitcnt vmcnt(" #n ")" ::: "memory")
; #define G_WAIT_L(n) asm volatile("s_waitcnt lgkmcnt(" #n ")" ::: "memory")
; #define G_BAR __builtin_amdgcn_s_barrier()
; #define G_SCHED __builtin_amdgcn_sched_barrier(0)
;     ...
;             G_LDA(At, 1, 1); G_STAGE(G_SB(1, 0), b02 + kstep, voffB); G_STAGE(G_SB(1, 1), b12 + kstep, voffB); G_STAGE(G_SA(1, 0), a02 + kstep, vA0);
;             G_WAIT_L(0); G_BAR; G_MMA(1, 0, At, B0); G_MMA(1, 1, At, B1); G_WAIT_V(8); G_BAR; G_SCHED;
;         }
	s_add_i32 s52, s54, s22
	v_lshl_add_u64 v[24:25], v[246:247], 0, s[10:11]
	s_mov_b32 m0, s52
	s_nop 0
	global_load_lds_dwordx4 v[24:25], off
	v_lshl_add_u64 v[24:25], v[248:249], 0, s[10:11]
	s_add_i32 m0, s52, 0x2000
	s_add_i32 s52, s55, s22
	s_sub_u32 s98, s10, 0x20000
	s_subb_u32 s99, s11, 0
	global_load_lds_dwordx4 v[24:25], off
	v_lshl_add_u64 v[24:25], v[250:251], 0, s[98:99]
	s_mov_b32 m0, s52
	s_nop 0
	global_load_lds_dwordx4 v[24:25], off
	v_lshl_add_u64 v[24:25], v[250:251], 0, s[10:11]
	s_add_i32 m0, s52, 0x2000
	s_nop 0
	global_load_lds_dwordx4 v[24:25], off
	v_lshl_add_u64 v[24:25], v[252:253], 0, s[10:11]
	s_mov_b32 m0, s62
	s_nop 0
	global_load_lds_dwordx4 v[24:25], off
	v_lshl_add_u64 v[24:25], v[134:135], 0, s[10:11]
	s_mov_b32 m0, s63
	s_nop 0
	global_load_lds_dwordx4 v[24:25], off
	ds_read_b128 v[16:19], v138 offset:49152
	ds_read_b128 v[20:23], v138 offset:50176
	ds_read_b128 v[158:161], v138 offset:51200
	ds_read_b128 v[162:165], v138 offset:52224
	ds_read_b128 v[166:169], v138 offset:53248
	ds_read_b128 v[170:173], v138 offset:54272
	ds_read_b128 v[174:177], v138 offset:55296
	ds_read_b128 v[178:181], v138 offset:56320
	s_waitcnt lgkmcnt(0)
	s_barrier
	s_setprio 1
	s_waitcnt lgkmcnt(0)
	v_mfma_scale_f32_16x16x128_f8f6f4 v[92:95], v[0:7], v[16:23], v[92:95], v139, v139 op_sel_hi:[0,0,0]
	v_mfma_scale_f32_16x16x128_f8f6f4 v[88:91], v[8:15], v[16:23], v[88:91], v139, v139 op_sel_hi:[0,0,0]
	v_mfma_scale_f32_16x16x128_f8f6f4 v[84:87], v[0:7], v[158:165], v[84:87], v139, v139 op_sel_hi:[0,0,0]
	v_mfma_scale_f32_16x16x128_f8f6f4 v[80:83], v[8:15], v[158:165], v[80:83], v139, v139 op_sel_hi:[0,0,0]
	v_mfma_scale_f32_16x16x128_f8f6f4 v[76:79], v[0:7], v[166:173], v[76:79], v139, v139 op_sel_hi:[0,0,0]
	v_mfma_scale_f32_16x16x128_f8f6f4 v[72:75], v[8:15], v[166:173], v[72:75], v139, v139 op_sel_hi:[0,0,0]
	v_mfma_scale_f32_16x16x128_f8f6f4 v[68:71], v[0:7], v[174:181], v[202:205], v139, v139 op_sel_hi:[0,0,0]
	v_mfma_scale_f32_16x16x128_f8f6f4 v[64:67], v[8:15], v[174:181], v[210:213], v139, v139 op_sel_hi:[0,0,0]
	v_mfma_scale_f32_16x16x128_f8f6f4 v[28:31], v[142:149], v[16:23], v[214:217], v139, v139 op_sel_hi:[0,0,0]
	v_mfma_scale_f32_16x16x128_f8f6f4 v[24:27], v[150:157], v[16:23], v[218:221], v139, v139 op_sel_hi:[0,0,0]
	v_mfma_scale_f32_16x16x128_f8f6f4 v[20:23], v[142:149], v[158:165], v[222:225], v139, v139 op_sel_hi:[0,0,0]
	v_mfma_scale_f32_16x16x128_f8f6f4 v[16:19], v[150:157], v[158:165], v[226:229], v139, v139 op_sel_hi:[0,0,0]
	v_mfma_scale_f32_16x16x128_f8f6f4 v[12:15], v[142:149], v[166:173], v[230:233], v139, v139 op_sel_hi:[0,0,0]
	v_mfma_scale_f32_16x16x128_f8f6f4 v[8:11], v[150:157], v[166:173], v[234:237], v139, v139 op_sel_hi:[0,0,0]
	v_mfma_scale_f32_16x16x128_f8f6f4 v[4:7], v[142:149], v[174:181], v[238:241], v139, v139 op_sel_hi:[0,0,0]
	v_mfma_scale_f32_16x16x128_f8f6f4 v[0:3], v[150:157], v[174:181], v[242:245], v139, v139 op_sel_hi:[0,0,0]
	s_setprio 0
	s_waitcnt vmcnt(8)
	s_barrier
	s_add_u32 s48, s48, 0x100
	s_addc_u32 s49, s49, 0
	s_cmp_ge_i32 s81, s0
	s_cbranch_scc1 .LBB0_1735
	s_mov_b32 s80, s81
	s_branch .LBB0_1724
